# v22 + in peeled K-loop bodies the 2nd half of the next B(1,1) piece is issued at the top of the next iteration's heavy phase (and once after the loop); second light phase 5 loads, vmcnt(7)
# baseline (speedup 1.0000x reference)
; #define PG8_STAGE(bufoff, rs_, soff_, voff) do { _Pragma("unroll") for (int _i = 0; _i < 2; ++_i) \
;         __builtin_amdgcn_raw_ptr_buffer_load_lds(rs_, (LAS void*)(lds + (bufoff) + ldsw + _i * 8192), 16, (int)(voff)[_i], (int)(soff_), 0, 0); } while (0)
; #define PG8_LDA(dst, b, h) do { _Pragma("unroll") for (int m = 0; m < 4; ++m) dst[m] = PG8_LD2(lds + PG8_SA(b, h) + aoff + m * 2048); } while (0)
; #define PG8_LDB(dst, b, h) do { _Pragma("unroll") for (int n = 0; n < 2; ++n) dst[n] = PG8_LD2(lds + PG8_SB(b, h) + boff + n * 2048); } while (0)
; #define PG8_WAIT_V(n) asm volatile("s_waitcnt vmcnt(" #n ")" ::: "memory")
; #define PG8_WAIT_L(n) asm volatile("s_waitcnt lgkmcnt(" #n ")" ::: "memory")
; #define PG8_BAR __builtin_amdgcn_s_barrier()
; #define PG8_SCHED __builtin_amdgcn_sched_barrier(0)
; template <class Epi, class Sched, bool ALIGN_EPI = false, bool SP2 = false, bool FP8 = false>
; __device__ __forceinline__ void gemm_phase(LAS unsigned char* lds, const Gemm g, const Sched& S, const Epi& E, int wbase) {
;     ...
;             PG8_LDB(B0, 0, 0); PG8_LDB(B1, 0, 1); PG8_SCHED; PG8_LDA(At, 0, 0); PG8_STAGE(PG8_SA(1, 1), rAc, a1 + hstep, voffA);
;             PG8_WAIT_V(8); PG8_WAIT_L(0); PG8_BAR; PG8_MMA(0, 0, At, B0); PG8_MMA(0, 1, At, B1); PG8_BAR; PG8_SCHED;
;             PG8_LDA(At, 0, 1); PG8_STAGE(PG8_SB(0, 0), rB2, b2, voffB); PG8_STAGE(PG8_SB(0, 1), rB2, b2 + hstep, voffB); PG8_STAGE(PG8_SA(0, 0), rA2, a2, voffA);
;             PG8_WAIT_V(8); PG8_WAIT_L(0); PG8_BAR; PG8_MMA(1, 0, At, B0); PG8_MMA(1, 1, At, B1); PG8_BAR; PG8_SCHED;
.LBB0_258:
	s_mov_b32 m0, s33
	s_nop 0
	buffer_load_dwordx4 v193, s[4:7], s31 offen lds
	ds_read_b128 v[128:131], v252
	ds_read_b128 v[132:135], v252 offset:1024
	ds_read_b128 v[136:139], v252 offset:2048
	ds_read_b128 v[140:143], v252 offset:3072
	ds_read_b128 v[144:147], v225
	ds_read_b128 v[148:151], v225 offset:1024
	ds_read_b128 v[152:155], v225 offset:2048
	ds_read_b128 v[156:159], v225 offset:3072
	s_add_i32 s6, s16, 0x80
	s_cmp_eq_u32 s18, s29
	s_cselect_b32 s46, s2, s6
	s_cselect_b32 s31, s3, s28
	s_or_b32 s30, s46, 0x80
	s_add_i32 s6, s41, s16
	s_mov_b32 m0, s19
	ds_read_b128 v[176:179], v172
	ds_read_b128 v[180:183], v172 offset:1024
	ds_read_b128 v[184:187], v172 offset:2048
	ds_read_b128 v[188:191], v172 offset:3072
	ds_read_b128 v[194:197], v172 offset:4096
	ds_read_b128 v[198:201], v172 offset:5120
	ds_read_b128 v[202:205], v172 offset:6144
	ds_read_b128 v[206:209], v172 offset:7168
	buffer_load_dwordx4 v192, s[36:39], s6 offen lds
	s_mov_b32 m0, s20
	s_nop 0
	buffer_load_dwordx4 v223, s[36:39], s6 offen lds
	s_waitcnt vmcnt(8)
	s_waitcnt lgkmcnt(0)
	s_barrier
	s_setprio 1
	v_mfma_f32_16x16x128_f8f6f4 v[124:127], v[128:135], v[176:183], v[124:127]
	v_mfma_f32_16x16x128_f8f6f4 v[120:123], v[136:143], v[176:183], v[120:123]
	v_mfma_f32_16x16x128_f8f6f4 v[108:111], v[128:135], v[184:191], v[108:111]
	v_mfma_f32_16x16x128_f8f6f4 v[104:107], v[136:143], v[184:191], v[104:107]
	v_mfma_f32_16x16x128_f8f6f4 v[160:163], v[128:135], v[194:201], v[92:95]
	v_mfma_f32_16x16x128_f8f6f4 v[210:213], v[136:143], v[194:201], v[88:91]
	v_mfma_f32_16x16x128_f8f6f4 v[214:217], v[128:135], v[202:209], v[76:79]
	v_mfma_f32_16x16x128_f8f6f4 v[218:221], v[136:143], v[202:209], v[72:75]
	v_mfma_f32_16x16x128_f8f6f4 v[116:119], v[144:151], v[176:183], v[116:119]
	v_mfma_f32_16x16x128_f8f6f4 v[112:115], v[152:159], v[176:183], v[112:115]
	v_mfma_f32_16x16x128_f8f6f4 v[100:103], v[144:151], v[184:191], v[100:103]
	v_mfma_f32_16x16x128_f8f6f4 v[96:99], v[152:159], v[184:191], v[96:99]
	v_mfma_f32_16x16x128_f8f6f4 v[176:179], v[144:151], v[194:201], v[84:87]
	v_mfma_f32_16x16x128_f8f6f4 v[180:183], v[152:159], v[194:201], v[80:83]
	v_mfma_f32_16x16x128_f8f6f4 v[184:187], v[144:151], v[202:209], v[68:71]
	v_mfma_f32_16x16x128_f8f6f4 v[188:191], v[152:159], v[202:209], v[64:67]
	s_setprio 0
	s_barrier
	s_mov_b32 m0, s43
	s_mov_b32 s6, s38
	s_mov_b32 s7, s39
	s_nop 1
	buffer_load_dwordx4 v222, s[4:7], s31 offen lds
	s_mov_b32 m0, s44
	ds_read_b128 v[64:67], v172 offset:16384
	s_add_i32 s47, s31, s41
	buffer_load_dwordx4 v193, s[4:7], s31 offen lds
	s_mov_b32 m0, s45
	ds_read_b128 v[68:71], v172 offset:17408
	buffer_load_dwordx4 v222, s[4:7], s47 offen lds
	s_mov_b32 m0, s42
	ds_read_b128 v[72:75], v172 offset:18432
	buffer_load_dwordx4 v192, s[36:39], s46 offen lds
	s_mov_b32 m0, s53
	ds_read_b128 v[76:79], v172 offset:19456
	buffer_load_dwordx4 v223, s[36:39], s46 offen lds
	ds_read_b128 v[80:83], v172 offset:20480
	ds_read_b128 v[84:87], v172 offset:21504
	ds_read_b128 v[88:91], v172 offset:22528
	ds_read_b128 v[92:95], v172 offset:23552
	s_waitcnt vmcnt(7)
	s_waitcnt lgkmcnt(0)
	s_barrier
	s_setprio 1
	v_mfma_f32_16x16x128_f8f6f4 v[60:63], v[128:135], v[64:71], v[60:63]
	v_mfma_f32_16x16x128_f8f6f4 v[56:59], v[136:143], v[64:71], v[56:59]
	v_mfma_f32_16x16x128_f8f6f4 v[194:197], v[128:135], v[72:79], v[44:47]
	v_mfma_f32_16x16x128_f8f6f4 v[198:201], v[136:143], v[72:79], v[40:43]
	v_mfma_f32_16x16x128_f8f6f4 v[202:205], v[128:135], v[80:87], v[28:31]
	v_mfma_f32_16x16x128_f8f6f4 v[206:209], v[136:143], v[80:87], v[24:27]
	v_mfma_f32_16x16x128_f8f6f4 v[236:239], v[128:135], v[88:95], v[12:15]
	v_mfma_f32_16x16x128_f8f6f4 v[240:243], v[136:143], v[88:95], v[8:11]
	v_mfma_f32_16x16x128_f8f6f4 v[52:55], v[144:151], v[64:71], v[52:55]
	v_mfma_f32_16x16x128_f8f6f4 v[48:51], v[152:159], v[64:71], v[48:51]
	v_mfma_f32_16x16x128_f8f6f4 v[244:247], v[144:151], v[72:79], v[36:39]
	v_mfma_f32_16x16x128_f8f6f4 v[248:251], v[152:159], v[72:79], v[32:35]
	v_mfma_f32_16x16x128_f8f6f4 v[226:229], v[144:151], v[80:87], v[20:23]
	v_mfma_f32_16x16x128_f8f6f4 v[232:235], v[152:159], v[80:87], v[16:19]
	v_mfma_f32_16x16x128_f8f6f4 v[164:167], v[144:151], v[88:95], v[4:7]
	v_mfma_f32_16x16x128_f8f6f4 v[168:171], v[152:159], v[88:95], v[0:3]
	s_setprio 0
	s_barrier
; #define PG8_STAGE(bufoff, rs_, soff_, voff) do { _Pragma("unroll") for (int _i = 0; _i < 2; ++_i) \
;         __builtin_amdgcn_raw_ptr_buffer_load_lds(rs_, (LAS void*)(lds + (bufoff) + ldsw + _i * 8192), 16, (int)(voff)[_i], (int)(soff_), 0, 0); } while (0)
; #define PG8_LDA(dst, b, h) do { _Pragma("unroll") for (int m = 0; m < 4; ++m) dst[m] = PG8_LD2(lds + PG8_SA(b, h) + aoff + m * 2048); } while (0)
; #define PG8_LDB(dst, b, h) do { _Pragma("unroll") for (int n = 0; n < 2; ++n) dst[n] = PG8_LD2(lds + PG8_SB(b, h) + boff + n * 2048); } while (0)
; #define PG8_WAIT_V(n) asm volatile("s_waitcnt vmcnt(" #n ")" ::: "memory")
; #define PG8_WAIT_L(n) asm volatile("s_waitcnt lgkmcnt(" #n ")" ::: "memory")
; #define PG8_BAR __builtin_amdgcn_s_barrier()
; #define PG8_SCHED __builtin_amdgcn_sched_barrier(0)
; template <class Epi, class Sched, bool ALIGN_EPI = false, bool SP2 = false, bool FP8 = false>
; __device__ __forceinline__ void gemm_phase(LAS unsigned char* lds, const Gemm g, const Sched& S, const Epi& E, int wbase) {
;     ...
;             PG8_LDA(At, 0, 1); PG8_STAGE(PG8_SB(0, 0), rB2, b2, voffB); PG8_STAGE(PG8_SB(0, 1), rB2, b2 + hstep, voffB); PG8_STAGE(PG8_SA(0, 0), rA2, a2, voffA);
;             PG8_WAIT_V(8); PG8_WAIT_L(0); PG8_BAR; PG8_MMA(1, 0, At, B0); PG8_MMA(1, 1, At, B1); PG8_BAR; PG8_SCHED;
;             PG8_LDB(B0, 1, 0); PG8_LDB(B1, 1, 1); PG8_SCHED; PG8_LDA(At, 1, 0); PG8_STAGE(PG8_SA(0, 1), rA2, a2 + hstep, voffA);
;             PG8_WAIT_V(8); PG8_WAIT_L(0); PG8_BAR; PG8_MMA(0, 0, At, B0); PG8_MMA(0, 1, At, B1); PG8_BAR; PG8_SCHED;
;             PG8_LDA(At, 1, 1); PG8_STAGE(PG8_SB(1, 0), rB2, b3, voffB); PG8_STAGE(PG8_SB(1, 1), rB2, b3 + hstep, voffB); PG8_STAGE(PG8_SA(1, 0), rA2, a3, voffA);
;             PG8_WAIT_V(8); PG8_WAIT_L(0); PG8_BAR; PG8_MMA(1, 0, At, B0); PG8_MMA(1, 1, At, B1); PG8_BAR; PG8_SCHED;
	s_mov_b32 m0, s52
	s_nop 0
	buffer_load_dwordx4 v193, s[4:7], s47 offen lds
	s_nop 4
	ds_read_b128 v[0:3], v173
	ds_read_b128 v[4:7], v173 offset:1024
	ds_read_b128 v[16:19], v173 offset:2048
	ds_read_b128 v[20:23], v173 offset:3072
	ds_read_b128 v[128:131], v174
	ds_read_b128 v[132:135], v174 offset:1024
	ds_read_b128 v[136:139], v174 offset:2048
	ds_read_b128 v[140:143], v174 offset:3072
	s_add_i32 s46, s46, s41
	s_mov_b32 m0, s56
	ds_read_b128 v[8:11], v172 offset:32768
	ds_read_b128 v[12:15], v172 offset:33792
	ds_read_b128 v[24:27], v172 offset:34816
	ds_read_b128 v[28:31], v172 offset:35840
	ds_read_b128 v[32:35], v172 offset:36864
	ds_read_b128 v[36:39], v172 offset:37888
	ds_read_b128 v[40:43], v172 offset:38912
	ds_read_b128 v[44:47], v172 offset:39936
	buffer_load_dwordx4 v192, s[36:39], s46 offen lds
	s_mov_b32 m0, s57
	s_nop 0
	buffer_load_dwordx4 v223, s[36:39], s46 offen lds
	s_waitcnt vmcnt(8)
	s_waitcnt lgkmcnt(0)
	s_barrier
	s_setprio 1
	v_mfma_f32_16x16x128_f8f6f4 v[124:127], v[0:7], v[8:15], v[124:127]
	v_mfma_f32_16x16x128_f8f6f4 v[120:123], v[16:23], v[8:15], v[120:123]
	v_mfma_f32_16x16x128_f8f6f4 v[108:111], v[0:7], v[24:31], v[108:111]
	v_mfma_f32_16x16x128_f8f6f4 v[104:107], v[16:23], v[24:31], v[104:107]
	v_mfma_f32_16x16x128_f8f6f4 v[92:95], v[0:7], v[32:39], v[160:163]
	v_mfma_f32_16x16x128_f8f6f4 v[88:91], v[16:23], v[32:39], v[210:213]
	v_mfma_f32_16x16x128_f8f6f4 v[76:79], v[0:7], v[40:47], v[214:217]
	v_mfma_f32_16x16x128_f8f6f4 v[72:75], v[16:23], v[40:47], v[218:221]
	v_mfma_f32_16x16x128_f8f6f4 v[116:119], v[128:135], v[8:15], v[116:119]
	v_mfma_f32_16x16x128_f8f6f4 v[112:115], v[136:143], v[8:15], v[112:115]
	v_mfma_f32_16x16x128_f8f6f4 v[100:103], v[128:135], v[24:31], v[100:103]
	v_mfma_f32_16x16x128_f8f6f4 v[96:99], v[136:143], v[24:31], v[96:99]
	v_mfma_f32_16x16x128_f8f6f4 v[84:87], v[128:135], v[32:39], v[176:179]
	v_mfma_f32_16x16x128_f8f6f4 v[80:83], v[136:143], v[32:39], v[180:183]
	v_mfma_f32_16x16x128_f8f6f4 v[68:71], v[128:135], v[40:47], v[184:187]
	v_mfma_f32_16x16x128_f8f6f4 v[64:67], v[136:143], v[40:47], v[188:191]
	s_setprio 0
	s_barrier
	s_mov_b32 m0, s58
	s_bitset1_b32 s31, 7
	buffer_load_dwordx4 v222, s[4:7], s31 offen lds
	s_mov_b32 m0, s59
	ds_read_b128 v[32:35], v172 offset:49152
	buffer_load_dwordx4 v193, s[4:7], s31 offen lds
	s_add_i32 s31, s31, s41
	s_mov_b32 m0, s65
	ds_read_b128 v[36:39], v172 offset:50176
	buffer_load_dwordx4 v222, s[4:7], s31 offen lds
	s_mov_b32 m0, s12
	ds_read_b128 v[144:147], v172 offset:51200
	buffer_load_dwordx4 v192, s[36:39], s30 offen lds
	s_mov_b32 m0, s13
	ds_read_b128 v[148:151], v172 offset:52224
	buffer_load_dwordx4 v223, s[36:39], s30 offen lds
	ds_read_b128 v[152:155], v172 offset:53248
	ds_read_b128 v[156:159], v172 offset:54272
	ds_read_b128 v[176:179], v172 offset:55296
	ds_read_b128 v[180:183], v172 offset:56320
	s_waitcnt vmcnt(7)
	s_waitcnt lgkmcnt(0)
	s_barrier
	s_setprio 1
	v_mfma_f32_16x16x128_f8f6f4 v[60:63], v[0:7], v[32:39], v[60:63]
	v_mfma_f32_16x16x128_f8f6f4 v[56:59], v[16:23], v[32:39], v[56:59]
	v_mfma_f32_16x16x128_f8f6f4 v[44:47], v[0:7], v[144:151], v[194:197]
	v_mfma_f32_16x16x128_f8f6f4 v[40:43], v[16:23], v[144:151], v[198:201]
	v_mfma_f32_16x16x128_f8f6f4 v[28:31], v[0:7], v[152:159], v[202:205]
	v_mfma_f32_16x16x128_f8f6f4 v[24:27], v[16:23], v[152:159], v[206:209]
	v_mfma_f32_16x16x128_f8f6f4 v[12:15], v[0:7], v[176:183], v[236:239]
	v_mfma_f32_16x16x128_f8f6f4 v[8:11], v[16:23], v[176:183], v[240:243]
	v_mfma_f32_16x16x128_f8f6f4 v[52:55], v[128:135], v[32:39], v[52:55]
	v_mfma_f32_16x16x128_f8f6f4 v[48:51], v[136:143], v[32:39], v[48:51]
	v_mfma_f32_16x16x128_f8f6f4 v[36:39], v[128:135], v[144:151], v[244:247]
	v_mfma_f32_16x16x128_f8f6f4 v[32:35], v[136:143], v[144:151], v[248:251]
	v_mfma_f32_16x16x128_f8f6f4 v[20:23], v[128:135], v[152:159], v[226:229]
	v_mfma_f32_16x16x128_f8f6f4 v[16:19], v[136:143], v[152:159], v[232:235]
	v_mfma_f32_16x16x128_f8f6f4 v[4:7], v[128:135], v[176:183], v[164:167]
	v_mfma_f32_16x16x128_f8f6f4 v[0:3], v[136:143], v[176:183], v[168:171]
	s_setprio 0
	s_barrier
	s_add_i32 s29, s29, 2
	s_addk_i32 s16, 0x100
	s_addk_i32 s28, 0x100
	s_cmp_ge_i32 s29, s77
	s_cbranch_scc0 .LBB0_258
	s_mov_b32 m0, s33
	s_nop 0
	buffer_load_dwordx4 v193, s[4:7], s31 offen lds

; #define PG8_STAGE(bufoff, rs_, soff_, voff) do { _Pragma("unroll") for (int _i = 0; _i < 2; ++_i) \
;         __builtin_amdgcn_raw_ptr_buffer_load_lds(rs_, (LAS void*)(lds + (bufoff) + ldsw + _i * 8192), 16, (int)(voff)[_i], (int)(soff_), 0, 0); } while (0)
; #define PG8_LDA(dst, b, h) do { _Pragma("unroll") for (int m = 0; m < 4; ++m) dst[m] = PG8_LD2(lds + PG8_SA(b, h) + aoff + m * 2048); } while (0)
; #define PG8_LDB(dst, b, h) do { _Pragma("unroll") for (int n = 0; n < 2; ++n) dst[n] = PG8_LD2(lds + PG8_SB(b, h) + boff + n * 2048); } while (0)
; #define PG8_WAIT_V(n) asm volatile("s_waitcnt vmcnt(" #n ")" ::: "memory")
; #define PG8_WAIT_L(n) asm volatile("s_waitcnt lgkmcnt(" #n ")" ::: "memory")
; #define PG8_BAR __builtin_amdgcn_s_barrier()
; #define PG8_SCHED __builtin_amdgcn_sched_barrier(0)
; template <class Epi, class Sched, bool ALIGN_EPI = false, bool SP2 = false, bool FP8 = false>
; __device__ __forceinline__ void gemm_phase(LAS unsigned char* lds, const Gemm g, const Sched& S, const Epi& E, int wbase) {
;     ...
;             PG8_LDB(B0, 0, 0); PG8_LDB(B1, 0, 1); PG8_SCHED; PG8_LDA(At, 0, 0); PG8_STAGE(PG8_SA(1, 1), rAc, a1 + hstep, voffA);
;             PG8_WAIT_V(8); PG8_WAIT_L(0); PG8_BAR; PG8_MMA(0, 0, At, B0); PG8_MMA(0, 1, At, B1); PG8_BAR; PG8_SCHED;
;             PG8_LDA(At, 0, 1); PG8_STAGE(PG8_SB(0, 0), rB2, b2, voffB); PG8_STAGE(PG8_SB(0, 1), rB2, b2 + hstep, voffB); PG8_STAGE(PG8_SA(0, 0), rA2, a2, voffA);
;             PG8_WAIT_V(8); PG8_WAIT_L(0); PG8_BAR; PG8_MMA(1, 0, At, B0); PG8_MMA(1, 1, At, B1); PG8_BAR; PG8_SCHED;
;             PG8_LDB(B0, 1, 0); PG8_LDB(B1, 1, 1); PG8_SCHED; PG8_LDA(At, 1, 0); PG8_STAGE(PG8_SA(0, 1), rA2, a2 + hstep, voffA);
;             PG8_WAIT_V(8); PG8_WAIT_L(0); PG8_BAR; PG8_MMA(0, 0, At, B0); PG8_MMA(0, 1, At, B1); PG8_BAR; PG8_SCHED;
.LBB0_352:
	s_mov_b32 m0, s76
	s_nop 0
	buffer_load_dwordx4 v167, s[4:7], s31 offen lds
	v_add_u32_e32 v140, 0x10000, v170
	v_add_u32_e32 v156, 0x14000, v170
	ds_read_b128 v[128:131], v140
	ds_read_b128 v[132:135], v140 offset:1024
	ds_read_b128 v[136:139], v140 offset:2048
	ds_read_b128 v[140:143], v140 offset:3072
	ds_read_b128 v[144:147], v156
	ds_read_b128 v[148:151], v156 offset:1024
	ds_read_b128 v[152:155], v156 offset:2048
	ds_read_b128 v[156:159], v156 offset:3072
	s_add_i32 s6, s16, 0x80
	s_cmp_eq_u32 s12, s29
	s_cselect_b32 s46, s2, s6
	s_cselect_b32 s31, s3, s28
	s_or_b32 s30, s46, 0x80
	s_add_i32 s6, s33, s16
	s_mov_b32 m0, s13
	ds_read_b128 v[160:163], v171
	ds_read_b128 v[172:175], v171 offset:1024
	ds_read_b128 v[176:179], v171 offset:2048
	ds_read_b128 v[180:183], v171 offset:3072
	ds_read_b128 v[184:187], v171 offset:4096
	ds_read_b128 v[188:191], v171 offset:5120
	ds_read_b128 v[194:197], v171 offset:6144
	ds_read_b128 v[198:201], v171 offset:7168
	buffer_load_dwordx4 v164, s[36:39], s6 offen lds
	s_mov_b32 m0, s83
	s_nop 0
	buffer_load_dwordx4 v166, s[36:39], s6 offen lds
	s_waitcnt vmcnt(8)
	s_waitcnt lgkmcnt(0)
	s_barrier
	s_setprio 1
	v_mfma_f32_16x16x32_bf16 v[124:127], v[128:131], v[160:163], v[124:127]
	v_mfma_f32_16x16x32_bf16 v[120:123], v[136:139], v[160:163], v[120:123]
	v_mfma_f32_16x16x32_bf16 v[108:111], v[128:131], v[176:179], v[108:111]
	v_mfma_f32_16x16x32_bf16 v[104:107], v[136:139], v[176:179], v[104:107]
	v_mfma_f32_16x16x32_bf16 v[92:95], v[128:131], v[184:187], v[92:95]
	v_mfma_f32_16x16x32_bf16 v[88:91], v[136:139], v[184:187], v[88:91]
	v_mfma_f32_16x16x32_bf16 v[76:79], v[128:131], v[194:197], v[76:79]
	v_mfma_f32_16x16x32_bf16 v[72:75], v[136:139], v[194:197], v[72:75]
	v_mfma_f32_16x16x32_bf16 v[124:127], v[132:135], v[172:175], v[124:127]
	v_mfma_f32_16x16x32_bf16 v[120:123], v[140:143], v[172:175], v[120:123]
	v_mfma_f32_16x16x32_bf16 v[108:111], v[132:135], v[180:183], v[108:111]
	v_mfma_f32_16x16x32_bf16 v[104:107], v[140:143], v[180:183], v[104:107]
	v_mfma_f32_16x16x32_bf16 v[92:95], v[132:135], v[188:191], v[92:95]
	v_mfma_f32_16x16x32_bf16 v[88:91], v[140:143], v[188:191], v[88:91]
	v_mfma_f32_16x16x32_bf16 v[76:79], v[132:135], v[198:201], v[76:79]
	v_mfma_f32_16x16x32_bf16 v[72:75], v[140:143], v[198:201], v[72:75]
	v_mfma_f32_16x16x32_bf16 v[116:119], v[144:147], v[160:163], v[116:119]
	v_mfma_f32_16x16x32_bf16 v[112:115], v[152:155], v[160:163], v[112:115]
	v_mfma_f32_16x16x32_bf16 v[100:103], v[144:147], v[176:179], v[100:103]
	v_mfma_f32_16x16x32_bf16 v[96:99], v[152:155], v[176:179], v[96:99]
	v_mfma_f32_16x16x32_bf16 v[84:87], v[144:147], v[184:187], v[84:87]
	v_mfma_f32_16x16x32_bf16 v[80:83], v[152:155], v[184:187], v[80:83]
	v_mfma_f32_16x16x32_bf16 v[68:71], v[144:147], v[194:197], v[68:71]
	v_mfma_f32_16x16x32_bf16 v[64:67], v[152:155], v[194:197], v[64:67]
	v_mfma_f32_16x16x32_bf16 v[116:119], v[148:151], v[172:175], v[116:119]
	v_mfma_f32_16x16x32_bf16 v[112:115], v[156:159], v[172:175], v[112:115]
	v_mfma_f32_16x16x32_bf16 v[100:103], v[148:151], v[180:183], v[100:103]
	v_mfma_f32_16x16x32_bf16 v[96:99], v[156:159], v[180:183], v[96:99]
	v_mfma_f32_16x16x32_bf16 v[84:87], v[148:151], v[188:191], v[84:87]
	v_mfma_f32_16x16x32_bf16 v[80:83], v[156:159], v[188:191], v[80:83]
	v_mfma_f32_16x16x32_bf16 v[68:71], v[148:151], v[198:201], v[68:71]
	v_mfma_f32_16x16x32_bf16 v[64:67], v[156:159], v[198:201], v[64:67]
	s_setprio 0
	s_barrier
	s_mov_b32 m0, s42
	s_mov_b32 s6, s38
	s_mov_b32 s7, s39
	buffer_load_dwordx4 v165, s[4:7], s31 offen lds
	s_mov_b32 m0, s43
	ds_read_b128 v[160:163], v171 offset:16384
	s_add_i32 s47, s31, s33
	buffer_load_dwordx4 v167, s[4:7], s31 offen lds
	s_mov_b32 m0, s44
	ds_read_b128 v[172:175], v171 offset:17408
	buffer_load_dwordx4 v165, s[4:7], s47 offen lds
	s_mov_b32 m0, s41
	ds_read_b128 v[176:179], v171 offset:18432
	buffer_load_dwordx4 v164, s[36:39], s46 offen lds
	s_mov_b32 m0, s52
	ds_read_b128 v[180:183], v171 offset:19456
	buffer_load_dwordx4 v166, s[36:39], s46 offen lds
	ds_read_b128 v[184:187], v171 offset:20480
	ds_read_b128 v[188:191], v171 offset:21504
	ds_read_b128 v[194:197], v171 offset:22528
	ds_read_b128 v[198:201], v171 offset:23552
	s_waitcnt vmcnt(7)
	s_waitcnt lgkmcnt(0)
	s_barrier
	s_setprio 1
	v_mfma_f32_16x16x32_bf16 v[60:63], v[128:131], v[160:163], v[60:63]
	v_mfma_f32_16x16x32_bf16 v[56:59], v[136:139], v[160:163], v[56:59]
	v_mfma_f32_16x16x32_bf16 v[44:47], v[128:131], v[176:179], v[44:47]
	v_mfma_f32_16x16x32_bf16 v[40:43], v[136:139], v[176:179], v[40:43]
	v_mfma_f32_16x16x32_bf16 v[28:31], v[128:131], v[184:187], v[28:31]
	v_mfma_f32_16x16x32_bf16 v[24:27], v[136:139], v[184:187], v[24:27]
	v_mfma_f32_16x16x32_bf16 v[12:15], v[128:131], v[194:197], v[12:15]
	v_mfma_f32_16x16x32_bf16 v[8:11], v[136:139], v[194:197], v[8:11]
	v_mfma_f32_16x16x32_bf16 v[60:63], v[132:135], v[172:175], v[60:63]
	v_mfma_f32_16x16x32_bf16 v[56:59], v[140:143], v[172:175], v[56:59]
	v_mfma_f32_16x16x32_bf16 v[44:47], v[132:135], v[180:183], v[44:47]
	v_mfma_f32_16x16x32_bf16 v[40:43], v[140:143], v[180:183], v[40:43]
	v_mfma_f32_16x16x32_bf16 v[28:31], v[132:135], v[188:191], v[28:31]
	v_mfma_f32_16x16x32_bf16 v[24:27], v[140:143], v[188:191], v[24:27]
	v_mfma_f32_16x16x32_bf16 v[12:15], v[132:135], v[198:201], v[12:15]
	v_mfma_f32_16x16x32_bf16 v[8:11], v[140:143], v[198:201], v[8:11]
	v_mfma_f32_16x16x32_bf16 v[52:55], v[144:147], v[160:163], v[52:55]
	v_mfma_f32_16x16x32_bf16 v[48:51], v[152:155], v[160:163], v[48:51]
	v_mfma_f32_16x16x32_bf16 v[36:39], v[144:147], v[176:179], v[36:39]
	v_mfma_f32_16x16x32_bf16 v[32:35], v[152:155], v[176:179], v[32:35]
	v_mfma_f32_16x16x32_bf16 v[20:23], v[144:147], v[184:187], v[20:23]
	v_mfma_f32_16x16x32_bf16 v[16:19], v[152:155], v[184:187], v[16:19]
	v_mfma_f32_16x16x32_bf16 v[4:7], v[144:147], v[194:197], v[4:7]
	v_mfma_f32_16x16x32_bf16 v[0:3], v[152:155], v[194:197], v[0:3]
	v_mfma_f32_16x16x32_bf16 v[52:55], v[148:151], v[172:175], v[52:55]
	v_mfma_f32_16x16x32_bf16 v[48:51], v[156:159], v[172:175], v[48:51]
	v_mfma_f32_16x16x32_bf16 v[36:39], v[148:151], v[180:183], v[36:39]
	v_mfma_f32_16x16x32_bf16 v[32:35], v[156:159], v[180:183], v[32:35]
	v_mfma_f32_16x16x32_bf16 v[20:23], v[148:151], v[188:191], v[20:23]
	v_mfma_f32_16x16x32_bf16 v[16:19], v[156:159], v[188:191], v[16:19]
	v_mfma_f32_16x16x32_bf16 v[4:7], v[148:151], v[198:201], v[4:7]
	v_mfma_f32_16x16x32_bf16 v[0:3], v[156:159], v[198:201], v[0:3]
	s_setprio 0
	s_barrier
; #define PG8_STAGE(bufoff, rs_, soff_, voff) do { _Pragma("unroll") for (int _i = 0; _i < 2; ++_i) \
;         __builtin_amdgcn_raw_ptr_buffer_load_lds(rs_, (LAS void*)(lds + (bufoff) + ldsw + _i * 8192), 16, (int)(voff)[_i], (int)(soff_), 0, 0); } while (0)
; #define PG8_LDA(dst, b, h) do { _Pragma("unroll") for (int m = 0; m < 4; ++m) dst[m] = PG8_LD2(lds + PG8_SA(b, h) + aoff + m * 2048); } while (0)
; #define PG8_LDB(dst, b, h) do { _Pragma("unroll") for (int n = 0; n < 2; ++n) dst[n] = PG8_LD2(lds + PG8_SB(b, h) + boff + n * 2048); } while (0)
; #define PG8_WAIT_V(n) asm volatile("s_waitcnt vmcnt(" #n ")" ::: "memory")
; #define PG8_WAIT_L(n) asm volatile("s_waitcnt lgkmcnt(" #n ")" ::: "memory")
; #define PG8_BAR __builtin_amdgcn_s_barrier()
; #define PG8_SCHED __builtin_amdgcn_sched_barrier(0)
; template <class Epi, class Sched, bool ALIGN_EPI = false, bool SP2 = false, bool FP8 = false>
; __device__ __forceinline__ void gemm_phase(LAS unsigned char* lds, const Gemm g, const Sched& S, const Epi& E, int wbase) {
;     ...
;         for (int t = 0; t < nt; t += 2) {
;             const bool last = (t == nt - 2);
;             const unsigned a1 = cA + (unsigned)(t + 1) * kstep;
;     ...
;             PG8_LDA(At, 0, 1); PG8_STAGE(PG8_SB(0, 0), rB2, b2, voffB); PG8_STAGE(PG8_SB(0, 1), rB2, b2 + hstep, voffB); PG8_STAGE(PG8_SA(0, 0), rA2, a2, voffA);
;             PG8_WAIT_V(8); PG8_WAIT_L(0); PG8_BAR; PG8_MMA(1, 0, At, B0); PG8_MMA(1, 1, At, B1); PG8_BAR; PG8_SCHED;
;             PG8_LDB(B0, 1, 0); PG8_LDB(B1, 1, 1); PG8_SCHED; PG8_LDA(At, 1, 0); PG8_STAGE(PG8_SA(0, 1), rA2, a2 + hstep, voffA);
;             PG8_WAIT_V(8); PG8_WAIT_L(0); PG8_BAR; PG8_MMA(0, 0, At, B0); PG8_MMA(0, 1, At, B1); PG8_BAR; PG8_SCHED;
;             PG8_LDA(At, 1, 1); PG8_STAGE(PG8_SB(1, 0), rB2, b3, voffB); PG8_STAGE(PG8_SB(1, 1), rB2, b3 + hstep, voffB); PG8_STAGE(PG8_SA(1, 0), rA2, a3, voffA);
;             PG8_WAIT_V(8); PG8_WAIT_L(0); PG8_BAR; PG8_MMA(1, 0, At, B0); PG8_MMA(1, 1, At, B1); PG8_BAR; PG8_SCHED;
	s_mov_b32 m0, s45
	s_nop 0
	buffer_load_dwordx4 v167, s[4:7], s47 offen lds
	v_add_u32_e32 v140, 0x18000, v170
	v_add_u32_e32 v156, 0x1c000, v170
	ds_read_b128 v[128:131], v140
	ds_read_b128 v[132:135], v140 offset:1024
	ds_read_b128 v[136:139], v140 offset:2048
	ds_read_b128 v[140:143], v140 offset:3072
	ds_read_b128 v[144:147], v156
	ds_read_b128 v[148:151], v156 offset:1024
	ds_read_b128 v[152:155], v156 offset:2048
	ds_read_b128 v[156:159], v156 offset:3072
	s_add_i32 s46, s46, s33
	s_mov_b32 m0, s53
	ds_read_b128 v[160:163], v171 offset:32768
	ds_read_b128 v[172:175], v171 offset:33792
	ds_read_b128 v[176:179], v171 offset:34816
	ds_read_b128 v[180:183], v171 offset:35840
	ds_read_b128 v[184:187], v171 offset:36864
	ds_read_b128 v[188:191], v171 offset:37888
	ds_read_b128 v[194:197], v171 offset:38912
	ds_read_b128 v[198:201], v171 offset:39936
	buffer_load_dwordx4 v164, s[36:39], s46 offen lds
	s_mov_b32 m0, s1
	s_nop 0
	buffer_load_dwordx4 v166, s[36:39], s46 offen lds
	s_waitcnt vmcnt(8)
	s_waitcnt lgkmcnt(0)
	s_barrier
	s_setprio 1
	v_mfma_f32_16x16x32_bf16 v[124:127], v[128:131], v[160:163], v[124:127]
	v_mfma_f32_16x16x32_bf16 v[120:123], v[136:139], v[160:163], v[120:123]
	v_mfma_f32_16x16x32_bf16 v[108:111], v[128:131], v[176:179], v[108:111]
	v_mfma_f32_16x16x32_bf16 v[104:107], v[136:139], v[176:179], v[104:107]
	v_mfma_f32_16x16x32_bf16 v[92:95], v[128:131], v[184:187], v[92:95]
	v_mfma_f32_16x16x32_bf16 v[88:91], v[136:139], v[184:187], v[88:91]
	v_mfma_f32_16x16x32_bf16 v[76:79], v[128:131], v[194:197], v[76:79]
	v_mfma_f32_16x16x32_bf16 v[72:75], v[136:139], v[194:197], v[72:75]
	v_mfma_f32_16x16x32_bf16 v[124:127], v[132:135], v[172:175], v[124:127]
	v_mfma_f32_16x16x32_bf16 v[120:123], v[140:143], v[172:175], v[120:123]
	v_mfma_f32_16x16x32_bf16 v[108:111], v[132:135], v[180:183], v[108:111]
	v_mfma_f32_16x16x32_bf16 v[104:107], v[140:143], v[180:183], v[104:107]
	v_mfma_f32_16x16x32_bf16 v[92:95], v[132:135], v[188:191], v[92:95]
	v_mfma_f32_16x16x32_bf16 v[88:91], v[140:143], v[188:191], v[88:91]
	v_mfma_f32_16x16x32_bf16 v[76:79], v[132:135], v[198:201], v[76:79]
	v_mfma_f32_16x16x32_bf16 v[72:75], v[140:143], v[198:201], v[72:75]
	v_mfma_f32_16x16x32_bf16 v[116:119], v[144:147], v[160:163], v[116:119]
	v_mfma_f32_16x16x32_bf16 v[112:115], v[152:155], v[160:163], v[112:115]
	v_mfma_f32_16x16x32_bf16 v[100:103], v[144:147], v[176:179], v[100:103]
	v_mfma_f32_16x16x32_bf16 v[96:99], v[152:155], v[176:179], v[96:99]
	v_mfma_f32_16x16x32_bf16 v[84:87], v[144:147], v[184:187], v[84:87]
	v_mfma_f32_16x16x32_bf16 v[80:83], v[152:155], v[184:187], v[80:83]
	v_mfma_f32_16x16x32_bf16 v[68:71], v[144:147], v[194:197], v[68:71]
	v_mfma_f32_16x16x32_bf16 v[64:67], v[152:155], v[194:197], v[64:67]
	v_mfma_f32_16x16x32_bf16 v[116:119], v[148:151], v[172:175], v[116:119]
	v_mfma_f32_16x16x32_bf16 v[112:115], v[156:159], v[172:175], v[112:115]
	v_mfma_f32_16x16x32_bf16 v[100:103], v[148:151], v[180:183], v[100:103]
	v_mfma_f32_16x16x32_bf16 v[96:99], v[156:159], v[180:183], v[96:99]
	v_mfma_f32_16x16x32_bf16 v[84:87], v[148:151], v[188:191], v[84:87]
	v_mfma_f32_16x16x32_bf16 v[80:83], v[156:159], v[188:191], v[80:83]
	v_mfma_f32_16x16x32_bf16 v[68:71], v[148:151], v[198:201], v[68:71]
	v_mfma_f32_16x16x32_bf16 v[64:67], v[156:159], v[198:201], v[64:67]
	s_setprio 0
	s_barrier
	s_mov_b32 m0, s56
	s_bitset1_b32 s31, 7
	buffer_load_dwordx4 v165, s[4:7], s31 offen lds
	s_mov_b32 m0, s57
	ds_read_b128 v[160:163], v171 offset:49152
	buffer_load_dwordx4 v167, s[4:7], s31 offen lds
	s_add_i32 s31, s31, s33
	s_mov_b32 m0, s65
	ds_read_b128 v[172:175], v171 offset:50176
	buffer_load_dwordx4 v165, s[4:7], s31 offen lds
	s_mov_b32 m0, s58
	ds_read_b128 v[176:179], v171 offset:51200
	buffer_load_dwordx4 v164, s[36:39], s30 offen lds
	s_mov_b32 m0, s59
	ds_read_b128 v[180:183], v171 offset:52224
	buffer_load_dwordx4 v166, s[36:39], s30 offen lds
	ds_read_b128 v[184:187], v171 offset:53248
	ds_read_b128 v[188:191], v171 offset:54272
	ds_read_b128 v[194:197], v171 offset:55296
	ds_read_b128 v[198:201], v171 offset:56320
	s_waitcnt vmcnt(7)
	s_waitcnt lgkmcnt(0)
	s_barrier
	s_setprio 1
	v_mfma_f32_16x16x32_bf16 v[60:63], v[128:131], v[160:163], v[60:63]
	v_mfma_f32_16x16x32_bf16 v[56:59], v[136:139], v[160:163], v[56:59]
	v_mfma_f32_16x16x32_bf16 v[44:47], v[128:131], v[176:179], v[44:47]
	v_mfma_f32_16x16x32_bf16 v[40:43], v[136:139], v[176:179], v[40:43]
	v_mfma_f32_16x16x32_bf16 v[28:31], v[128:131], v[184:187], v[28:31]
	v_mfma_f32_16x16x32_bf16 v[24:27], v[136:139], v[184:187], v[24:27]
	v_mfma_f32_16x16x32_bf16 v[12:15], v[128:131], v[194:197], v[12:15]
	v_mfma_f32_16x16x32_bf16 v[8:11], v[136:139], v[194:197], v[8:11]
	v_mfma_f32_16x16x32_bf16 v[60:63], v[132:135], v[172:175], v[60:63]
	v_mfma_f32_16x16x32_bf16 v[56:59], v[140:143], v[172:175], v[56:59]
	v_mfma_f32_16x16x32_bf16 v[44:47], v[132:135], v[180:183], v[44:47]
	v_mfma_f32_16x16x32_bf16 v[40:43], v[140:143], v[180:183], v[40:43]
	v_mfma_f32_16x16x32_bf16 v[28:31], v[132:135], v[188:191], v[28:31]
	v_mfma_f32_16x16x32_bf16 v[24:27], v[140:143], v[188:191], v[24:27]
	v_mfma_f32_16x16x32_bf16 v[12:15], v[132:135], v[198:201], v[12:15]
	v_mfma_f32_16x16x32_bf16 v[8:11], v[140:143], v[198:201], v[8:11]
	v_mfma_f32_16x16x32_bf16 v[52:55], v[144:147], v[160:163], v[52:55]
	v_mfma_f32_16x16x32_bf16 v[48:51], v[152:155], v[160:163], v[48:51]
	v_mfma_f32_16x16x32_bf16 v[36:39], v[144:147], v[176:179], v[36:39]
	v_mfma_f32_16x16x32_bf16 v[32:35], v[152:155], v[176:179], v[32:35]
	v_mfma_f32_16x16x32_bf16 v[20:23], v[144:147], v[184:187], v[20:23]
	v_mfma_f32_16x16x32_bf16 v[16:19], v[152:155], v[184:187], v[16:19]
	v_mfma_f32_16x16x32_bf16 v[4:7], v[144:147], v[194:197], v[4:7]
	v_mfma_f32_16x16x32_bf16 v[0:3], v[152:155], v[194:197], v[0:3]
	v_mfma_f32_16x16x32_bf16 v[52:55], v[148:151], v[172:175], v[52:55]
	v_mfma_f32_16x16x32_bf16 v[48:51], v[156:159], v[172:175], v[48:51]
	v_mfma_f32_16x16x32_bf16 v[36:39], v[148:151], v[180:183], v[36:39]
	v_mfma_f32_16x16x32_bf16 v[32:35], v[156:159], v[180:183], v[32:35]
	v_mfma_f32_16x16x32_bf16 v[20:23], v[148:151], v[188:191], v[20:23]
	v_mfma_f32_16x16x32_bf16 v[16:19], v[156:159], v[188:191], v[16:19]
	v_mfma_f32_16x16x32_bf16 v[4:7], v[148:151], v[198:201], v[4:7]
	v_mfma_f32_16x16x32_bf16 v[0:3], v[156:159], v[198:201], v[0:3]
	s_setprio 0
	s_barrier
	s_add_i32 s29, s29, 2
	s_addk_i32 s16, 0x100
	s_addk_i32 s28, 0x100
	s_cmp_ge_i32 s29, s82
	s_cbranch_scc0 .LBB0_352
	s_mov_b32 m0, s76
	s_nop 0
	buffer_load_dwordx4 v167, s[4:7], s31 offen lds

; #define PG8_STAGE(bufoff, rs_, soff_, voff) do { _Pragma("unroll") for (int _i = 0; _i < 2; ++_i) \
;         __builtin_amdgcn_raw_ptr_buffer_load_lds(rs_, (LAS void*)(lds + (bufoff) + ldsw + _i * 8192), 16, (int)(voff)[_i], (int)(soff_), 0, 0); } while (0)
; #define PG8_LDA(dst, b, h) do { _Pragma("unroll") for (int m = 0; m < 4; ++m) dst[m] = PG8_LD2(lds + PG8_SA(b, h) + aoff + m * 2048); } while (0)
; #define PG8_LDB(dst, b, h) do { _Pragma("unroll") for (int n = 0; n < 2; ++n) dst[n] = PG8_LD2(lds + PG8_SB(b, h) + boff + n * 2048); } while (0)
; #define PG8_WAIT_V(n) asm volatile("s_waitcnt vmcnt(" #n ")" ::: "memory")
; #define PG8_WAIT_L(n) asm volatile("s_waitcnt lgkmcnt(" #n ")" ::: "memory")
; #define PG8_BAR __builtin_amdgcn_s_barrier()
; #define PG8_SCHED __builtin_amdgcn_sched_barrier(0)
; template <class Epi, class Sched, bool ALIGN_EPI = false, bool SP2 = false, bool FP8 = false>
; __device__ __forceinline__ void gemm_phase(LAS unsigned char* lds, const Gemm g, const Sched& S, const Epi& E, int wbase) {
;     ...
;             PG8_LDB(B0, 0, 0); PG8_LDB(B1, 0, 1); PG8_SCHED; PG8_LDA(At, 0, 0); PG8_STAGE(PG8_SA(1, 1), rAc, a1 + hstep, voffA);
;             PG8_WAIT_V(8); PG8_WAIT_L(0); PG8_BAR; PG8_MMA(0, 0, At, B0); PG8_MMA(0, 1, At, B1); PG8_BAR; PG8_SCHED;
;             PG8_LDA(At, 0, 1); PG8_STAGE(PG8_SB(0, 0), rB2, b2, voffB); PG8_STAGE(PG8_SB(0, 1), rB2, b2 + hstep, voffB); PG8_STAGE(PG8_SA(0, 0), rA2, a2, voffA);
;             PG8_WAIT_V(8); PG8_WAIT_L(0); PG8_BAR; PG8_MMA(1, 0, At, B0); PG8_MMA(1, 1, At, B1); PG8_BAR; PG8_SCHED;
;             PG8_LDB(B0, 1, 0); PG8_LDB(B1, 1, 1); PG8_SCHED; PG8_LDA(At, 1, 0); PG8_STAGE(PG8_SA(0, 1), rA2, a2 + hstep, voffA);
;             PG8_WAIT_V(8); PG8_WAIT_L(0); PG8_BAR; PG8_MMA(0, 0, At, B0); PG8_MMA(0, 1, At, B1); PG8_BAR; PG8_SCHED;
.LBB0_450:
	s_mov_b32 m0, s34
	s_nop 0
	buffer_load_dwordx4 v135, s[4:7], s55 offen lds
	v_add_u32_e32 v148, 0x10000, v138
	v_add_u32_e32 v164, 0x14000, v138
	ds_read_b128 v[128:131], v148
	ds_read_b128 v[140:143], v148 offset:1024
	ds_read_b128 v[144:147], v148 offset:2048
	ds_read_b128 v[148:151], v148 offset:3072
	ds_read_b128 v[152:155], v164
	ds_read_b128 v[156:159], v164 offset:1024
	ds_read_b128 v[160:163], v164 offset:2048
	ds_read_b128 v[164:167], v164 offset:3072
	s_add_i32 s6, s58, 0x80
	s_cmp_eq_u32 s42, s60
	s_cselect_b32 s61, s56, s6
	s_cselect_b32 s55, s57, s59
	s_or_b32 s54, s61, 0x80
	s_add_i32 s6, s19, s58
	s_mov_b32 m0, s43
	ds_read_b128 v[168:171], v139
	ds_read_b128 v[172:175], v139 offset:1024
	ds_read_b128 v[176:179], v139 offset:2048
	ds_read_b128 v[180:183], v139 offset:3072
	ds_read_b128 v[184:187], v139 offset:4096
	ds_read_b128 v[188:191], v139 offset:5120
	ds_read_b128 v[194:197], v139 offset:6144
	ds_read_b128 v[198:201], v139 offset:7168
	buffer_load_dwordx4 v132, s[36:39], s6 offen lds
	s_mov_b32 m0, s44
	s_nop 0
	buffer_load_dwordx4 v134, s[36:39], s6 offen lds
	s_waitcnt vmcnt(8)
	s_waitcnt lgkmcnt(0)
	s_barrier
	s_setprio 1
	v_mfma_f32_16x16x32_bf16 v[124:127], v[128:131], v[168:171], v[124:127]
	v_mfma_f32_16x16x32_bf16 v[120:123], v[144:147], v[168:171], v[120:123]
	v_mfma_f32_16x16x32_bf16 v[108:111], v[128:131], v[176:179], v[108:111]
	v_mfma_f32_16x16x32_bf16 v[104:107], v[144:147], v[176:179], v[104:107]
	v_mfma_f32_16x16x32_bf16 v[92:95], v[128:131], v[184:187], v[92:95]
	v_mfma_f32_16x16x32_bf16 v[88:91], v[144:147], v[184:187], v[88:91]
	v_mfma_f32_16x16x32_bf16 v[76:79], v[128:131], v[194:197], v[76:79]
	v_mfma_f32_16x16x32_bf16 v[72:75], v[144:147], v[194:197], v[72:75]
	v_mfma_f32_16x16x32_bf16 v[124:127], v[140:143], v[172:175], v[124:127]
	v_mfma_f32_16x16x32_bf16 v[120:123], v[148:151], v[172:175], v[120:123]
	v_mfma_f32_16x16x32_bf16 v[108:111], v[140:143], v[180:183], v[108:111]
	v_mfma_f32_16x16x32_bf16 v[104:107], v[148:151], v[180:183], v[104:107]
	v_mfma_f32_16x16x32_bf16 v[92:95], v[140:143], v[188:191], v[92:95]
	v_mfma_f32_16x16x32_bf16 v[88:91], v[148:151], v[188:191], v[88:91]
	v_mfma_f32_16x16x32_bf16 v[76:79], v[140:143], v[198:201], v[76:79]
	v_mfma_f32_16x16x32_bf16 v[72:75], v[148:151], v[198:201], v[72:75]
	v_mfma_f32_16x16x32_bf16 v[116:119], v[152:155], v[168:171], v[116:119]
	v_mfma_f32_16x16x32_bf16 v[112:115], v[160:163], v[168:171], v[112:115]
	v_mfma_f32_16x16x32_bf16 v[100:103], v[152:155], v[176:179], v[100:103]
	v_mfma_f32_16x16x32_bf16 v[96:99], v[160:163], v[176:179], v[96:99]
	v_mfma_f32_16x16x32_bf16 v[84:87], v[152:155], v[184:187], v[84:87]
	v_mfma_f32_16x16x32_bf16 v[80:83], v[160:163], v[184:187], v[80:83]
	v_mfma_f32_16x16x32_bf16 v[68:71], v[152:155], v[194:197], v[68:71]
	v_mfma_f32_16x16x32_bf16 v[64:67], v[160:163], v[194:197], v[64:67]
	v_mfma_f32_16x16x32_bf16 v[116:119], v[156:159], v[172:175], v[116:119]
	v_mfma_f32_16x16x32_bf16 v[112:115], v[164:167], v[172:175], v[112:115]
	v_mfma_f32_16x16x32_bf16 v[100:103], v[156:159], v[180:183], v[100:103]
	v_mfma_f32_16x16x32_bf16 v[96:99], v[164:167], v[180:183], v[96:99]
	v_mfma_f32_16x16x32_bf16 v[84:87], v[156:159], v[188:191], v[84:87]
	v_mfma_f32_16x16x32_bf16 v[80:83], v[164:167], v[188:191], v[80:83]
	v_mfma_f32_16x16x32_bf16 v[68:71], v[156:159], v[198:201], v[68:71]
	v_mfma_f32_16x16x32_bf16 v[64:67], v[164:167], v[198:201], v[64:67]
	s_setprio 0
	s_barrier
	s_mov_b32 m0, s21
	s_mov_b32 s6, s38
	s_mov_b32 s7, s39
	buffer_load_dwordx4 v133, s[4:7], s55 offen lds
	s_mov_b32 m0, s22
	ds_read_b128 v[168:171], v139 offset:16384
	s_add_i32 s62, s55, s19
	buffer_load_dwordx4 v135, s[4:7], s55 offen lds
	s_mov_b32 m0, s23
	ds_read_b128 v[172:175], v139 offset:17408
	buffer_load_dwordx4 v133, s[4:7], s62 offen lds
	s_mov_b32 m0, s20
	ds_read_b128 v[176:179], v139 offset:18432
	buffer_load_dwordx4 v132, s[36:39], s61 offen lds
	s_mov_b32 m0, s25
	ds_read_b128 v[180:183], v139 offset:19456
	buffer_load_dwordx4 v134, s[36:39], s61 offen lds
	ds_read_b128 v[184:187], v139 offset:20480
	ds_read_b128 v[188:191], v139 offset:21504
	ds_read_b128 v[194:197], v139 offset:22528
	ds_read_b128 v[198:201], v139 offset:23552
	s_waitcnt vmcnt(7)
	s_waitcnt lgkmcnt(0)
	s_barrier
	s_setprio 1
	v_mfma_f32_16x16x32_bf16 v[60:63], v[128:131], v[168:171], v[60:63]
	v_mfma_f32_16x16x32_bf16 v[56:59], v[144:147], v[168:171], v[56:59]
	v_mfma_f32_16x16x32_bf16 v[44:47], v[128:131], v[176:179], v[44:47]
	v_mfma_f32_16x16x32_bf16 v[40:43], v[144:147], v[176:179], v[40:43]
	v_mfma_f32_16x16x32_bf16 v[28:31], v[128:131], v[184:187], v[28:31]
	v_mfma_f32_16x16x32_bf16 v[24:27], v[144:147], v[184:187], v[24:27]
	v_mfma_f32_16x16x32_bf16 v[12:15], v[128:131], v[194:197], v[12:15]
	v_mfma_f32_16x16x32_bf16 v[8:11], v[144:147], v[194:197], v[8:11]
	v_mfma_f32_16x16x32_bf16 v[60:63], v[140:143], v[172:175], v[60:63]
	v_mfma_f32_16x16x32_bf16 v[56:59], v[148:151], v[172:175], v[56:59]
	v_mfma_f32_16x16x32_bf16 v[44:47], v[140:143], v[180:183], v[44:47]
	v_mfma_f32_16x16x32_bf16 v[40:43], v[148:151], v[180:183], v[40:43]
	v_mfma_f32_16x16x32_bf16 v[28:31], v[140:143], v[188:191], v[28:31]
	v_mfma_f32_16x16x32_bf16 v[24:27], v[148:151], v[188:191], v[24:27]
	v_mfma_f32_16x16x32_bf16 v[12:15], v[140:143], v[198:201], v[12:15]
	v_mfma_f32_16x16x32_bf16 v[8:11], v[148:151], v[198:201], v[8:11]
	v_mfma_f32_16x16x32_bf16 v[52:55], v[152:155], v[168:171], v[52:55]
	v_mfma_f32_16x16x32_bf16 v[48:51], v[160:163], v[168:171], v[48:51]
	v_mfma_f32_16x16x32_bf16 v[36:39], v[152:155], v[176:179], v[36:39]
	v_mfma_f32_16x16x32_bf16 v[32:35], v[160:163], v[176:179], v[32:35]
	v_mfma_f32_16x16x32_bf16 v[20:23], v[152:155], v[184:187], v[20:23]
	v_mfma_f32_16x16x32_bf16 v[16:19], v[160:163], v[184:187], v[16:19]
	v_mfma_f32_16x16x32_bf16 v[4:7], v[152:155], v[194:197], v[4:7]
	v_mfma_f32_16x16x32_bf16 v[0:3], v[160:163], v[194:197], v[0:3]
	v_mfma_f32_16x16x32_bf16 v[52:55], v[156:159], v[172:175], v[52:55]
	v_mfma_f32_16x16x32_bf16 v[48:51], v[164:167], v[172:175], v[48:51]
	v_mfma_f32_16x16x32_bf16 v[36:39], v[156:159], v[180:183], v[36:39]
	v_mfma_f32_16x16x32_bf16 v[32:35], v[164:167], v[180:183], v[32:35]
	v_mfma_f32_16x16x32_bf16 v[20:23], v[156:159], v[188:191], v[20:23]
	v_mfma_f32_16x16x32_bf16 v[16:19], v[164:167], v[188:191], v[16:19]
	v_mfma_f32_16x16x32_bf16 v[4:7], v[156:159], v[198:201], v[4:7]
	v_mfma_f32_16x16x32_bf16 v[0:3], v[164:167], v[198:201], v[0:3]
	s_setprio 0
	s_barrier
; #define PG8_STAGE(bufoff, rs_, soff_, voff) do { _Pragma("unroll") for (int _i = 0; _i < 2; ++_i) \
;         __builtin_amdgcn_raw_ptr_buffer_load_lds(rs_, (LAS void*)(lds + (bufoff) + ldsw + _i * 8192), 16, (int)(voff)[_i], (int)(soff_), 0, 0); } while (0)
; #define PG8_LDA(dst, b, h) do { _Pragma("unroll") for (int m = 0; m < 4; ++m) dst[m] = PG8_LD2(lds + PG8_SA(b, h) + aoff + m * 2048); } while (0)
; #define PG8_LDB(dst, b, h) do { _Pragma("unroll") for (int n = 0; n < 2; ++n) dst[n] = PG8_LD2(lds + PG8_SB(b, h) + boff + n * 2048); } while (0)
; #define PG8_WAIT_V(n) asm volatile("s_waitcnt vmcnt(" #n ")" ::: "memory")
; #define PG8_WAIT_L(n) asm volatile("s_waitcnt lgkmcnt(" #n ")" ::: "memory")
; #define PG8_BAR __builtin_amdgcn_s_barrier()
; #define PG8_SCHED __builtin_amdgcn_sched_barrier(0)
; template <class Epi, class Sched, bool ALIGN_EPI = false, bool SP2 = false, bool FP8 = false>
; __device__ __forceinline__ void gemm_phase(LAS unsigned char* lds, const Gemm g, const Sched& S, const Epi& E, int wbase) {
;     ...
;         for (int t = 0; t < nt; t += 2) {
;             const bool last = (t == nt - 2);
;             const unsigned a1 = cA + (unsigned)(t + 1) * kstep;
;     ...
;             PG8_LDA(At, 0, 1); PG8_STAGE(PG8_SB(0, 0), rB2, b2, voffB); PG8_STAGE(PG8_SB(0, 1), rB2, b2 + hstep, voffB); PG8_STAGE(PG8_SA(0, 0), rA2, a2, voffA);
;             PG8_WAIT_V(8); PG8_WAIT_L(0); PG8_BAR; PG8_MMA(1, 0, At, B0); PG8_MMA(1, 1, At, B1); PG8_BAR; PG8_SCHED;
;             PG8_LDB(B0, 1, 0); PG8_LDB(B1, 1, 1); PG8_SCHED; PG8_LDA(At, 1, 0); PG8_STAGE(PG8_SA(0, 1), rA2, a2 + hstep, voffA);
;             PG8_WAIT_V(8); PG8_WAIT_L(0); PG8_BAR; PG8_MMA(0, 0, At, B0); PG8_MMA(0, 1, At, B1); PG8_BAR; PG8_SCHED;
;             PG8_LDA(At, 1, 1); PG8_STAGE(PG8_SB(1, 0), rB2, b3, voffB); PG8_STAGE(PG8_SB(1, 1), rB2, b3 + hstep, voffB); PG8_STAGE(PG8_SA(1, 0), rA2, a3, voffA);
;             PG8_WAIT_V(8); PG8_WAIT_L(0); PG8_BAR; PG8_MMA(1, 0, At, B0); PG8_MMA(1, 1, At, B1); PG8_BAR; PG8_SCHED;
	s_mov_b32 m0, s24
	s_nop 0
	buffer_load_dwordx4 v135, s[4:7], s62 offen lds
	v_add_u32_e32 v148, 0x18000, v138
	v_add_u32_e32 v164, 0x1c000, v138
	ds_read_b128 v[128:131], v148
	ds_read_b128 v[140:143], v148 offset:1024
	ds_read_b128 v[144:147], v148 offset:2048
	ds_read_b128 v[148:151], v148 offset:3072
	ds_read_b128 v[152:155], v164
	ds_read_b128 v[156:159], v164 offset:1024
	ds_read_b128 v[160:163], v164 offset:2048
	ds_read_b128 v[164:167], v164 offset:3072
	s_add_i32 s61, s61, s19
	s_mov_b32 m0, s26
	ds_read_b128 v[168:171], v139 offset:32768
	ds_read_b128 v[172:175], v139 offset:33792
	ds_read_b128 v[176:179], v139 offset:34816
	ds_read_b128 v[180:183], v139 offset:35840
	ds_read_b128 v[184:187], v139 offset:36864
	ds_read_b128 v[188:191], v139 offset:37888
	ds_read_b128 v[194:197], v139 offset:38912
	ds_read_b128 v[198:201], v139 offset:39936
	buffer_load_dwordx4 v132, s[36:39], s61 offen lds
	s_mov_b32 m0, s27
	s_nop 0
	buffer_load_dwordx4 v134, s[36:39], s61 offen lds
	s_waitcnt vmcnt(8)
	s_waitcnt lgkmcnt(0)
	s_barrier
	s_setprio 1
	v_mfma_f32_16x16x32_bf16 v[124:127], v[128:131], v[168:171], v[124:127]
	v_mfma_f32_16x16x32_bf16 v[120:123], v[144:147], v[168:171], v[120:123]
	v_mfma_f32_16x16x32_bf16 v[108:111], v[128:131], v[176:179], v[108:111]
	v_mfma_f32_16x16x32_bf16 v[104:107], v[144:147], v[176:179], v[104:107]
	v_mfma_f32_16x16x32_bf16 v[92:95], v[128:131], v[184:187], v[92:95]
	v_mfma_f32_16x16x32_bf16 v[88:91], v[144:147], v[184:187], v[88:91]
	v_mfma_f32_16x16x32_bf16 v[76:79], v[128:131], v[194:197], v[76:79]
	v_mfma_f32_16x16x32_bf16 v[72:75], v[144:147], v[194:197], v[72:75]
	v_mfma_f32_16x16x32_bf16 v[124:127], v[140:143], v[172:175], v[124:127]
	v_mfma_f32_16x16x32_bf16 v[120:123], v[148:151], v[172:175], v[120:123]
	v_mfma_f32_16x16x32_bf16 v[108:111], v[140:143], v[180:183], v[108:111]
	v_mfma_f32_16x16x32_bf16 v[104:107], v[148:151], v[180:183], v[104:107]
	v_mfma_f32_16x16x32_bf16 v[92:95], v[140:143], v[188:191], v[92:95]
	v_mfma_f32_16x16x32_bf16 v[88:91], v[148:151], v[188:191], v[88:91]
	v_mfma_f32_16x16x32_bf16 v[76:79], v[140:143], v[198:201], v[76:79]
	v_mfma_f32_16x16x32_bf16 v[72:75], v[148:151], v[198:201], v[72:75]
	v_mfma_f32_16x16x32_bf16 v[116:119], v[152:155], v[168:171], v[116:119]
	v_mfma_f32_16x16x32_bf16 v[112:115], v[160:163], v[168:171], v[112:115]
	v_mfma_f32_16x16x32_bf16 v[100:103], v[152:155], v[176:179], v[100:103]
	v_mfma_f32_16x16x32_bf16 v[96:99], v[160:163], v[176:179], v[96:99]
	v_mfma_f32_16x16x32_bf16 v[84:87], v[152:155], v[184:187], v[84:87]
	v_mfma_f32_16x16x32_bf16 v[80:83], v[160:163], v[184:187], v[80:83]
	v_mfma_f32_16x16x32_bf16 v[68:71], v[152:155], v[194:197], v[68:71]
	v_mfma_f32_16x16x32_bf16 v[64:67], v[160:163], v[194:197], v[64:67]
	v_mfma_f32_16x16x32_bf16 v[116:119], v[156:159], v[172:175], v[116:119]
	v_mfma_f32_16x16x32_bf16 v[112:115], v[164:167], v[172:175], v[112:115]
	v_mfma_f32_16x16x32_bf16 v[100:103], v[156:159], v[180:183], v[100:103]
	v_mfma_f32_16x16x32_bf16 v[96:99], v[164:167], v[180:183], v[96:99]
	v_mfma_f32_16x16x32_bf16 v[84:87], v[156:159], v[188:191], v[84:87]
	v_mfma_f32_16x16x32_bf16 v[80:83], v[164:167], v[188:191], v[80:83]
	v_mfma_f32_16x16x32_bf16 v[68:71], v[156:159], v[198:201], v[68:71]
	v_mfma_f32_16x16x32_bf16 v[64:67], v[164:167], v[198:201], v[64:67]
	s_setprio 0
	s_barrier
	s_mov_b32 m0, s28
	s_bitset1_b32 s55, 7
	buffer_load_dwordx4 v133, s[4:7], s55 offen lds
	s_mov_b32 m0, s29
	ds_read_b128 v[168:171], v139 offset:49152
	buffer_load_dwordx4 v135, s[4:7], s55 offen lds
	s_add_i32 s55, s55, s19
	s_mov_b32 m0, s33
	ds_read_b128 v[172:175], v139 offset:50176
	buffer_load_dwordx4 v133, s[4:7], s55 offen lds
	s_mov_b32 m0, s30
	ds_read_b128 v[176:179], v139 offset:51200
	buffer_load_dwordx4 v132, s[36:39], s54 offen lds
	s_mov_b32 m0, s31
	ds_read_b128 v[180:183], v139 offset:52224
	buffer_load_dwordx4 v134, s[36:39], s54 offen lds
	ds_read_b128 v[184:187], v139 offset:53248
	ds_read_b128 v[188:191], v139 offset:54272
	ds_read_b128 v[194:197], v139 offset:55296
	ds_read_b128 v[198:201], v139 offset:56320
	s_waitcnt vmcnt(7)
	s_waitcnt lgkmcnt(0)
	s_barrier
	s_setprio 1
	v_mfma_f32_16x16x32_bf16 v[60:63], v[128:131], v[168:171], v[60:63]
	v_mfma_f32_16x16x32_bf16 v[56:59], v[144:147], v[168:171], v[56:59]
	v_mfma_f32_16x16x32_bf16 v[44:47], v[128:131], v[176:179], v[44:47]
	v_mfma_f32_16x16x32_bf16 v[40:43], v[144:147], v[176:179], v[40:43]
	v_mfma_f32_16x16x32_bf16 v[28:31], v[128:131], v[184:187], v[28:31]
	v_mfma_f32_16x16x32_bf16 v[24:27], v[144:147], v[184:187], v[24:27]
	v_mfma_f32_16x16x32_bf16 v[12:15], v[128:131], v[194:197], v[12:15]
	v_mfma_f32_16x16x32_bf16 v[8:11], v[144:147], v[194:197], v[8:11]
	v_mfma_f32_16x16x32_bf16 v[60:63], v[140:143], v[172:175], v[60:63]
	v_mfma_f32_16x16x32_bf16 v[56:59], v[148:151], v[172:175], v[56:59]
	v_mfma_f32_16x16x32_bf16 v[44:47], v[140:143], v[180:183], v[44:47]
	v_mfma_f32_16x16x32_bf16 v[40:43], v[148:151], v[180:183], v[40:43]
	v_mfma_f32_16x16x32_bf16 v[28:31], v[140:143], v[188:191], v[28:31]
	v_mfma_f32_16x16x32_bf16 v[24:27], v[148:151], v[188:191], v[24:27]
	v_mfma_f32_16x16x32_bf16 v[12:15], v[140:143], v[198:201], v[12:15]
	v_mfma_f32_16x16x32_bf16 v[8:11], v[148:151], v[198:201], v[8:11]
	v_mfma_f32_16x16x32_bf16 v[52:55], v[152:155], v[168:171], v[52:55]
	v_mfma_f32_16x16x32_bf16 v[48:51], v[160:163], v[168:171], v[48:51]
	v_mfma_f32_16x16x32_bf16 v[36:39], v[152:155], v[176:179], v[36:39]
	v_mfma_f32_16x16x32_bf16 v[32:35], v[160:163], v[176:179], v[32:35]
	v_mfma_f32_16x16x32_bf16 v[20:23], v[152:155], v[184:187], v[20:23]
	v_mfma_f32_16x16x32_bf16 v[16:19], v[160:163], v[184:187], v[16:19]
	v_mfma_f32_16x16x32_bf16 v[4:7], v[152:155], v[194:197], v[4:7]
	v_mfma_f32_16x16x32_bf16 v[0:3], v[160:163], v[194:197], v[0:3]
	v_mfma_f32_16x16x32_bf16 v[52:55], v[156:159], v[172:175], v[52:55]
	v_mfma_f32_16x16x32_bf16 v[48:51], v[164:167], v[172:175], v[48:51]
	v_mfma_f32_16x16x32_bf16 v[36:39], v[156:159], v[180:183], v[36:39]
	v_mfma_f32_16x16x32_bf16 v[32:35], v[164:167], v[180:183], v[32:35]
	v_mfma_f32_16x16x32_bf16 v[20:23], v[156:159], v[188:191], v[20:23]
	v_mfma_f32_16x16x32_bf16 v[16:19], v[164:167], v[188:191], v[16:19]
	v_mfma_f32_16x16x32_bf16 v[4:7], v[156:159], v[198:201], v[4:7]
	v_mfma_f32_16x16x32_bf16 v[0:3], v[164:167], v[198:201], v[0:3]
	s_setprio 0
	s_barrier
	s_add_i32 s60, s60, 2
	s_addk_i32 s58, 0x100
	s_addk_i32 s59, 0x100
	s_cmp_ge_i32 s60, s35
	s_cbranch_scc0 .LBB0_450
	s_mov_b32 m0, s34
	s_nop 0
	buffer_load_dwordx4 v135, s[4:7], s55 offen lds

; #define PG8_STAGE(bufoff, rs_, soff_, voff) do { _Pragma("unroll") for (int _i = 0; _i < 2; ++_i) \
;         __builtin_amdgcn_raw_ptr_buffer_load_lds(rs_, (LAS void*)(lds + (bufoff) + ldsw + _i * 8192), 16, (int)(voff)[_i], (int)(soff_), 0, 0); } while (0)
; #define PG8_LDA(dst, b, h) do { _Pragma("unroll") for (int m = 0; m < 4; ++m) dst[m] = PG8_LD2(lds + PG8_SA(b, h) + aoff + m * 2048); } while (0)
; #define PG8_LDB(dst, b, h) do { _Pragma("unroll") for (int n = 0; n < 2; ++n) dst[n] = PG8_LD2(lds + PG8_SB(b, h) + boff + n * 2048); } while (0)
; #define PG8_WAIT_V(n) asm volatile("s_waitcnt vmcnt(" #n ")" ::: "memory")
; #define PG8_WAIT_L(n) asm volatile("s_waitcnt lgkmcnt(" #n ")" ::: "memory")
; #define PG8_BAR __builtin_amdgcn_s_barrier()
; #define PG8_SCHED __builtin_amdgcn_sched_barrier(0)
; template <class Epi, class Sched, bool ALIGN_EPI = false, bool SP2 = false, bool FP8 = false>
; __device__ __forceinline__ void gemm_phase(LAS unsigned char* lds, const Gemm g, const Sched& S, const Epi& E, int wbase) {
;     ...
;             PG8_LDB(B0, 0, 0); PG8_LDB(B1, 0, 1); PG8_SCHED; PG8_LDA(At, 0, 0); PG8_STAGE(PG8_SA(1, 1), rAc, a1 + hstep, voffA);
;             PG8_WAIT_V(8); PG8_WAIT_L(0); PG8_BAR; PG8_MMA(0, 0, At, B0); PG8_MMA(0, 1, At, B1); PG8_BAR; PG8_SCHED;
;             PG8_LDA(At, 0, 1); PG8_STAGE(PG8_SB(0, 0), rB2, b2, voffB); PG8_STAGE(PG8_SB(0, 1), rB2, b2 + hstep, voffB); PG8_STAGE(PG8_SA(0, 0), rA2, a2, voffA);
;             PG8_WAIT_V(8); PG8_WAIT_L(0); PG8_BAR; PG8_MMA(1, 0, At, B0); PG8_MMA(1, 1, At, B1); PG8_BAR; PG8_SCHED;
;             PG8_LDB(B0, 1, 0); PG8_LDB(B1, 1, 1); PG8_SCHED; PG8_LDA(At, 1, 0); PG8_STAGE(PG8_SA(0, 1), rA2, a2 + hstep, voffA);
;             PG8_WAIT_V(8); PG8_WAIT_L(0); PG8_BAR; PG8_MMA(0, 0, At, B0); PG8_MMA(0, 1, At, B1); PG8_BAR; PG8_SCHED;
.LBB0_926:
	s_mov_b32 m0, s53
	s_nop 0
	buffer_load_dwordx4 v157, s[12:15], s55 offen lds
	v_add_u32_e32 v120, 0x10000, v160
	ds_read_b128 v[132:135], v120
	ds_read_b128 v[136:139], v120 offset:1024
	ds_read_b128 v[140:143], v120 offset:2048
	ds_read_b128 v[144:147], v120 offset:3072
	v_add_u32_e32 v120, 0x14000, v160
	ds_read_b128 v[162:165], v120
	ds_read_b128 v[166:169], v120 offset:1024
	ds_read_b128 v[170:173], v120 offset:2048
	ds_read_b128 v[174:177], v120 offset:3072
	s_add_i32 s14, s4, 0x80
	s_cmp_eq_u32 s60, s11
	s_cselect_b32 s66, s2, s14
	s_cselect_b32 s55, s3, s5
	s_or_b32 s54, s66, 0x80
	s_add_i32 s14, s30, s4
	s_mov_b32 m0, s61
	ds_read_b128 v[178:181], v161
	ds_read_b128 v[182:185], v161 offset:1024
	ds_read_b128 v[194:197], v161 offset:2048
	ds_read_b128 v[198:201], v161 offset:3072
	ds_read_b128 v[202:205], v161 offset:4096
	ds_read_b128 v[206:209], v161 offset:5120
	ds_read_b128 v[210:213], v161 offset:6144
	ds_read_b128 v[214:217], v161 offset:7168
	buffer_load_dwordx4 v222, s[36:39], s14 offen lds
	s_mov_b32 m0, s62
	s_nop 0
	buffer_load_dwordx4 v156, s[36:39], s14 offen lds
	s_waitcnt vmcnt(8)
	s_waitcnt lgkmcnt(0)
	s_barrier
	s_setprio 1
	v_mfma_f32_16x16x128_f8f6f4 v[124:127], v[140:147], v[178:185], v[124:127]
	v_mfma_f32_16x16x128_f8f6f4 v[108:111], v[132:139], v[194:201], v[108:111]
	v_mfma_f32_16x16x128_f8f6f4 v[104:107], v[140:147], v[194:201], v[104:107]
	v_mfma_f32_16x16x128_f8f6f4 v[120:123], v[132:139], v[178:185], v[128:131]
	v_mfma_f32_16x16x128_f8f6f4 v[148:151], v[132:139], v[202:209], v[92:95]
	v_mfma_f32_16x16x128_f8f6f4 v[186:189], v[140:147], v[202:209], v[88:91]
	v_mfma_f32_16x16x128_f8f6f4 v[218:221], v[132:139], v[210:217], v[76:79]
	v_mfma_f32_16x16x128_f8f6f4 v[226:229], v[140:147], v[210:217], v[72:75]
	v_mfma_f32_16x16x128_f8f6f4 v[116:119], v[162:169], v[178:185], v[116:119]
	v_mfma_f32_16x16x128_f8f6f4 v[112:115], v[170:177], v[178:185], v[112:115]
	v_mfma_f32_16x16x128_f8f6f4 v[100:103], v[162:169], v[194:201], v[100:103]
	v_mfma_f32_16x16x128_f8f6f4 v[96:99], v[170:177], v[194:201], v[96:99]
	v_mfma_f32_16x16x128_f8f6f4 v[178:181], v[162:169], v[202:209], v[84:87]
	v_mfma_f32_16x16x128_f8f6f4 v[182:185], v[170:177], v[202:209], v[80:83]
	v_mfma_f32_16x16x128_f8f6f4 v[194:197], v[162:169], v[210:217], v[68:71]
	v_mfma_f32_16x16x128_f8f6f4 v[198:201], v[170:177], v[210:217], v[64:67]
	s_setprio 0
	s_barrier
	s_mov_b32 m0, s33
	s_mov_b32 s14, s38
	s_mov_b32 s15, s39
	s_nop 1
	buffer_load_dwordx4 v223, s[12:15], s55 offen lds
	s_mov_b32 m0, s34
	ds_read_b128 v[64:67], v161 offset:16384
	s_add_i32 s67, s55, s30
	buffer_load_dwordx4 v157, s[12:15], s55 offen lds
	s_mov_b32 m0, s35
	ds_read_b128 v[68:71], v161 offset:17408
	buffer_load_dwordx4 v223, s[12:15], s67 offen lds
	s_mov_b32 m0, s31
	ds_read_b128 v[72:75], v161 offset:18432
	buffer_load_dwordx4 v222, s[36:39], s66 offen lds
	s_mov_b32 m0, s42
	ds_read_b128 v[76:79], v161 offset:19456
	buffer_load_dwordx4 v156, s[36:39], s66 offen lds
	ds_read_b128 v[80:83], v161 offset:20480
	ds_read_b128 v[84:87], v161 offset:21504
	ds_read_b128 v[88:91], v161 offset:22528
	ds_read_b128 v[92:95], v161 offset:23552
	s_waitcnt vmcnt(7)
	s_waitcnt lgkmcnt(0)
	s_barrier
	s_setprio 1
	v_mfma_f32_16x16x128_f8f6f4 v[60:63], v[132:139], v[64:71], v[60:63]
	v_mfma_f32_16x16x128_f8f6f4 v[56:59], v[140:147], v[64:71], v[56:59]
	v_mfma_f32_16x16x128_f8f6f4 v[202:205], v[132:139], v[72:79], v[44:47]
	v_mfma_f32_16x16x128_f8f6f4 v[206:209], v[140:147], v[72:79], v[40:43]
	v_mfma_f32_16x16x128_f8f6f4 v[210:213], v[132:139], v[80:87], v[28:31]
	v_mfma_f32_16x16x128_f8f6f4 v[214:217], v[140:147], v[80:87], v[24:27]
	v_mfma_f32_16x16x128_f8f6f4 v[230:233], v[132:139], v[88:95], v[12:15]
	v_mfma_f32_16x16x128_f8f6f4 v[234:237], v[140:147], v[88:95], v[8:11]
	v_mfma_f32_16x16x128_f8f6f4 v[52:55], v[162:169], v[64:71], v[52:55]
	v_mfma_f32_16x16x128_f8f6f4 v[48:51], v[170:177], v[64:71], v[48:51]
	v_mfma_f32_16x16x128_f8f6f4 v[238:241], v[162:169], v[72:79], v[36:39]
	v_mfma_f32_16x16x128_f8f6f4 v[242:245], v[170:177], v[72:79], v[32:35]
	v_mfma_f32_16x16x128_f8f6f4 v[246:249], v[162:169], v[80:87], v[20:23]
	v_mfma_f32_16x16x128_f8f6f4 v[250:253], v[170:177], v[80:87], v[16:19]
	v_mfma_f32_16x16x128_f8f6f4 v[190:193], v[162:169], v[88:95], v[4:7]
	v_mfma_f32_16x16x128_f8f6f4 v[152:155], v[170:177], v[88:95], v[0:3]
	s_setprio 0
	s_barrier
; #define PG8_STAGE(bufoff, rs_, soff_, voff) do { _Pragma("unroll") for (int _i = 0; _i < 2; ++_i) \
;         __builtin_amdgcn_raw_ptr_buffer_load_lds(rs_, (LAS void*)(lds + (bufoff) + ldsw + _i * 8192), 16, (int)(voff)[_i], (int)(soff_), 0, 0); } while (0)
; #define PG8_LDA(dst, b, h) do { _Pragma("unroll") for (int m = 0; m < 4; ++m) dst[m] = PG8_LD2(lds + PG8_SA(b, h) + aoff + m * 2048); } while (0)
; #define PG8_LDB(dst, b, h) do { _Pragma("unroll") for (int n = 0; n < 2; ++n) dst[n] = PG8_LD2(lds + PG8_SB(b, h) + boff + n * 2048); } while (0)
; #define PG8_WAIT_V(n) asm volatile("s_waitcnt vmcnt(" #n ")" ::: "memory")
; #define PG8_WAIT_L(n) asm volatile("s_waitcnt lgkmcnt(" #n ")" ::: "memory")
; #define PG8_BAR __builtin_amdgcn_s_barrier()
; #define PG8_SCHED __builtin_amdgcn_sched_barrier(0)
; template <class Epi, class Sched, bool ALIGN_EPI = false, bool SP2 = false, bool FP8 = false>
; __device__ __forceinline__ void gemm_phase(LAS unsigned char* lds, const Gemm g, const Sched& S, const Epi& E, int wbase) {
;     ...
;             PG8_LDA(At, 0, 1); PG8_STAGE(PG8_SB(0, 0), rB2, b2, voffB); PG8_STAGE(PG8_SB(0, 1), rB2, b2 + hstep, voffB); PG8_STAGE(PG8_SA(0, 0), rA2, a2, voffA);
;             PG8_WAIT_V(8); PG8_WAIT_L(0); PG8_BAR; PG8_MMA(1, 0, At, B0); PG8_MMA(1, 1, At, B1); PG8_BAR; PG8_SCHED;
;             PG8_LDB(B0, 1, 0); PG8_LDB(B1, 1, 1); PG8_SCHED; PG8_LDA(At, 1, 0); PG8_STAGE(PG8_SA(0, 1), rA2, a2 + hstep, voffA);
;             PG8_WAIT_V(8); PG8_WAIT_L(0); PG8_BAR; PG8_MMA(0, 0, At, B0); PG8_MMA(0, 1, At, B1); PG8_BAR; PG8_SCHED;
;             PG8_LDA(At, 1, 1); PG8_STAGE(PG8_SB(1, 0), rB2, b3, voffB); PG8_STAGE(PG8_SB(1, 1), rB2, b3 + hstep, voffB); PG8_STAGE(PG8_SA(1, 0), rA2, a3, voffA);
;             PG8_WAIT_V(8); PG8_WAIT_L(0); PG8_BAR; PG8_MMA(1, 0, At, B0); PG8_MMA(1, 1, At, B1); PG8_BAR; PG8_SCHED;
	s_mov_b32 m0, s41
	s_nop 0
	buffer_load_dwordx4 v157, s[12:15], s67 offen lds
	v_add_u32_e32 v8, 0x18000, v160
	s_nop 3
	ds_read_b128 v[0:3], v8
	ds_read_b128 v[4:7], v8 offset:1024
	ds_read_b128 v[16:19], v8 offset:2048
	ds_read_b128 v[20:23], v8 offset:3072
	v_add_u32_e32 v8, 0x1c000, v160
	ds_read_b128 v[132:135], v8
	ds_read_b128 v[136:139], v8 offset:1024
	ds_read_b128 v[140:143], v8 offset:2048
	ds_read_b128 v[144:147], v8 offset:3072
	s_add_i32 s66, s66, s30
	s_mov_b32 m0, s43
	ds_read_b128 v[8:11], v161 offset:32768
	ds_read_b128 v[12:15], v161 offset:33792
	ds_read_b128 v[24:27], v161 offset:34816
	ds_read_b128 v[28:31], v161 offset:35840
	ds_read_b128 v[32:35], v161 offset:36864
	ds_read_b128 v[36:39], v161 offset:37888
	ds_read_b128 v[40:43], v161 offset:38912
	ds_read_b128 v[44:47], v161 offset:39936
	buffer_load_dwordx4 v222, s[36:39], s66 offen lds
	s_mov_b32 m0, s44
	s_nop 0
	buffer_load_dwordx4 v156, s[36:39], s66 offen lds
	s_waitcnt vmcnt(8)
	s_waitcnt lgkmcnt(0)
	s_barrier
	s_setprio 1
	v_mfma_f32_16x16x128_f8f6f4 v[128:131], v[0:7], v[8:15], v[120:123]
	v_mfma_f32_16x16x128_f8f6f4 v[124:127], v[16:23], v[8:15], v[124:127]
	v_mfma_f32_16x16x128_f8f6f4 v[108:111], v[0:7], v[24:31], v[108:111]
	v_mfma_f32_16x16x128_f8f6f4 v[104:107], v[16:23], v[24:31], v[104:107]
	v_mfma_f32_16x16x128_f8f6f4 v[92:95], v[0:7], v[32:39], v[148:151]
	v_mfma_f32_16x16x128_f8f6f4 v[88:91], v[16:23], v[32:39], v[186:189]
	v_mfma_f32_16x16x128_f8f6f4 v[76:79], v[0:7], v[40:47], v[218:221]
	v_mfma_f32_16x16x128_f8f6f4 v[72:75], v[16:23], v[40:47], v[226:229]
	v_mfma_f32_16x16x128_f8f6f4 v[116:119], v[132:139], v[8:15], v[116:119]
	v_mfma_f32_16x16x128_f8f6f4 v[112:115], v[140:147], v[8:15], v[112:115]
	v_mfma_f32_16x16x128_f8f6f4 v[100:103], v[132:139], v[24:31], v[100:103]
	v_mfma_f32_16x16x128_f8f6f4 v[96:99], v[140:147], v[24:31], v[96:99]
	v_mfma_f32_16x16x128_f8f6f4 v[84:87], v[132:139], v[32:39], v[178:181]
	v_mfma_f32_16x16x128_f8f6f4 v[80:83], v[140:147], v[32:39], v[182:185]
	v_mfma_f32_16x16x128_f8f6f4 v[68:71], v[132:139], v[40:47], v[194:197]
	v_mfma_f32_16x16x128_f8f6f4 v[64:67], v[140:147], v[40:47], v[198:201]
	s_setprio 0
	s_barrier
	s_mov_b32 m0, s45
	s_bitset1_b32 s55, 7
	buffer_load_dwordx4 v223, s[12:15], s55 offen lds
	s_mov_b32 m0, s46
	ds_read_b128 v[32:35], v161 offset:49152
	buffer_load_dwordx4 v157, s[12:15], s55 offen lds
	s_add_i32 s55, s55, s30
	s_mov_b32 m0, s52
	ds_read_b128 v[36:39], v161 offset:50176
	buffer_load_dwordx4 v223, s[12:15], s55 offen lds
	s_mov_b32 m0, s47
	ds_read_b128 v[162:165], v161 offset:51200
	buffer_load_dwordx4 v222, s[36:39], s54 offen lds
	s_mov_b32 m0, s48
	ds_read_b128 v[166:169], v161 offset:52224
	buffer_load_dwordx4 v156, s[36:39], s54 offen lds
	ds_read_b128 v[170:173], v161 offset:53248
	ds_read_b128 v[174:177], v161 offset:54272
	ds_read_b128 v[178:181], v161 offset:55296
	ds_read_b128 v[182:185], v161 offset:56320
	s_waitcnt vmcnt(7)
	s_waitcnt lgkmcnt(0)
	s_barrier
	s_setprio 1
	v_mfma_f32_16x16x128_f8f6f4 v[60:63], v[0:7], v[32:39], v[60:63]
	v_mfma_f32_16x16x128_f8f6f4 v[56:59], v[16:23], v[32:39], v[56:59]
	v_mfma_f32_16x16x128_f8f6f4 v[44:47], v[0:7], v[162:169], v[202:205]
	v_mfma_f32_16x16x128_f8f6f4 v[40:43], v[16:23], v[162:169], v[206:209]
	v_mfma_f32_16x16x128_f8f6f4 v[28:31], v[0:7], v[170:177], v[210:213]
	v_mfma_f32_16x16x128_f8f6f4 v[24:27], v[16:23], v[170:177], v[214:217]
	v_mfma_f32_16x16x128_f8f6f4 v[12:15], v[0:7], v[178:185], v[230:233]
	v_mfma_f32_16x16x128_f8f6f4 v[8:11], v[16:23], v[178:185], v[234:237]
	v_mfma_f32_16x16x128_f8f6f4 v[52:55], v[132:139], v[32:39], v[52:55]
	v_mfma_f32_16x16x128_f8f6f4 v[48:51], v[140:147], v[32:39], v[48:51]
	v_mfma_f32_16x16x128_f8f6f4 v[36:39], v[132:139], v[162:169], v[238:241]
	v_mfma_f32_16x16x128_f8f6f4 v[32:35], v[140:147], v[162:169], v[242:245]
	v_mfma_f32_16x16x128_f8f6f4 v[20:23], v[132:139], v[170:177], v[246:249]
	v_mfma_f32_16x16x128_f8f6f4 v[16:19], v[140:147], v[170:177], v[250:253]
	v_mfma_f32_16x16x128_f8f6f4 v[4:7], v[132:139], v[178:185], v[190:193]
	v_mfma_f32_16x16x128_f8f6f4 v[0:3], v[140:147], v[178:185], v[152:155]
	s_setprio 0
	s_barrier
	s_add_i32 s11, s11, 2
	s_addk_i32 s4, 0x100
	s_addk_i32 s5, 0x100
	s_cmp_ge_i32 s11, s58
	s_cbranch_scc0 .LBB0_926
	s_mov_b32 m0, s53
	s_nop 0
	buffer_load_dwordx4 v157, s[12:15], s55 offen lds

; #define PG8_STAGE(bufoff, rs_, soff_, voff) do { _Pragma("unroll") for (int _i = 0; _i < 2; ++_i) \
;         __builtin_amdgcn_raw_ptr_buffer_load_lds(rs_, (LAS void*)(lds + (bufoff) + ldsw + _i * 8192), 16, (int)(voff)[_i], (int)(soff_), 0, 0); } while (0)
; #define PG8_LDA(dst, b, h) do { _Pragma("unroll") for (int m = 0; m < 4; ++m) dst[m] = PG8_LD2(lds + PG8_SA(b, h) + aoff + m * 2048); } while (0)
; #define PG8_LDB(dst, b, h) do { _Pragma("unroll") for (int n = 0; n < 2; ++n) dst[n] = PG8_LD2(lds + PG8_SB(b, h) + boff + n * 2048); } while (0)
; #define PG8_WAIT_V(n) asm volatile("s_waitcnt vmcnt(" #n ")" ::: "memory")
; #define PG8_WAIT_L(n) asm volatile("s_waitcnt lgkmcnt(" #n ")" ::: "memory")
; #define PG8_BAR __builtin_amdgcn_s_barrier()
; #define PG8_SCHED __builtin_amdgcn_sched_barrier(0)
; template <class Epi, class Sched, bool ALIGN_EPI = false, bool SP2 = false, bool FP8 = false>
; __device__ __forceinline__ void gemm_phase(LAS unsigned char* lds, const Gemm g, const Sched& S, const Epi& E, int wbase) {
;     ...
;             PG8_LDB(B0, 0, 0); PG8_LDB(B1, 0, 1); PG8_SCHED; PG8_LDA(At, 0, 0); PG8_STAGE(PG8_SA(1, 1), rAc, a1 + hstep, voffA);
;             PG8_WAIT_V(8); PG8_WAIT_L(0); PG8_BAR; PG8_MMA(0, 0, At, B0); PG8_MMA(0, 1, At, B1); PG8_BAR; PG8_SCHED;
;             PG8_LDA(At, 0, 1); PG8_STAGE(PG8_SB(0, 0), rB2, b2, voffB); PG8_STAGE(PG8_SB(0, 1), rB2, b2 + hstep, voffB); PG8_STAGE(PG8_SA(0, 0), rA2, a2, voffA);
;             PG8_WAIT_V(8); PG8_WAIT_L(0); PG8_BAR; PG8_MMA(1, 0, At, B0); PG8_MMA(1, 1, At, B1); PG8_BAR; PG8_SCHED;
;             PG8_LDB(B0, 1, 0); PG8_LDB(B1, 1, 1); PG8_SCHED; PG8_LDA(At, 1, 0); PG8_STAGE(PG8_SA(0, 1), rA2, a2 + hstep, voffA);
;             PG8_WAIT_V(8); PG8_WAIT_L(0); PG8_BAR; PG8_MMA(0, 0, At, B0); PG8_MMA(0, 1, At, B1); PG8_BAR; PG8_SCHED;
.LBB0_1004:
	s_mov_b32 m0, s57
	s_nop 0
	buffer_load_dwordx4 v177, s[12:15], s55 offen lds
	v_add_u32_e32 v132, 0x10000, v180
	v_add_u32_e32 v156, 0x14000, v180
	ds_read_b128 v[96:99], v132
	ds_read_b128 v[108:111], v132 offset:1024
	ds_read_b128 v[120:123], v132 offset:2048
	ds_read_b128 v[132:135], v132 offset:3072
	ds_read_b128 v[136:139], v156
	ds_read_b128 v[144:147], v156 offset:1024
	ds_read_b128 v[152:155], v156 offset:2048
	ds_read_b128 v[156:159], v156 offset:3072
	s_add_i32 s14, s4, 0x80
	s_cmp_eq_u32 s62, s11
	s_cselect_b32 s66, s2, s14
	s_cselect_b32 s55, s3, s5
	s_or_b32 s54, s66, 0x80
	s_add_i32 s14, s33, s4
	s_mov_b32 m0, s63
	ds_read_b128 v[160:163], v181
	ds_read_b128 v[164:167], v181 offset:1024
	ds_read_b128 v[168:171], v181 offset:2048
	ds_read_b128 v[182:185], v181 offset:3072
	ds_read_b128 v[186:189], v181 offset:4096
	ds_read_b128 v[190:193], v181 offset:5120
	ds_read_b128 v[194:197], v181 offset:6144
	ds_read_b128 v[198:201], v181 offset:7168
	buffer_load_dwordx4 v174, s[36:39], s14 offen lds
	s_mov_b32 m0, s65
	s_nop 0
	buffer_load_dwordx4 v176, s[36:39], s14 offen lds
	s_waitcnt vmcnt(8)
	s_waitcnt lgkmcnt(0)
	s_barrier
	s_setprio 1
	v_mfma_f32_16x16x32_bf16 v[148:151], v[96:99], v[160:163], v[148:151]
	v_mfma_f32_16x16x32_bf16 v[140:143], v[120:123], v[160:163], v[140:143]
	v_mfma_f32_16x16x32_bf16 v[116:119], v[96:99], v[168:171], v[116:119]
	v_mfma_f32_16x16x32_bf16 v[112:115], v[120:123], v[168:171], v[112:115]
	v_mfma_f32_16x16x32_bf16 v[92:95], v[96:99], v[186:189], v[92:95]
	v_mfma_f32_16x16x32_bf16 v[88:91], v[120:123], v[186:189], v[88:91]
	v_mfma_f32_16x16x32_bf16 v[76:79], v[96:99], v[194:197], v[76:79]
	v_mfma_f32_16x16x32_bf16 v[72:75], v[120:123], v[194:197], v[72:75]
	v_mfma_f32_16x16x32_bf16 v[148:151], v[108:111], v[164:167], v[148:151]
	v_mfma_f32_16x16x32_bf16 v[140:143], v[132:135], v[164:167], v[140:143]
	v_mfma_f32_16x16x32_bf16 v[116:119], v[108:111], v[182:185], v[116:119]
	v_mfma_f32_16x16x32_bf16 v[112:115], v[132:135], v[182:185], v[112:115]
	v_mfma_f32_16x16x32_bf16 v[92:95], v[108:111], v[190:193], v[92:95]
	v_mfma_f32_16x16x32_bf16 v[88:91], v[132:135], v[190:193], v[88:91]
	v_mfma_f32_16x16x32_bf16 v[76:79], v[108:111], v[198:201], v[76:79]
	v_mfma_f32_16x16x32_bf16 v[72:75], v[132:135], v[198:201], v[72:75]
	v_mfma_f32_16x16x32_bf16 v[128:131], v[136:139], v[160:163], v[128:131]
	v_mfma_f32_16x16x32_bf16 v[124:127], v[152:155], v[160:163], v[124:127]
	v_mfma_f32_16x16x32_bf16 v[104:107], v[136:139], v[168:171], v[104:107]
	v_mfma_f32_16x16x32_bf16 v[100:103], v[152:155], v[168:171], v[100:103]
	v_mfma_f32_16x16x32_bf16 v[84:87], v[136:139], v[186:189], v[84:87]
	v_mfma_f32_16x16x32_bf16 v[80:83], v[152:155], v[186:189], v[80:83]
	v_mfma_f32_16x16x32_bf16 v[68:71], v[136:139], v[194:197], v[68:71]
	v_mfma_f32_16x16x32_bf16 v[64:67], v[152:155], v[194:197], v[64:67]
	v_mfma_f32_16x16x32_bf16 v[128:131], v[144:147], v[164:167], v[128:131]
	v_mfma_f32_16x16x32_bf16 v[124:127], v[156:159], v[164:167], v[124:127]
	v_mfma_f32_16x16x32_bf16 v[104:107], v[144:147], v[182:185], v[104:107]
	v_mfma_f32_16x16x32_bf16 v[100:103], v[156:159], v[182:185], v[100:103]
	v_mfma_f32_16x16x32_bf16 v[84:87], v[144:147], v[190:193], v[84:87]
	v_mfma_f32_16x16x32_bf16 v[80:83], v[156:159], v[190:193], v[80:83]
	v_mfma_f32_16x16x32_bf16 v[68:71], v[144:147], v[198:201], v[68:71]
	v_mfma_f32_16x16x32_bf16 v[64:67], v[156:159], v[198:201], v[64:67]
	s_setprio 0
	s_barrier
	s_mov_b32 m0, s35
	s_mov_b32 s14, s38
	s_mov_b32 s15, s39
	buffer_load_dwordx4 v175, s[12:15], s55 offen lds
	s_mov_b32 m0, s41
	ds_read_b128 v[160:163], v181 offset:16384
	s_add_i32 s67, s55, s33
	buffer_load_dwordx4 v177, s[12:15], s55 offen lds
	s_mov_b32 m0, s42
	ds_read_b128 v[164:167], v181 offset:17408
	buffer_load_dwordx4 v175, s[12:15], s67 offen lds
	s_mov_b32 m0, s34
	ds_read_b128 v[168:171], v181 offset:18432
	buffer_load_dwordx4 v174, s[36:39], s66 offen lds
	s_mov_b32 m0, s44
	ds_read_b128 v[182:185], v181 offset:19456
	buffer_load_dwordx4 v176, s[36:39], s66 offen lds
	ds_read_b128 v[186:189], v181 offset:20480
	ds_read_b128 v[190:193], v181 offset:21504
	ds_read_b128 v[194:197], v181 offset:22528
	ds_read_b128 v[198:201], v181 offset:23552
	s_waitcnt vmcnt(7)
	s_waitcnt lgkmcnt(0)
	s_barrier
	s_setprio 1
	v_mfma_f32_16x16x32_bf16 v[60:63], v[96:99], v[160:163], v[60:63]
	v_mfma_f32_16x16x32_bf16 v[56:59], v[120:123], v[160:163], v[56:59]
	v_mfma_f32_16x16x32_bf16 v[44:47], v[96:99], v[168:171], v[44:47]
	v_mfma_f32_16x16x32_bf16 v[40:43], v[120:123], v[168:171], v[40:43]
	v_mfma_f32_16x16x32_bf16 v[28:31], v[96:99], v[186:189], v[28:31]
	v_mfma_f32_16x16x32_bf16 v[24:27], v[120:123], v[186:189], v[24:27]
	v_mfma_f32_16x16x32_bf16 v[12:15], v[96:99], v[194:197], v[12:15]
	v_mfma_f32_16x16x32_bf16 v[8:11], v[120:123], v[194:197], v[8:11]
	v_mfma_f32_16x16x32_bf16 v[60:63], v[108:111], v[164:167], v[60:63]
	v_mfma_f32_16x16x32_bf16 v[56:59], v[132:135], v[164:167], v[56:59]
	v_mfma_f32_16x16x32_bf16 v[44:47], v[108:111], v[182:185], v[44:47]
	v_mfma_f32_16x16x32_bf16 v[40:43], v[132:135], v[182:185], v[40:43]
	v_mfma_f32_16x16x32_bf16 v[28:31], v[108:111], v[190:193], v[28:31]
	v_mfma_f32_16x16x32_bf16 v[24:27], v[132:135], v[190:193], v[24:27]
	v_mfma_f32_16x16x32_bf16 v[12:15], v[108:111], v[198:201], v[12:15]
	v_mfma_f32_16x16x32_bf16 v[8:11], v[132:135], v[198:201], v[8:11]
	v_mfma_f32_16x16x32_bf16 v[52:55], v[136:139], v[160:163], v[52:55]
	v_mfma_f32_16x16x32_bf16 v[48:51], v[152:155], v[160:163], v[48:51]
	v_mfma_f32_16x16x32_bf16 v[36:39], v[136:139], v[168:171], v[36:39]
	v_mfma_f32_16x16x32_bf16 v[32:35], v[152:155], v[168:171], v[32:35]
	v_mfma_f32_16x16x32_bf16 v[20:23], v[136:139], v[186:189], v[20:23]
	v_mfma_f32_16x16x32_bf16 v[16:19], v[152:155], v[186:189], v[16:19]
	v_mfma_f32_16x16x32_bf16 v[4:7], v[136:139], v[194:197], v[4:7]
	v_mfma_f32_16x16x32_bf16 v[0:3], v[152:155], v[194:197], v[0:3]
	v_mfma_f32_16x16x32_bf16 v[52:55], v[144:147], v[164:167], v[52:55]
	v_mfma_f32_16x16x32_bf16 v[48:51], v[156:159], v[164:167], v[48:51]
	v_mfma_f32_16x16x32_bf16 v[36:39], v[144:147], v[182:185], v[36:39]
	v_mfma_f32_16x16x32_bf16 v[32:35], v[156:159], v[182:185], v[32:35]
	v_mfma_f32_16x16x32_bf16 v[20:23], v[144:147], v[190:193], v[20:23]
	v_mfma_f32_16x16x32_bf16 v[16:19], v[156:159], v[190:193], v[16:19]
	v_mfma_f32_16x16x32_bf16 v[4:7], v[144:147], v[198:201], v[4:7]
	v_mfma_f32_16x16x32_bf16 v[0:3], v[156:159], v[198:201], v[0:3]
	s_setprio 0
	s_barrier
; #define PG8_STAGE(bufoff, rs_, soff_, voff) do { _Pragma("unroll") for (int _i = 0; _i < 2; ++_i) \
;         __builtin_amdgcn_raw_ptr_buffer_load_lds(rs_, (LAS void*)(lds + (bufoff) + ldsw + _i * 8192), 16, (int)(voff)[_i], (int)(soff_), 0, 0); } while (0)
; #define PG8_LDA(dst, b, h) do { _Pragma("unroll") for (int m = 0; m < 4; ++m) dst[m] = PG8_LD2(lds + PG8_SA(b, h) + aoff + m * 2048); } while (0)
; #define PG8_LDB(dst, b, h) do { _Pragma("unroll") for (int n = 0; n < 2; ++n) dst[n] = PG8_LD2(lds + PG8_SB(b, h) + boff + n * 2048); } while (0)
; #define PG8_WAIT_V(n) asm volatile("s_waitcnt vmcnt(" #n ")" ::: "memory")
; #define PG8_WAIT_L(n) asm volatile("s_waitcnt lgkmcnt(" #n ")" ::: "memory")
; #define PG8_BAR __builtin_amdgcn_s_barrier()
; #define PG8_SCHED __builtin_amdgcn_sched_barrier(0)
; template <class Epi, class Sched, bool ALIGN_EPI = false, bool SP2 = false, bool FP8 = false>
; __device__ __forceinline__ void gemm_phase(LAS unsigned char* lds, const Gemm g, const Sched& S, const Epi& E, int wbase) {
;     ...
;         for (int t = 0; t < nt; t += 2) {
;             const bool last = (t == nt - 2);
;             const unsigned a1 = cA + (unsigned)(t + 1) * kstep;
;     ...
;             PG8_LDA(At, 0, 1); PG8_STAGE(PG8_SB(0, 0), rB2, b2, voffB); PG8_STAGE(PG8_SB(0, 1), rB2, b2 + hstep, voffB); PG8_STAGE(PG8_SA(0, 0), rA2, a2, voffA);
;             PG8_WAIT_V(8); PG8_WAIT_L(0); PG8_BAR; PG8_MMA(1, 0, At, B0); PG8_MMA(1, 1, At, B1); PG8_BAR; PG8_SCHED;
;             PG8_LDB(B0, 1, 0); PG8_LDB(B1, 1, 1); PG8_SCHED; PG8_LDA(At, 1, 0); PG8_STAGE(PG8_SA(0, 1), rA2, a2 + hstep, voffA);
;             PG8_WAIT_V(8); PG8_WAIT_L(0); PG8_BAR; PG8_MMA(0, 0, At, B0); PG8_MMA(0, 1, At, B1); PG8_BAR; PG8_SCHED;
;             PG8_LDA(At, 1, 1); PG8_STAGE(PG8_SB(1, 0), rB2, b3, voffB); PG8_STAGE(PG8_SB(1, 1), rB2, b3 + hstep, voffB); PG8_STAGE(PG8_SA(1, 0), rA2, a3, voffA);
;             PG8_WAIT_V(8); PG8_WAIT_L(0); PG8_BAR; PG8_MMA(1, 0, At, B0); PG8_MMA(1, 1, At, B1); PG8_BAR; PG8_SCHED;
	s_mov_b32 m0, s43
	s_nop 0
	buffer_load_dwordx4 v177, s[12:15], s67 offen lds
	v_add_u32_e32 v132, 0x18000, v180
	v_add_u32_e32 v156, 0x1c000, v180
	ds_read_b128 v[96:99], v132
	ds_read_b128 v[108:111], v132 offset:1024
	ds_read_b128 v[120:123], v132 offset:2048
	ds_read_b128 v[132:135], v132 offset:3072
	ds_read_b128 v[136:139], v156
	ds_read_b128 v[144:147], v156 offset:1024
	ds_read_b128 v[152:155], v156 offset:2048
	ds_read_b128 v[156:159], v156 offset:3072
	s_add_i32 s66, s66, s33
	s_mov_b32 m0, s45
	ds_read_b128 v[160:163], v181 offset:32768
	ds_read_b128 v[164:167], v181 offset:33792
	ds_read_b128 v[168:171], v181 offset:34816
	ds_read_b128 v[182:185], v181 offset:35840
	ds_read_b128 v[186:189], v181 offset:36864
	ds_read_b128 v[190:193], v181 offset:37888
	ds_read_b128 v[194:197], v181 offset:38912
	ds_read_b128 v[198:201], v181 offset:39936
	buffer_load_dwordx4 v174, s[36:39], s66 offen lds
	s_mov_b32 m0, s46
	s_nop 0
	buffer_load_dwordx4 v176, s[36:39], s66 offen lds
	s_waitcnt vmcnt(8)
	s_waitcnt lgkmcnt(0)
	s_barrier
	s_setprio 1
	v_mfma_f32_16x16x32_bf16 v[148:151], v[96:99], v[160:163], v[148:151]
	v_mfma_f32_16x16x32_bf16 v[140:143], v[120:123], v[160:163], v[140:143]
	v_mfma_f32_16x16x32_bf16 v[116:119], v[96:99], v[168:171], v[116:119]
	v_mfma_f32_16x16x32_bf16 v[112:115], v[120:123], v[168:171], v[112:115]
	v_mfma_f32_16x16x32_bf16 v[92:95], v[96:99], v[186:189], v[92:95]
	v_mfma_f32_16x16x32_bf16 v[88:91], v[120:123], v[186:189], v[88:91]
	v_mfma_f32_16x16x32_bf16 v[76:79], v[96:99], v[194:197], v[76:79]
	v_mfma_f32_16x16x32_bf16 v[72:75], v[120:123], v[194:197], v[72:75]
	v_mfma_f32_16x16x32_bf16 v[148:151], v[108:111], v[164:167], v[148:151]
	v_mfma_f32_16x16x32_bf16 v[140:143], v[132:135], v[164:167], v[140:143]
	v_mfma_f32_16x16x32_bf16 v[116:119], v[108:111], v[182:185], v[116:119]
	v_mfma_f32_16x16x32_bf16 v[112:115], v[132:135], v[182:185], v[112:115]
	v_mfma_f32_16x16x32_bf16 v[92:95], v[108:111], v[190:193], v[92:95]
	v_mfma_f32_16x16x32_bf16 v[88:91], v[132:135], v[190:193], v[88:91]
	v_mfma_f32_16x16x32_bf16 v[76:79], v[108:111], v[198:201], v[76:79]
	v_mfma_f32_16x16x32_bf16 v[72:75], v[132:135], v[198:201], v[72:75]
	v_mfma_f32_16x16x32_bf16 v[128:131], v[136:139], v[160:163], v[128:131]
	v_mfma_f32_16x16x32_bf16 v[124:127], v[152:155], v[160:163], v[124:127]
	v_mfma_f32_16x16x32_bf16 v[104:107], v[136:139], v[168:171], v[104:107]
	v_mfma_f32_16x16x32_bf16 v[100:103], v[152:155], v[168:171], v[100:103]
	v_mfma_f32_16x16x32_bf16 v[84:87], v[136:139], v[186:189], v[84:87]
	v_mfma_f32_16x16x32_bf16 v[80:83], v[152:155], v[186:189], v[80:83]
	v_mfma_f32_16x16x32_bf16 v[68:71], v[136:139], v[194:197], v[68:71]
	v_mfma_f32_16x16x32_bf16 v[64:67], v[152:155], v[194:197], v[64:67]
	v_mfma_f32_16x16x32_bf16 v[128:131], v[144:147], v[164:167], v[128:131]
	v_mfma_f32_16x16x32_bf16 v[124:127], v[156:159], v[164:167], v[124:127]
	v_mfma_f32_16x16x32_bf16 v[104:107], v[144:147], v[182:185], v[104:107]
	v_mfma_f32_16x16x32_bf16 v[100:103], v[156:159], v[182:185], v[100:103]
	v_mfma_f32_16x16x32_bf16 v[84:87], v[144:147], v[190:193], v[84:87]
	v_mfma_f32_16x16x32_bf16 v[80:83], v[156:159], v[190:193], v[80:83]
	v_mfma_f32_16x16x32_bf16 v[68:71], v[144:147], v[198:201], v[68:71]
	v_mfma_f32_16x16x32_bf16 v[64:67], v[156:159], v[198:201], v[64:67]
	s_setprio 0
	s_barrier
	s_mov_b32 m0, s47
	s_bitset1_b32 s55, 7
	buffer_load_dwordx4 v175, s[12:15], s55 offen lds
	s_mov_b32 m0, s48
	ds_read_b128 v[160:163], v181 offset:49152
	buffer_load_dwordx4 v177, s[12:15], s55 offen lds
	s_add_i32 s55, s55, s33
	s_mov_b32 m0, s56
	ds_read_b128 v[164:167], v181 offset:50176
	buffer_load_dwordx4 v175, s[12:15], s55 offen lds
	s_mov_b32 m0, s52
	ds_read_b128 v[168:171], v181 offset:51200
	buffer_load_dwordx4 v174, s[36:39], s54 offen lds
	s_mov_b32 m0, s53
	ds_read_b128 v[182:185], v181 offset:52224
	buffer_load_dwordx4 v176, s[36:39], s54 offen lds
	ds_read_b128 v[186:189], v181 offset:53248
	ds_read_b128 v[190:193], v181 offset:54272
	ds_read_b128 v[194:197], v181 offset:55296
	ds_read_b128 v[198:201], v181 offset:56320
	s_waitcnt vmcnt(7)
	s_waitcnt lgkmcnt(0)
	s_barrier
	s_setprio 1
	v_mfma_f32_16x16x32_bf16 v[60:63], v[96:99], v[160:163], v[60:63]
	v_mfma_f32_16x16x32_bf16 v[56:59], v[120:123], v[160:163], v[56:59]
	v_mfma_f32_16x16x32_bf16 v[44:47], v[96:99], v[168:171], v[44:47]
	v_mfma_f32_16x16x32_bf16 v[40:43], v[120:123], v[168:171], v[40:43]
	v_mfma_f32_16x16x32_bf16 v[28:31], v[96:99], v[186:189], v[28:31]
	v_mfma_f32_16x16x32_bf16 v[24:27], v[120:123], v[186:189], v[24:27]
	v_mfma_f32_16x16x32_bf16 v[12:15], v[96:99], v[194:197], v[12:15]
	v_mfma_f32_16x16x32_bf16 v[8:11], v[120:123], v[194:197], v[8:11]
	v_mfma_f32_16x16x32_bf16 v[60:63], v[108:111], v[164:167], v[60:63]
	v_mfma_f32_16x16x32_bf16 v[56:59], v[132:135], v[164:167], v[56:59]
	v_mfma_f32_16x16x32_bf16 v[44:47], v[108:111], v[182:185], v[44:47]
	v_mfma_f32_16x16x32_bf16 v[40:43], v[132:135], v[182:185], v[40:43]
	v_mfma_f32_16x16x32_bf16 v[28:31], v[108:111], v[190:193], v[28:31]
	v_mfma_f32_16x16x32_bf16 v[24:27], v[132:135], v[190:193], v[24:27]
	v_mfma_f32_16x16x32_bf16 v[12:15], v[108:111], v[198:201], v[12:15]
	v_mfma_f32_16x16x32_bf16 v[8:11], v[132:135], v[198:201], v[8:11]
	v_mfma_f32_16x16x32_bf16 v[52:55], v[136:139], v[160:163], v[52:55]
	v_mfma_f32_16x16x32_bf16 v[48:51], v[152:155], v[160:163], v[48:51]
	v_mfma_f32_16x16x32_bf16 v[36:39], v[136:139], v[168:171], v[36:39]
	v_mfma_f32_16x16x32_bf16 v[32:35], v[152:155], v[168:171], v[32:35]
	v_mfma_f32_16x16x32_bf16 v[20:23], v[136:139], v[186:189], v[20:23]
	v_mfma_f32_16x16x32_bf16 v[16:19], v[152:155], v[186:189], v[16:19]
	v_mfma_f32_16x16x32_bf16 v[4:7], v[136:139], v[194:197], v[4:7]
	v_mfma_f32_16x16x32_bf16 v[0:3], v[152:155], v[194:197], v[0:3]
	v_mfma_f32_16x16x32_bf16 v[52:55], v[144:147], v[164:167], v[52:55]
	v_mfma_f32_16x16x32_bf16 v[48:51], v[156:159], v[164:167], v[48:51]
	v_mfma_f32_16x16x32_bf16 v[36:39], v[144:147], v[182:185], v[36:39]
	v_mfma_f32_16x16x32_bf16 v[32:35], v[156:159], v[182:185], v[32:35]
	v_mfma_f32_16x16x32_bf16 v[20:23], v[144:147], v[190:193], v[20:23]
	v_mfma_f32_16x16x32_bf16 v[16:19], v[156:159], v[190:193], v[16:19]
	v_mfma_f32_16x16x32_bf16 v[4:7], v[144:147], v[198:201], v[4:7]
	v_mfma_f32_16x16x32_bf16 v[0:3], v[156:159], v[198:201], v[0:3]
	s_setprio 0
	s_barrier
	s_add_i32 s11, s11, 2
	s_addk_i32 s4, 0x100
	s_addk_i32 s5, 0x100
	s_cmp_ge_i32 s11, s60
	s_cbranch_scc0 .LBB0_1004
	s_mov_b32 m0, s57
	s_nop 0
	buffer_load_dwordx4 v177, s[12:15], s55 offen lds

; #define PG8_STAGE(bufoff, rs_, soff_, voff) do { _Pragma("unroll") for (int _i = 0; _i < 2; ++_i) \
;         __builtin_amdgcn_raw_ptr_buffer_load_lds(rs_, (LAS void*)(lds + (bufoff) + ldsw + _i * 8192), 16, (int)(voff)[_i], (int)(soff_), 0, 0); } while (0)
; #define PG8_LDA(dst, b, h) do { _Pragma("unroll") for (int m = 0; m < 4; ++m) dst[m] = PG8_LD2(lds + PG8_SA(b, h) + aoff + m * 2048); } while (0)
; #define PG8_LDB(dst, b, h) do { _Pragma("unroll") for (int n = 0; n < 2; ++n) dst[n] = PG8_LD2(lds + PG8_SB(b, h) + boff + n * 2048); } while (0)
; #define PG8_WAIT_V(n) asm volatile("s_waitcnt vmcnt(" #n ")" ::: "memory")
; #define PG8_WAIT_L(n) asm volatile("s_waitcnt lgkmcnt(" #n ")" ::: "memory")
; #define PG8_BAR __builtin_amdgcn_s_barrier()
; #define PG8_SCHED __builtin_amdgcn_sched_barrier(0)
; template <class Epi, class Sched, bool ALIGN_EPI = false, bool SP2 = false, bool FP8 = false>
; __device__ __forceinline__ void gemm_phase(LAS unsigned char* lds, const Gemm g, const Sched& S, const Epi& E, int wbase) {
;     ...
;             PG8_LDB(B0, 0, 0); PG8_LDB(B1, 0, 1); PG8_SCHED; PG8_LDA(At, 0, 0); PG8_STAGE(PG8_SA(1, 1), rAc, a1 + hstep, voffA);
;             PG8_WAIT_V(8); PG8_WAIT_L(0); PG8_BAR; PG8_MMA(0, 0, At, B0); PG8_MMA(0, 1, At, B1); PG8_BAR; PG8_SCHED;
;             PG8_LDA(At, 0, 1); PG8_STAGE(PG8_SB(0, 0), rB2, b2, voffB); PG8_STAGE(PG8_SB(0, 1), rB2, b2 + hstep, voffB); PG8_STAGE(PG8_SA(0, 0), rA2, a2, voffA);
;             PG8_WAIT_V(8); PG8_WAIT_L(0); PG8_BAR; PG8_MMA(1, 0, At, B0); PG8_MMA(1, 1, At, B1); PG8_BAR; PG8_SCHED;
;             PG8_LDB(B0, 1, 0); PG8_LDB(B1, 1, 1); PG8_SCHED; PG8_LDA(At, 1, 0); PG8_STAGE(PG8_SA(0, 1), rA2, a2 + hstep, voffA);
;             PG8_WAIT_V(8); PG8_WAIT_L(0); PG8_BAR; PG8_MMA(0, 0, At, B0); PG8_MMA(0, 1, At, B1); PG8_BAR; PG8_SCHED;
.LBB0_1628:
	s_mov_b32 m0, s42
	s_nop 0
	buffer_load_dwordx4 v149, s[4:7], s55 offen lds
	v_add_u32_e32 v136, 0x10000, v161
	ds_read_b128 v[128:131], v136
	ds_read_b128 v[132:135], v136 offset:1024
	ds_read_b128 v[164:167], v136 offset:2048
	ds_read_b128 v[168:171], v136 offset:3072
	v_add_u32_e32 v136, 0x14000, v161
	ds_read_b128 v[172:175], v136
	ds_read_b128 v[176:179], v136 offset:1024
	ds_read_b128 v[180:183], v136 offset:2048
	ds_read_b128 v[184:187], v136 offset:3072
	s_add_i32 s6, s61, 0x80
	s_cmp_eq_u32 s46, s63
	s_cselect_b32 s65, s59, s6
	s_cselect_b32 s55, s60, s62
	s_or_b32 s54, s65, 0x80
	s_add_i32 s6, s22, s61
	s_mov_b32 m0, s47
	ds_read_b128 v[188:191], v162
	ds_read_b128 v[192:195], v162 offset:1024
	ds_read_b128 v[196:199], v162 offset:2048
	ds_read_b128 v[200:203], v162 offset:3072
	ds_read_b128 v[204:207], v162 offset:4096
	ds_read_b128 v[208:211], v162 offset:5120
	ds_read_b128 v[212:215], v162 offset:6144
	ds_read_b128 v[216:219], v162 offset:7168
	buffer_load_dwordx4 v137, s[36:39], s6 offen lds
	s_mov_b32 m0, s48
	s_nop 0
	buffer_load_dwordx4 v145, s[36:39], s6 offen lds
	s_waitcnt vmcnt(8)
	s_waitcnt lgkmcnt(0)
	s_barrier
	s_setprio 1
	v_mfma_f32_16x16x32_bf16 v[120:123], v[128:131], v[188:191], v[120:123]
	v_mfma_f32_16x16x32_bf16 v[124:127], v[164:167], v[188:191], v[124:127]
	v_mfma_f32_16x16x32_bf16 v[104:107], v[128:131], v[196:199], v[104:107]
	v_mfma_f32_16x16x32_bf16 v[108:111], v[164:167], v[196:199], v[108:111]
	v_mfma_f32_16x16x32_bf16 v[88:91], v[128:131], v[204:207], v[88:91]
	v_mfma_f32_16x16x32_bf16 v[92:95], v[164:167], v[204:207], v[92:95]
	v_mfma_f32_16x16x32_bf16 v[72:75], v[128:131], v[212:215], v[72:75]
	v_mfma_f32_16x16x32_bf16 v[76:79], v[164:167], v[212:215], v[76:79]
	v_mfma_f32_16x16x32_bf16 v[120:123], v[132:135], v[192:195], v[120:123]
	v_mfma_f32_16x16x32_bf16 v[124:127], v[168:171], v[192:195], v[124:127]
	v_mfma_f32_16x16x32_bf16 v[104:107], v[132:135], v[200:203], v[104:107]
	v_mfma_f32_16x16x32_bf16 v[108:111], v[168:171], v[200:203], v[108:111]
	v_mfma_f32_16x16x32_bf16 v[88:91], v[132:135], v[208:211], v[88:91]
	v_mfma_f32_16x16x32_bf16 v[92:95], v[168:171], v[208:211], v[92:95]
	v_mfma_f32_16x16x32_bf16 v[72:75], v[132:135], v[216:219], v[72:75]
	v_mfma_f32_16x16x32_bf16 v[76:79], v[168:171], v[216:219], v[76:79]
	v_mfma_f32_16x16x32_bf16 v[112:115], v[172:175], v[188:191], v[112:115]
	v_mfma_f32_16x16x32_bf16 v[116:119], v[180:183], v[188:191], v[116:119]
	v_mfma_f32_16x16x32_bf16 v[96:99], v[172:175], v[196:199], v[96:99]
	v_mfma_f32_16x16x32_bf16 v[100:103], v[180:183], v[196:199], v[100:103]
	v_mfma_f32_16x16x32_bf16 v[80:83], v[172:175], v[204:207], v[80:83]
	v_mfma_f32_16x16x32_bf16 v[84:87], v[180:183], v[204:207], v[84:87]
	v_mfma_f32_16x16x32_bf16 v[64:67], v[172:175], v[212:215], v[64:67]
	v_mfma_f32_16x16x32_bf16 v[68:71], v[180:183], v[212:215], v[68:71]
	v_mfma_f32_16x16x32_bf16 v[112:115], v[176:179], v[192:195], v[112:115]
	v_mfma_f32_16x16x32_bf16 v[116:119], v[184:187], v[192:195], v[116:119]
	v_mfma_f32_16x16x32_bf16 v[96:99], v[176:179], v[200:203], v[96:99]
	v_mfma_f32_16x16x32_bf16 v[100:103], v[184:187], v[200:203], v[100:103]
	v_mfma_f32_16x16x32_bf16 v[80:83], v[176:179], v[208:211], v[80:83]
	v_mfma_f32_16x16x32_bf16 v[84:87], v[184:187], v[208:211], v[84:87]
	v_mfma_f32_16x16x32_bf16 v[64:67], v[176:179], v[216:219], v[64:67]
	v_mfma_f32_16x16x32_bf16 v[68:71], v[184:187], v[216:219], v[68:71]
	s_setprio 0
	s_barrier
	s_mov_b32 m0, s24
	s_mov_b32 s6, s38
	s_mov_b32 s7, s39
	buffer_load_dwordx4 v141, s[4:7], s55 offen lds
	s_mov_b32 m0, s25
	ds_read_b128 v[188:191], v162 offset:16384
	s_add_i32 s66, s55, s22
	buffer_load_dwordx4 v149, s[4:7], s55 offen lds
	s_mov_b32 m0, s26
	ds_read_b128 v[192:195], v162 offset:17408
	buffer_load_dwordx4 v141, s[4:7], s66 offen lds
	s_mov_b32 m0, s23
	ds_read_b128 v[196:199], v162 offset:18432
	buffer_load_dwordx4 v137, s[36:39], s65 offen lds
	s_mov_b32 m0, s28
	ds_read_b128 v[200:203], v162 offset:19456
	buffer_load_dwordx4 v145, s[36:39], s65 offen lds
	ds_read_b128 v[204:207], v162 offset:20480
	ds_read_b128 v[208:211], v162 offset:21504
	ds_read_b128 v[212:215], v162 offset:22528
	ds_read_b128 v[216:219], v162 offset:23552
	s_waitcnt vmcnt(7)
	s_waitcnt lgkmcnt(0)
	s_barrier
	s_setprio 1
	v_mfma_f32_16x16x32_bf16 v[56:59], v[128:131], v[188:191], v[56:59]
	v_mfma_f32_16x16x32_bf16 v[60:63], v[164:167], v[188:191], v[60:63]
	v_mfma_f32_16x16x32_bf16 v[40:43], v[128:131], v[196:199], v[40:43]
	v_mfma_f32_16x16x32_bf16 v[44:47], v[164:167], v[196:199], v[44:47]
	v_mfma_f32_16x16x32_bf16 v[24:27], v[128:131], v[204:207], v[24:27]
	v_mfma_f32_16x16x32_bf16 v[28:31], v[164:167], v[204:207], v[28:31]
	v_mfma_f32_16x16x32_bf16 v[8:11], v[128:131], v[212:215], v[8:11]
	v_mfma_f32_16x16x32_bf16 v[12:15], v[164:167], v[212:215], v[12:15]
	v_mfma_f32_16x16x32_bf16 v[56:59], v[132:135], v[192:195], v[56:59]
	v_mfma_f32_16x16x32_bf16 v[60:63], v[168:171], v[192:195], v[60:63]
	v_mfma_f32_16x16x32_bf16 v[40:43], v[132:135], v[200:203], v[40:43]
	v_mfma_f32_16x16x32_bf16 v[44:47], v[168:171], v[200:203], v[44:47]
	v_mfma_f32_16x16x32_bf16 v[24:27], v[132:135], v[208:211], v[24:27]
	v_mfma_f32_16x16x32_bf16 v[28:31], v[168:171], v[208:211], v[28:31]
	v_mfma_f32_16x16x32_bf16 v[8:11], v[132:135], v[216:219], v[8:11]
	v_mfma_f32_16x16x32_bf16 v[12:15], v[168:171], v[216:219], v[12:15]
	v_mfma_f32_16x16x32_bf16 v[48:51], v[172:175], v[188:191], v[48:51]
	v_mfma_f32_16x16x32_bf16 v[52:55], v[180:183], v[188:191], v[52:55]
	v_mfma_f32_16x16x32_bf16 v[32:35], v[172:175], v[196:199], v[32:35]
	v_mfma_f32_16x16x32_bf16 v[36:39], v[180:183], v[196:199], v[36:39]
	v_mfma_f32_16x16x32_bf16 v[16:19], v[172:175], v[204:207], v[16:19]
	v_mfma_f32_16x16x32_bf16 v[20:23], v[180:183], v[204:207], v[20:23]
	v_mfma_f32_16x16x32_bf16 v[4:7], v[172:175], v[212:215], v[4:7]
	v_mfma_f32_16x16x32_bf16 v[0:3], v[180:183], v[212:215], v[0:3]
	v_mfma_f32_16x16x32_bf16 v[48:51], v[176:179], v[192:195], v[48:51]
	v_mfma_f32_16x16x32_bf16 v[52:55], v[184:187], v[192:195], v[52:55]
	v_mfma_f32_16x16x32_bf16 v[32:35], v[176:179], v[200:203], v[32:35]
	v_mfma_f32_16x16x32_bf16 v[36:39], v[184:187], v[200:203], v[36:39]
	v_mfma_f32_16x16x32_bf16 v[16:19], v[176:179], v[208:211], v[16:19]
	v_mfma_f32_16x16x32_bf16 v[20:23], v[184:187], v[208:211], v[20:23]
	v_mfma_f32_16x16x32_bf16 v[4:7], v[176:179], v[216:219], v[4:7]
	v_mfma_f32_16x16x32_bf16 v[0:3], v[184:187], v[216:219], v[0:3]
	s_setprio 0
	s_barrier
; #define PG8_STAGE(bufoff, rs_, soff_, voff) do { _Pragma("unroll") for (int _i = 0; _i < 2; ++_i) \
;         __builtin_amdgcn_raw_ptr_buffer_load_lds(rs_, (LAS void*)(lds + (bufoff) + ldsw + _i * 8192), 16, (int)(voff)[_i], (int)(soff_), 0, 0); } while (0)
; #define PG8_LDA(dst, b, h) do { _Pragma("unroll") for (int m = 0; m < 4; ++m) dst[m] = PG8_LD2(lds + PG8_SA(b, h) + aoff + m * 2048); } while (0)
; #define PG8_LDB(dst, b, h) do { _Pragma("unroll") for (int n = 0; n < 2; ++n) dst[n] = PG8_LD2(lds + PG8_SB(b, h) + boff + n * 2048); } while (0)
; #define PG8_WAIT_V(n) asm volatile("s_waitcnt vmcnt(" #n ")" ::: "memory")
; #define PG8_WAIT_L(n) asm volatile("s_waitcnt lgkmcnt(" #n ")" ::: "memory")
; #define PG8_BAR __builtin_amdgcn_s_barrier()
; #define PG8_SCHED __builtin_amdgcn_sched_barrier(0)
; template <class Epi, class Sched, bool ALIGN_EPI = false, bool SP2 = false, bool FP8 = false>
; __device__ __forceinline__ void gemm_phase(LAS unsigned char* lds, const Gemm g, const Sched& S, const Epi& E, int wbase) {
;     ...
;         for (int t = 0; t < nt; t += 2) {
;             const bool last = (t == nt - 2);
;             const unsigned a1 = cA + (unsigned)(t + 1) * kstep;
;     ...
;             PG8_LDA(At, 0, 1); PG8_STAGE(PG8_SB(0, 0), rB2, b2, voffB); PG8_STAGE(PG8_SB(0, 1), rB2, b2 + hstep, voffB); PG8_STAGE(PG8_SA(0, 0), rA2, a2, voffA);
;             PG8_WAIT_V(8); PG8_WAIT_L(0); PG8_BAR; PG8_MMA(1, 0, At, B0); PG8_MMA(1, 1, At, B1); PG8_BAR; PG8_SCHED;
;             PG8_LDB(B0, 1, 0); PG8_LDB(B1, 1, 1); PG8_SCHED; PG8_LDA(At, 1, 0); PG8_STAGE(PG8_SA(0, 1), rA2, a2 + hstep, voffA);
;             PG8_WAIT_V(8); PG8_WAIT_L(0); PG8_BAR; PG8_MMA(0, 0, At, B0); PG8_MMA(0, 1, At, B1); PG8_BAR; PG8_SCHED;
;             PG8_LDA(At, 1, 1); PG8_STAGE(PG8_SB(1, 0), rB2, b3, voffB); PG8_STAGE(PG8_SB(1, 1), rB2, b3 + hstep, voffB); PG8_STAGE(PG8_SA(1, 0), rA2, a3, voffA);
;             PG8_WAIT_V(8); PG8_WAIT_L(0); PG8_BAR; PG8_MMA(1, 0, At, B0); PG8_MMA(1, 1, At, B1); PG8_BAR; PG8_SCHED;
	s_mov_b32 m0, s27
	s_nop 0
	buffer_load_dwordx4 v149, s[4:7], s66 offen lds
	v_add_u32_e32 v136, 0x18000, v161
	ds_read_b128 v[128:131], v136
	ds_read_b128 v[132:135], v136 offset:1024
	ds_read_b128 v[164:167], v136 offset:2048
	ds_read_b128 v[168:171], v136 offset:3072
	v_add_u32_e32 v136, 0x1c000, v161
	ds_read_b128 v[172:175], v136
	ds_read_b128 v[176:179], v136 offset:1024
	ds_read_b128 v[180:183], v136 offset:2048
	ds_read_b128 v[184:187], v136 offset:3072
	s_add_i32 s65, s65, s22
	s_mov_b32 m0, s29
	ds_read_b128 v[188:191], v162 offset:32768
	ds_read_b128 v[192:195], v162 offset:33792
	ds_read_b128 v[196:199], v162 offset:34816
	ds_read_b128 v[200:203], v162 offset:35840
	ds_read_b128 v[204:207], v162 offset:36864
	ds_read_b128 v[208:211], v162 offset:37888
	ds_read_b128 v[212:215], v162 offset:38912
	ds_read_b128 v[216:219], v162 offset:39936
	buffer_load_dwordx4 v137, s[36:39], s65 offen lds
	s_mov_b32 m0, s30
	s_nop 0
	buffer_load_dwordx4 v145, s[36:39], s65 offen lds
	s_waitcnt vmcnt(8)
	s_waitcnt lgkmcnt(0)
	s_barrier
	s_setprio 1
	v_mfma_f32_16x16x32_bf16 v[120:123], v[128:131], v[188:191], v[120:123]
	v_mfma_f32_16x16x32_bf16 v[124:127], v[164:167], v[188:191], v[124:127]
	v_mfma_f32_16x16x32_bf16 v[104:107], v[128:131], v[196:199], v[104:107]
	v_mfma_f32_16x16x32_bf16 v[108:111], v[164:167], v[196:199], v[108:111]
	v_mfma_f32_16x16x32_bf16 v[88:91], v[128:131], v[204:207], v[88:91]
	v_mfma_f32_16x16x32_bf16 v[92:95], v[164:167], v[204:207], v[92:95]
	v_mfma_f32_16x16x32_bf16 v[72:75], v[128:131], v[212:215], v[72:75]
	v_mfma_f32_16x16x32_bf16 v[76:79], v[164:167], v[212:215], v[76:79]
	v_mfma_f32_16x16x32_bf16 v[120:123], v[132:135], v[192:195], v[120:123]
	v_mfma_f32_16x16x32_bf16 v[124:127], v[168:171], v[192:195], v[124:127]
	v_mfma_f32_16x16x32_bf16 v[104:107], v[132:135], v[200:203], v[104:107]
	v_mfma_f32_16x16x32_bf16 v[108:111], v[168:171], v[200:203], v[108:111]
	v_mfma_f32_16x16x32_bf16 v[88:91], v[132:135], v[208:211], v[88:91]
	v_mfma_f32_16x16x32_bf16 v[92:95], v[168:171], v[208:211], v[92:95]
	v_mfma_f32_16x16x32_bf16 v[72:75], v[132:135], v[216:219], v[72:75]
	v_mfma_f32_16x16x32_bf16 v[76:79], v[168:171], v[216:219], v[76:79]
	v_mfma_f32_16x16x32_bf16 v[112:115], v[172:175], v[188:191], v[112:115]
	v_mfma_f32_16x16x32_bf16 v[116:119], v[180:183], v[188:191], v[116:119]
	v_mfma_f32_16x16x32_bf16 v[96:99], v[172:175], v[196:199], v[96:99]
	v_mfma_f32_16x16x32_bf16 v[100:103], v[180:183], v[196:199], v[100:103]
	v_mfma_f32_16x16x32_bf16 v[80:83], v[172:175], v[204:207], v[80:83]
	v_mfma_f32_16x16x32_bf16 v[84:87], v[180:183], v[204:207], v[84:87]
	v_mfma_f32_16x16x32_bf16 v[64:67], v[172:175], v[212:215], v[64:67]
	v_mfma_f32_16x16x32_bf16 v[68:71], v[180:183], v[212:215], v[68:71]
	v_mfma_f32_16x16x32_bf16 v[112:115], v[176:179], v[192:195], v[112:115]
	v_mfma_f32_16x16x32_bf16 v[116:119], v[184:187], v[192:195], v[116:119]
	v_mfma_f32_16x16x32_bf16 v[96:99], v[176:179], v[200:203], v[96:99]
	v_mfma_f32_16x16x32_bf16 v[100:103], v[184:187], v[200:203], v[100:103]
	v_mfma_f32_16x16x32_bf16 v[80:83], v[176:179], v[208:211], v[80:83]
	v_mfma_f32_16x16x32_bf16 v[84:87], v[184:187], v[208:211], v[84:87]
	v_mfma_f32_16x16x32_bf16 v[64:67], v[176:179], v[216:219], v[64:67]
	v_mfma_f32_16x16x32_bf16 v[68:71], v[184:187], v[216:219], v[68:71]
	s_setprio 0
	s_barrier
	s_mov_b32 m0, s31
	s_bitset1_b32 s55, 7
	buffer_load_dwordx4 v141, s[4:7], s55 offen lds
	s_mov_b32 m0, s33
	ds_read_b128 v[188:191], v162 offset:49152
	buffer_load_dwordx4 v149, s[4:7], s55 offen lds
	s_add_i32 s55, s55, s22
	s_mov_b32 m0, s41
	ds_read_b128 v[192:195], v162 offset:50176
	buffer_load_dwordx4 v141, s[4:7], s55 offen lds
	s_mov_b32 m0, s34
	ds_read_b128 v[196:199], v162 offset:51200
	buffer_load_dwordx4 v137, s[36:39], s54 offen lds
	s_mov_b32 m0, s35
	ds_read_b128 v[200:203], v162 offset:52224
	buffer_load_dwordx4 v145, s[36:39], s54 offen lds
	ds_read_b128 v[204:207], v162 offset:53248
	ds_read_b128 v[208:211], v162 offset:54272
	ds_read_b128 v[212:215], v162 offset:55296
	ds_read_b128 v[216:219], v162 offset:56320
	s_waitcnt vmcnt(7)
	s_waitcnt lgkmcnt(0)
	s_barrier
	s_setprio 1
	v_mfma_f32_16x16x32_bf16 v[56:59], v[128:131], v[188:191], v[56:59]
	v_mfma_f32_16x16x32_bf16 v[60:63], v[164:167], v[188:191], v[60:63]
	v_mfma_f32_16x16x32_bf16 v[40:43], v[128:131], v[196:199], v[40:43]
	v_mfma_f32_16x16x32_bf16 v[44:47], v[164:167], v[196:199], v[44:47]
	v_mfma_f32_16x16x32_bf16 v[24:27], v[128:131], v[204:207], v[24:27]
	v_mfma_f32_16x16x32_bf16 v[28:31], v[164:167], v[204:207], v[28:31]
	v_mfma_f32_16x16x32_bf16 v[8:11], v[128:131], v[212:215], v[8:11]
	v_mfma_f32_16x16x32_bf16 v[12:15], v[164:167], v[212:215], v[12:15]
	v_mfma_f32_16x16x32_bf16 v[56:59], v[132:135], v[192:195], v[56:59]
	v_mfma_f32_16x16x32_bf16 v[60:63], v[168:171], v[192:195], v[60:63]
	v_mfma_f32_16x16x32_bf16 v[40:43], v[132:135], v[200:203], v[40:43]
	v_mfma_f32_16x16x32_bf16 v[44:47], v[168:171], v[200:203], v[44:47]
	v_mfma_f32_16x16x32_bf16 v[24:27], v[132:135], v[208:211], v[24:27]
	v_mfma_f32_16x16x32_bf16 v[28:31], v[168:171], v[208:211], v[28:31]
	v_mfma_f32_16x16x32_bf16 v[8:11], v[132:135], v[216:219], v[8:11]
	v_mfma_f32_16x16x32_bf16 v[12:15], v[168:171], v[216:219], v[12:15]
	v_mfma_f32_16x16x32_bf16 v[48:51], v[172:175], v[188:191], v[48:51]
	v_mfma_f32_16x16x32_bf16 v[52:55], v[180:183], v[188:191], v[52:55]
	v_mfma_f32_16x16x32_bf16 v[32:35], v[172:175], v[196:199], v[32:35]
	v_mfma_f32_16x16x32_bf16 v[36:39], v[180:183], v[196:199], v[36:39]
	v_mfma_f32_16x16x32_bf16 v[16:19], v[172:175], v[204:207], v[16:19]
	v_mfma_f32_16x16x32_bf16 v[20:23], v[180:183], v[204:207], v[20:23]
	v_mfma_f32_16x16x32_bf16 v[4:7], v[172:175], v[212:215], v[4:7]
	v_mfma_f32_16x16x32_bf16 v[0:3], v[180:183], v[212:215], v[0:3]
	v_mfma_f32_16x16x32_bf16 v[48:51], v[176:179], v[192:195], v[48:51]
	v_mfma_f32_16x16x32_bf16 v[52:55], v[184:187], v[192:195], v[52:55]
	v_mfma_f32_16x16x32_bf16 v[32:35], v[176:179], v[200:203], v[32:35]
	v_mfma_f32_16x16x32_bf16 v[36:39], v[184:187], v[200:203], v[36:39]
	v_mfma_f32_16x16x32_bf16 v[16:19], v[176:179], v[208:211], v[16:19]
	v_mfma_f32_16x16x32_bf16 v[20:23], v[184:187], v[208:211], v[20:23]
	v_mfma_f32_16x16x32_bf16 v[4:7], v[176:179], v[216:219], v[4:7]
	v_mfma_f32_16x16x32_bf16 v[0:3], v[184:187], v[216:219], v[0:3]
	s_setprio 0
	s_barrier
	s_add_i32 s63, s63, 2
	s_addk_i32 s61, 0x100
	s_addk_i32 s62, 0x100
	s_cmp_ge_i32 s63, s44
	s_cbranch_scc0 .LBB0_1628
	s_mov_b32 m0, s42
	s_nop 0
	buffer_load_dwordx4 v149, s[4:7], s55 offen lds

; #define PG8_STAGE(bufoff, rs_, soff_, voff) do { _Pragma("unroll") for (int _i = 0; _i < 2; ++_i) \
;         __builtin_amdgcn_raw_ptr_buffer_load_lds(rs_, (LAS void*)(lds + (bufoff) + ldsw + _i * 8192), 16, (int)(voff)[_i], (int)(soff_), 0, 0); } while (0)
; #define PG8_LDA(dst, b, h) do { _Pragma("unroll") for (int m = 0; m < 4; ++m) dst[m] = PG8_LD2(lds + PG8_SA(b, h) + aoff + m * 2048); } while (0)
; #define PG8_LDB(dst, b, h) do { _Pragma("unroll") for (int n = 0; n < 2; ++n) dst[n] = PG8_LD2(lds + PG8_SB(b, h) + boff + n * 2048); } while (0)
; #define PG8_WAIT_V(n) asm volatile("s_waitcnt vmcnt(" #n ")" ::: "memory")
; #define PG8_WAIT_L(n) asm volatile("s_waitcnt lgkmcnt(" #n ")" ::: "memory")
; #define PG8_BAR __builtin_amdgcn_s_barrier()
; #define PG8_SCHED __builtin_amdgcn_sched_barrier(0)
; template <class Epi, class Sched, bool ALIGN_EPI = false, bool SP2 = false, bool FP8 = false>
; __device__ __forceinline__ void gemm_phase(LAS unsigned char* lds, const Gemm g, const Sched& S, const Epi& E, int wbase) {
;     ...
;             PG8_LDB(B0, 0, 0); PG8_LDB(B1, 0, 1); PG8_SCHED; PG8_LDA(At, 0, 0); PG8_STAGE(PG8_SA(1, 1), rAc, a1 + hstep, voffA);
;             PG8_WAIT_V(8); PG8_WAIT_L(0); PG8_BAR; PG8_MMA(0, 0, At, B0); PG8_MMA(0, 1, At, B1); PG8_BAR; PG8_SCHED;
;             PG8_LDA(At, 0, 1); PG8_STAGE(PG8_SB(0, 0), rB2, b2, voffB); PG8_STAGE(PG8_SB(0, 1), rB2, b2 + hstep, voffB); PG8_STAGE(PG8_SA(0, 0), rA2, a2, voffA);
;             PG8_WAIT_V(8); PG8_WAIT_L(0); PG8_BAR; PG8_MMA(1, 0, At, B0); PG8_MMA(1, 1, At, B1); PG8_BAR; PG8_SCHED;
;             PG8_LDB(B0, 1, 0); PG8_LDB(B1, 1, 1); PG8_SCHED; PG8_LDA(At, 1, 0); PG8_STAGE(PG8_SA(0, 1), rA2, a2 + hstep, voffA);
;             PG8_WAIT_V(8); PG8_WAIT_L(0); PG8_BAR; PG8_MMA(0, 0, At, B0); PG8_MMA(0, 1, At, B1); PG8_BAR; PG8_SCHED;
.LBB0_1701:
	s_mov_b32 m0, s44
	s_nop 0
	buffer_load_dwordx4 v173, s[4:7], s55 offen lds
	v_add_u32_e32 v140, 0x10000, v176
	v_add_u32_e32 v156, 0x14000, v176
	ds_read_b128 v[112:115], v140
	ds_read_b128 v[124:127], v140 offset:1024
	ds_read_b128 v[136:139], v140 offset:2048
	ds_read_b128 v[140:143], v140 offset:3072
	ds_read_b128 v[144:147], v156
	ds_read_b128 v[148:151], v156 offset:1024
	ds_read_b128 v[152:155], v156 offset:2048
	ds_read_b128 v[156:159], v156 offset:3072
	s_add_i32 s6, s65, 0x80
	s_cmp_eq_u32 s52, s67
	s_cselect_b32 s68, s21, s6
	s_cselect_b32 s55, s63, s66
	s_or_b32 s54, s68, 0x80
	s_add_i32 s6, s25, s65
	s_mov_b32 m0, s53
	ds_read_b128 v[160:163], v177
	ds_read_b128 v[164:167], v177 offset:1024
	ds_read_b128 v[178:181], v177 offset:2048
	ds_read_b128 v[182:185], v177 offset:3072
	ds_read_b128 v[186:189], v177 offset:4096
	ds_read_b128 v[190:193], v177 offset:5120
	ds_read_b128 v[194:197], v177 offset:6144
	ds_read_b128 v[198:201], v177 offset:7168
	buffer_load_dwordx4 v170, s[36:39], s6 offen lds
	s_mov_b32 m0, s56
	s_nop 0
	buffer_load_dwordx4 v172, s[36:39], s6 offen lds
	s_waitcnt vmcnt(8)
	s_waitcnt lgkmcnt(0)
	s_barrier
	s_setprio 1
	v_mfma_f32_16x16x32_bf16 v[132:135], v[112:115], v[160:163], v[132:135]
	v_mfma_f32_16x16x32_bf16 v[128:131], v[136:139], v[160:163], v[128:131]
	v_mfma_f32_16x16x32_bf16 v[108:111], v[112:115], v[178:181], v[108:111]
	v_mfma_f32_16x16x32_bf16 v[104:107], v[136:139], v[178:181], v[104:107]
	v_mfma_f32_16x16x32_bf16 v[92:95], v[112:115], v[186:189], v[92:95]
	v_mfma_f32_16x16x32_bf16 v[88:91], v[136:139], v[186:189], v[88:91]
	v_mfma_f32_16x16x32_bf16 v[76:79], v[112:115], v[194:197], v[76:79]
	v_mfma_f32_16x16x32_bf16 v[72:75], v[136:139], v[194:197], v[72:75]
	v_mfma_f32_16x16x32_bf16 v[132:135], v[124:127], v[164:167], v[132:135]
	v_mfma_f32_16x16x32_bf16 v[128:131], v[140:143], v[164:167], v[128:131]
	v_mfma_f32_16x16x32_bf16 v[108:111], v[124:127], v[182:185], v[108:111]
	v_mfma_f32_16x16x32_bf16 v[104:107], v[140:143], v[182:185], v[104:107]
	v_mfma_f32_16x16x32_bf16 v[92:95], v[124:127], v[190:193], v[92:95]
	v_mfma_f32_16x16x32_bf16 v[88:91], v[140:143], v[190:193], v[88:91]
	v_mfma_f32_16x16x32_bf16 v[76:79], v[124:127], v[198:201], v[76:79]
	v_mfma_f32_16x16x32_bf16 v[72:75], v[140:143], v[198:201], v[72:75]
	v_mfma_f32_16x16x32_bf16 v[120:123], v[144:147], v[160:163], v[120:123]
	v_mfma_f32_16x16x32_bf16 v[116:119], v[152:155], v[160:163], v[116:119]
	v_mfma_f32_16x16x32_bf16 v[100:103], v[144:147], v[178:181], v[100:103]
	v_mfma_f32_16x16x32_bf16 v[96:99], v[152:155], v[178:181], v[96:99]
	v_mfma_f32_16x16x32_bf16 v[84:87], v[144:147], v[186:189], v[84:87]
	v_mfma_f32_16x16x32_bf16 v[80:83], v[152:155], v[186:189], v[80:83]
	v_mfma_f32_16x16x32_bf16 v[68:71], v[144:147], v[194:197], v[68:71]
	v_mfma_f32_16x16x32_bf16 v[64:67], v[152:155], v[194:197], v[64:67]
	v_mfma_f32_16x16x32_bf16 v[120:123], v[148:151], v[164:167], v[120:123]
	v_mfma_f32_16x16x32_bf16 v[116:119], v[156:159], v[164:167], v[116:119]
	v_mfma_f32_16x16x32_bf16 v[100:103], v[148:151], v[182:185], v[100:103]
	v_mfma_f32_16x16x32_bf16 v[96:99], v[156:159], v[182:185], v[96:99]
	v_mfma_f32_16x16x32_bf16 v[84:87], v[148:151], v[190:193], v[84:87]
	v_mfma_f32_16x16x32_bf16 v[80:83], v[156:159], v[190:193], v[80:83]
	v_mfma_f32_16x16x32_bf16 v[68:71], v[148:151], v[198:201], v[68:71]
	v_mfma_f32_16x16x32_bf16 v[64:67], v[156:159], v[198:201], v[64:67]
	s_setprio 0
	s_barrier
	s_mov_b32 m0, s27
	s_mov_b32 s6, s38
	s_mov_b32 s7, s39
	buffer_load_dwordx4 v171, s[4:7], s55 offen lds
	s_mov_b32 m0, s28
	ds_read_b128 v[160:163], v177 offset:16384
	s_add_i32 s69, s55, s25
	buffer_load_dwordx4 v173, s[4:7], s55 offen lds
	s_mov_b32 m0, s29
	ds_read_b128 v[164:167], v177 offset:17408
	buffer_load_dwordx4 v171, s[4:7], s69 offen lds
	s_mov_b32 m0, s26
	ds_read_b128 v[178:181], v177 offset:18432
	buffer_load_dwordx4 v170, s[36:39], s68 offen lds
	s_mov_b32 m0, s31
	ds_read_b128 v[182:185], v177 offset:19456
	buffer_load_dwordx4 v172, s[36:39], s68 offen lds
	ds_read_b128 v[186:189], v177 offset:20480
	ds_read_b128 v[190:193], v177 offset:21504
	ds_read_b128 v[194:197], v177 offset:22528
	ds_read_b128 v[198:201], v177 offset:23552
	s_waitcnt vmcnt(7)
	s_waitcnt lgkmcnt(0)
	s_barrier
	s_setprio 1
	v_mfma_f32_16x16x32_bf16 v[60:63], v[112:115], v[160:163], v[60:63]
	v_mfma_f32_16x16x32_bf16 v[56:59], v[136:139], v[160:163], v[56:59]
	v_mfma_f32_16x16x32_bf16 v[44:47], v[112:115], v[178:181], v[44:47]
	v_mfma_f32_16x16x32_bf16 v[40:43], v[136:139], v[178:181], v[40:43]
	v_mfma_f32_16x16x32_bf16 v[28:31], v[112:115], v[186:189], v[28:31]
	v_mfma_f32_16x16x32_bf16 v[24:27], v[136:139], v[186:189], v[24:27]
	v_mfma_f32_16x16x32_bf16 v[12:15], v[112:115], v[194:197], v[12:15]
	v_mfma_f32_16x16x32_bf16 v[8:11], v[136:139], v[194:197], v[8:11]
	v_mfma_f32_16x16x32_bf16 v[60:63], v[124:127], v[164:167], v[60:63]
	v_mfma_f32_16x16x32_bf16 v[56:59], v[140:143], v[164:167], v[56:59]
	v_mfma_f32_16x16x32_bf16 v[44:47], v[124:127], v[182:185], v[44:47]
	v_mfma_f32_16x16x32_bf16 v[40:43], v[140:143], v[182:185], v[40:43]
	v_mfma_f32_16x16x32_bf16 v[28:31], v[124:127], v[190:193], v[28:31]
	v_mfma_f32_16x16x32_bf16 v[24:27], v[140:143], v[190:193], v[24:27]
	v_mfma_f32_16x16x32_bf16 v[12:15], v[124:127], v[198:201], v[12:15]
	v_mfma_f32_16x16x32_bf16 v[8:11], v[140:143], v[198:201], v[8:11]
	v_mfma_f32_16x16x32_bf16 v[52:55], v[144:147], v[160:163], v[52:55]
	v_mfma_f32_16x16x32_bf16 v[48:51], v[152:155], v[160:163], v[48:51]
	v_mfma_f32_16x16x32_bf16 v[36:39], v[144:147], v[178:181], v[36:39]
	v_mfma_f32_16x16x32_bf16 v[32:35], v[152:155], v[178:181], v[32:35]
	v_mfma_f32_16x16x32_bf16 v[20:23], v[144:147], v[186:189], v[20:23]
	v_mfma_f32_16x16x32_bf16 v[16:19], v[152:155], v[186:189], v[16:19]
	v_mfma_f32_16x16x32_bf16 v[4:7], v[144:147], v[194:197], v[4:7]
	v_mfma_f32_16x16x32_bf16 v[0:3], v[152:155], v[194:197], v[0:3]
	v_mfma_f32_16x16x32_bf16 v[52:55], v[148:151], v[164:167], v[52:55]
	v_mfma_f32_16x16x32_bf16 v[48:51], v[156:159], v[164:167], v[48:51]
	v_mfma_f32_16x16x32_bf16 v[36:39], v[148:151], v[182:185], v[36:39]
	v_mfma_f32_16x16x32_bf16 v[32:35], v[156:159], v[182:185], v[32:35]
	v_mfma_f32_16x16x32_bf16 v[20:23], v[148:151], v[190:193], v[20:23]
	v_mfma_f32_16x16x32_bf16 v[16:19], v[156:159], v[190:193], v[16:19]
	v_mfma_f32_16x16x32_bf16 v[4:7], v[148:151], v[198:201], v[4:7]
	v_mfma_f32_16x16x32_bf16 v[0:3], v[156:159], v[198:201], v[0:3]
	s_setprio 0
	s_barrier
; #define PG8_STAGE(bufoff, rs_, soff_, voff) do { _Pragma("unroll") for (int _i = 0; _i < 2; ++_i) \
;         __builtin_amdgcn_raw_ptr_buffer_load_lds(rs_, (LAS void*)(lds + (bufoff) + ldsw + _i * 8192), 16, (int)(voff)[_i], (int)(soff_), 0, 0); } while (0)
; #define PG8_LDA(dst, b, h) do { _Pragma("unroll") for (int m = 0; m < 4; ++m) dst[m] = PG8_LD2(lds + PG8_SA(b, h) + aoff + m * 2048); } while (0)
; #define PG8_LDB(dst, b, h) do { _Pragma("unroll") for (int n = 0; n < 2; ++n) dst[n] = PG8_LD2(lds + PG8_SB(b, h) + boff + n * 2048); } while (0)
; #define PG8_WAIT_V(n) asm volatile("s_waitcnt vmcnt(" #n ")" ::: "memory")
; #define PG8_WAIT_L(n) asm volatile("s_waitcnt lgkmcnt(" #n ")" ::: "memory")
; #define PG8_BAR __builtin_amdgcn_s_barrier()
; #define PG8_SCHED __builtin_amdgcn_sched_barrier(0)
; template <class Epi, class Sched, bool ALIGN_EPI = false, bool SP2 = false, bool FP8 = false>
; __device__ __forceinline__ void gemm_phase(LAS unsigned char* lds, const Gemm g, const Sched& S, const Epi& E, int wbase) {
;     ...
;         for (int t = 0; t < nt; t += 2) {
;             const bool last = (t == nt - 2);
;             const unsigned a1 = cA + (unsigned)(t + 1) * kstep;
;     ...
;             PG8_LDA(At, 0, 1); PG8_STAGE(PG8_SB(0, 0), rB2, b2, voffB); PG8_STAGE(PG8_SB(0, 1), rB2, b2 + hstep, voffB); PG8_STAGE(PG8_SA(0, 0), rA2, a2, voffA);
;             PG8_WAIT_V(8); PG8_WAIT_L(0); PG8_BAR; PG8_MMA(1, 0, At, B0); PG8_MMA(1, 1, At, B1); PG8_BAR; PG8_SCHED;
;             PG8_LDB(B0, 1, 0); PG8_LDB(B1, 1, 1); PG8_SCHED; PG8_LDA(At, 1, 0); PG8_STAGE(PG8_SA(0, 1), rA2, a2 + hstep, voffA);
;             PG8_WAIT_V(8); PG8_WAIT_L(0); PG8_BAR; PG8_MMA(0, 0, At, B0); PG8_MMA(0, 1, At, B1); PG8_BAR; PG8_SCHED;
;             PG8_LDA(At, 1, 1); PG8_STAGE(PG8_SB(1, 0), rB2, b3, voffB); PG8_STAGE(PG8_SB(1, 1), rB2, b3 + hstep, voffB); PG8_STAGE(PG8_SA(1, 0), rA2, a3, voffA);
;             PG8_WAIT_V(8); PG8_WAIT_L(0); PG8_BAR; PG8_MMA(1, 0, At, B0); PG8_MMA(1, 1, At, B1); PG8_BAR; PG8_SCHED;
	s_mov_b32 m0, s30
	s_nop 0
	buffer_load_dwordx4 v173, s[4:7], s69 offen lds
	v_add_u32_e32 v140, 0x18000, v176
	v_add_u32_e32 v156, 0x1c000, v176
	ds_read_b128 v[112:115], v140
	ds_read_b128 v[124:127], v140 offset:1024
	ds_read_b128 v[136:139], v140 offset:2048
	ds_read_b128 v[140:143], v140 offset:3072
	ds_read_b128 v[144:147], v156
	ds_read_b128 v[148:151], v156 offset:1024
	ds_read_b128 v[152:155], v156 offset:2048
	ds_read_b128 v[156:159], v156 offset:3072
	s_add_i32 s68, s68, s25
	s_mov_b32 m0, s33
	ds_read_b128 v[160:163], v177 offset:32768
	ds_read_b128 v[164:167], v177 offset:33792
	ds_read_b128 v[178:181], v177 offset:34816
	ds_read_b128 v[182:185], v177 offset:35840
	ds_read_b128 v[186:189], v177 offset:36864
	ds_read_b128 v[190:193], v177 offset:37888
	ds_read_b128 v[194:197], v177 offset:38912
	ds_read_b128 v[198:201], v177 offset:39936
	buffer_load_dwordx4 v170, s[36:39], s68 offen lds
	s_mov_b32 m0, s34
	s_nop 0
	buffer_load_dwordx4 v172, s[36:39], s68 offen lds
	s_waitcnt vmcnt(8)
	s_waitcnt lgkmcnt(0)
	s_barrier
	s_setprio 1
	v_mfma_f32_16x16x32_bf16 v[132:135], v[112:115], v[160:163], v[132:135]
	v_mfma_f32_16x16x32_bf16 v[128:131], v[136:139], v[160:163], v[128:131]
	v_mfma_f32_16x16x32_bf16 v[108:111], v[112:115], v[178:181], v[108:111]
	v_mfma_f32_16x16x32_bf16 v[104:107], v[136:139], v[178:181], v[104:107]
	v_mfma_f32_16x16x32_bf16 v[92:95], v[112:115], v[186:189], v[92:95]
	v_mfma_f32_16x16x32_bf16 v[88:91], v[136:139], v[186:189], v[88:91]
	v_mfma_f32_16x16x32_bf16 v[76:79], v[112:115], v[194:197], v[76:79]
	v_mfma_f32_16x16x32_bf16 v[72:75], v[136:139], v[194:197], v[72:75]
	v_mfma_f32_16x16x32_bf16 v[132:135], v[124:127], v[164:167], v[132:135]
	v_mfma_f32_16x16x32_bf16 v[128:131], v[140:143], v[164:167], v[128:131]
	v_mfma_f32_16x16x32_bf16 v[108:111], v[124:127], v[182:185], v[108:111]
	v_mfma_f32_16x16x32_bf16 v[104:107], v[140:143], v[182:185], v[104:107]
	v_mfma_f32_16x16x32_bf16 v[92:95], v[124:127], v[190:193], v[92:95]
	v_mfma_f32_16x16x32_bf16 v[88:91], v[140:143], v[190:193], v[88:91]
	v_mfma_f32_16x16x32_bf16 v[76:79], v[124:127], v[198:201], v[76:79]
	v_mfma_f32_16x16x32_bf16 v[72:75], v[140:143], v[198:201], v[72:75]
	v_mfma_f32_16x16x32_bf16 v[120:123], v[144:147], v[160:163], v[120:123]
	v_mfma_f32_16x16x32_bf16 v[116:119], v[152:155], v[160:163], v[116:119]
	v_mfma_f32_16x16x32_bf16 v[100:103], v[144:147], v[178:181], v[100:103]
	v_mfma_f32_16x16x32_bf16 v[96:99], v[152:155], v[178:181], v[96:99]
	v_mfma_f32_16x16x32_bf16 v[84:87], v[144:147], v[186:189], v[84:87]
	v_mfma_f32_16x16x32_bf16 v[80:83], v[152:155], v[186:189], v[80:83]
	v_mfma_f32_16x16x32_bf16 v[68:71], v[144:147], v[194:197], v[68:71]
	v_mfma_f32_16x16x32_bf16 v[64:67], v[152:155], v[194:197], v[64:67]
	v_mfma_f32_16x16x32_bf16 v[120:123], v[148:151], v[164:167], v[120:123]
	v_mfma_f32_16x16x32_bf16 v[116:119], v[156:159], v[164:167], v[116:119]
	v_mfma_f32_16x16x32_bf16 v[100:103], v[148:151], v[182:185], v[100:103]
	v_mfma_f32_16x16x32_bf16 v[96:99], v[156:159], v[182:185], v[96:99]
	v_mfma_f32_16x16x32_bf16 v[84:87], v[148:151], v[190:193], v[84:87]
	v_mfma_f32_16x16x32_bf16 v[80:83], v[156:159], v[190:193], v[80:83]
	v_mfma_f32_16x16x32_bf16 v[68:71], v[148:151], v[198:201], v[68:71]
	v_mfma_f32_16x16x32_bf16 v[64:67], v[156:159], v[198:201], v[64:67]
	s_setprio 0
	s_barrier
	s_mov_b32 m0, s1
	s_bitset1_b32 s55, 7
	buffer_load_dwordx4 v171, s[4:7], s55 offen lds
	s_mov_b32 m0, s35
	ds_read_b128 v[160:163], v177 offset:49152
	buffer_load_dwordx4 v173, s[4:7], s55 offen lds
	s_add_i32 s55, s55, s25
	s_mov_b32 m0, s43
	ds_read_b128 v[164:167], v177 offset:50176
	buffer_load_dwordx4 v171, s[4:7], s55 offen lds
	s_mov_b32 m0, s41
	ds_read_b128 v[178:181], v177 offset:51200
	buffer_load_dwordx4 v170, s[36:39], s54 offen lds
	s_mov_b32 m0, s42
	ds_read_b128 v[182:185], v177 offset:52224
	buffer_load_dwordx4 v172, s[36:39], s54 offen lds
	ds_read_b128 v[186:189], v177 offset:53248
	ds_read_b128 v[190:193], v177 offset:54272
	ds_read_b128 v[194:197], v177 offset:55296
	ds_read_b128 v[198:201], v177 offset:56320
	s_waitcnt vmcnt(7)
	s_waitcnt lgkmcnt(0)
	s_barrier
	s_setprio 1
	v_mfma_f32_16x16x32_bf16 v[60:63], v[112:115], v[160:163], v[60:63]
	v_mfma_f32_16x16x32_bf16 v[56:59], v[136:139], v[160:163], v[56:59]
	v_mfma_f32_16x16x32_bf16 v[44:47], v[112:115], v[178:181], v[44:47]
	v_mfma_f32_16x16x32_bf16 v[40:43], v[136:139], v[178:181], v[40:43]
	v_mfma_f32_16x16x32_bf16 v[28:31], v[112:115], v[186:189], v[28:31]
	v_mfma_f32_16x16x32_bf16 v[24:27], v[136:139], v[186:189], v[24:27]
	v_mfma_f32_16x16x32_bf16 v[12:15], v[112:115], v[194:197], v[12:15]
	v_mfma_f32_16x16x32_bf16 v[8:11], v[136:139], v[194:197], v[8:11]
	v_mfma_f32_16x16x32_bf16 v[60:63], v[124:127], v[164:167], v[60:63]
	v_mfma_f32_16x16x32_bf16 v[56:59], v[140:143], v[164:167], v[56:59]
	v_mfma_f32_16x16x32_bf16 v[44:47], v[124:127], v[182:185], v[44:47]
	v_mfma_f32_16x16x32_bf16 v[40:43], v[140:143], v[182:185], v[40:43]
	v_mfma_f32_16x16x32_bf16 v[28:31], v[124:127], v[190:193], v[28:31]
	v_mfma_f32_16x16x32_bf16 v[24:27], v[140:143], v[190:193], v[24:27]
	v_mfma_f32_16x16x32_bf16 v[12:15], v[124:127], v[198:201], v[12:15]
	v_mfma_f32_16x16x32_bf16 v[8:11], v[140:143], v[198:201], v[8:11]
	v_mfma_f32_16x16x32_bf16 v[52:55], v[144:147], v[160:163], v[52:55]
	v_mfma_f32_16x16x32_bf16 v[48:51], v[152:155], v[160:163], v[48:51]
	v_mfma_f32_16x16x32_bf16 v[36:39], v[144:147], v[178:181], v[36:39]
	v_mfma_f32_16x16x32_bf16 v[32:35], v[152:155], v[178:181], v[32:35]
	v_mfma_f32_16x16x32_bf16 v[20:23], v[144:147], v[186:189], v[20:23]
	v_mfma_f32_16x16x32_bf16 v[16:19], v[152:155], v[186:189], v[16:19]
	v_mfma_f32_16x16x32_bf16 v[4:7], v[144:147], v[194:197], v[4:7]
	v_mfma_f32_16x16x32_bf16 v[0:3], v[152:155], v[194:197], v[0:3]
	v_mfma_f32_16x16x32_bf16 v[52:55], v[148:151], v[164:167], v[52:55]
	v_mfma_f32_16x16x32_bf16 v[48:51], v[156:159], v[164:167], v[48:51]
	v_mfma_f32_16x16x32_bf16 v[36:39], v[148:151], v[182:185], v[36:39]
	v_mfma_f32_16x16x32_bf16 v[32:35], v[156:159], v[182:185], v[32:35]
	v_mfma_f32_16x16x32_bf16 v[20:23], v[148:151], v[190:193], v[20:23]
	v_mfma_f32_16x16x32_bf16 v[16:19], v[156:159], v[190:193], v[16:19]
	v_mfma_f32_16x16x32_bf16 v[4:7], v[148:151], v[198:201], v[4:7]
	v_mfma_f32_16x16x32_bf16 v[0:3], v[156:159], v[198:201], v[0:3]
	s_setprio 0
	s_barrier
	s_add_i32 s67, s67, 2
	s_addk_i32 s65, 0x100
	s_addk_i32 s66, 0x100
	s_cmp_ge_i32 s67, s47
	s_cbranch_scc0 .LBB0_1701
	s_mov_b32 m0, s44
	s_nop 0
	buffer_load_dwordx4 v173, s[4:7], s55 offen lds

; #define PG8_STAGE(bufoff, rs_, soff_, voff) do { _Pragma("unroll") for (int _i = 0; _i < 2; ++_i) \
;         __builtin_amdgcn_raw_ptr_buffer_load_lds(rs_, (LAS void*)(lds + (bufoff) + ldsw + _i * 8192), 16, (int)(voff)[_i], (int)(soff_), 0, 0); } while (0)
; #define PG8_LDA(dst, b, h) do { _Pragma("unroll") for (int m = 0; m < 4; ++m) dst[m] = PG8_LD2(lds + PG8_SA(b, h) + aoff + m * 2048); } while (0)
; #define PG8_LDB(dst, b, h) do { _Pragma("unroll") for (int n = 0; n < 2; ++n) dst[n] = PG8_LD2(lds + PG8_SB(b, h) + boff + n * 2048); } while (0)
; #define PG8_WAIT_V(n) asm volatile("s_waitcnt vmcnt(" #n ")" ::: "memory")
; #define PG8_WAIT_L(n) asm volatile("s_waitcnt lgkmcnt(" #n ")" ::: "memory")
; #define PG8_BAR __builtin_amdgcn_s_barrier()
; #define PG8_SCHED __builtin_amdgcn_sched_barrier(0)
; template <class Epi, class Sched, bool ALIGN_EPI = false, bool SP2 = false, bool FP8 = false>
; __device__ __forceinline__ void gemm_phase(LAS unsigned char* lds, const Gemm g, const Sched& S, const Epi& E, int wbase) {
;     ...
;             PG8_LDB(B0, 0, 0); PG8_LDB(B1, 0, 1); PG8_SCHED; PG8_LDA(At, 0, 0); PG8_STAGE(PG8_SA(1, 1), rAc, a1 + hstep, voffA);
;             PG8_WAIT_V(8); PG8_WAIT_L(0); PG8_BAR; PG8_MMA(0, 0, At, B0); PG8_MMA(0, 1, At, B1); PG8_BAR; PG8_SCHED;
;             PG8_LDA(At, 0, 1); PG8_STAGE(PG8_SB(0, 0), rB2, b2, voffB); PG8_STAGE(PG8_SB(0, 1), rB2, b2 + hstep, voffB); PG8_STAGE(PG8_SA(0, 0), rA2, a2, voffA);
;             PG8_WAIT_V(8); PG8_WAIT_L(0); PG8_BAR; PG8_MMA(1, 0, At, B0); PG8_MMA(1, 1, At, B1); PG8_BAR; PG8_SCHED;
;             PG8_LDB(B0, 1, 0); PG8_LDB(B1, 1, 1); PG8_SCHED; PG8_LDA(At, 1, 0); PG8_STAGE(PG8_SA(0, 1), rA2, a2 + hstep, voffA);
;             PG8_WAIT_V(8); PG8_WAIT_L(0); PG8_BAR; PG8_MMA(0, 0, At, B0); PG8_MMA(0, 1, At, B1); PG8_BAR; PG8_SCHED;
.LBB0_1781:
	s_mov_b32 m0, s41
	s_nop 0
	buffer_load_dwordx4 v151, s[4:7], s55 offen lds
	v_add_u32_e32 v140, 0x10000, v154
	v_add_u32_e32 v144, 0x14000, v154
	ds_read_b128 v[128:131], v140
	ds_read_b128 v[132:135], v140 offset:1024
	ds_read_b128 v[136:139], v140 offset:2048
	ds_read_b128 v[140:143], v140 offset:3072
	ds_read_b128 v[156:159], v144
	ds_read_b128 v[160:163], v144 offset:1024
	ds_read_b128 v[164:167], v144 offset:2048
	ds_read_b128 v[168:171], v144 offset:3072
	s_add_i32 s6, s61, 0x80
	s_cmp_eq_u32 s45, s63
	s_cselect_b32 s65, s59, s6
	s_cselect_b32 s55, s60, s62
	s_or_b32 s54, s65, 0x80
	s_add_i32 s6, s21, s61
	s_mov_b32 m0, s46
	ds_read_b128 v[172:175], v155
	ds_read_b128 v[176:179], v155 offset:1024
	ds_read_b128 v[180:183], v155 offset:2048
	ds_read_b128 v[184:187], v155 offset:3072
	ds_read_b128 v[194:197], v155 offset:4096
	ds_read_b128 v[198:201], v155 offset:5120
	ds_read_b128 v[202:205], v155 offset:6144
	ds_read_b128 v[206:209], v155 offset:7168
	buffer_load_dwordx4 v148, s[36:39], s6 offen lds
	s_mov_b32 m0, s47
	s_nop 0
	buffer_load_dwordx4 v150, s[36:39], s6 offen lds
	s_waitcnt vmcnt(8)
	s_waitcnt lgkmcnt(0)
	s_barrier
	s_setprio 1
	v_mfma_f32_16x16x128_f8f6f4 v[120:123], v[128:135], v[172:179], v[120:123]
	v_mfma_f32_16x16x128_f8f6f4 v[124:127], v[136:143], v[172:179], v[124:127]
	v_mfma_f32_16x16x128_f8f6f4 v[104:107], v[128:135], v[180:187], v[104:107]
	v_mfma_f32_16x16x128_f8f6f4 v[108:111], v[136:143], v[180:187], v[108:111]
	v_mfma_f32_16x16x128_f8f6f4 v[144:147], v[128:135], v[194:201], v[88:91]
	v_mfma_f32_16x16x128_f8f6f4 v[188:191], v[136:143], v[194:201], v[92:95]
	v_mfma_f32_16x16x128_f8f6f4 v[210:213], v[128:135], v[202:209], v[72:75]
	v_mfma_f32_16x16x128_f8f6f4 v[214:217], v[136:143], v[202:209], v[76:79]
	v_mfma_f32_16x16x128_f8f6f4 v[112:115], v[156:163], v[172:179], v[112:115]
	v_mfma_f32_16x16x128_f8f6f4 v[116:119], v[164:171], v[172:179], v[116:119]
	v_mfma_f32_16x16x128_f8f6f4 v[96:99], v[156:163], v[180:187], v[96:99]
	v_mfma_f32_16x16x128_f8f6f4 v[100:103], v[164:171], v[180:187], v[100:103]
	v_mfma_f32_16x16x128_f8f6f4 v[172:175], v[156:163], v[194:201], v[80:83]
	v_mfma_f32_16x16x128_f8f6f4 v[176:179], v[164:171], v[194:201], v[84:87]
	v_mfma_f32_16x16x128_f8f6f4 v[180:183], v[156:163], v[202:209], v[64:67]
	v_mfma_f32_16x16x128_f8f6f4 v[184:187], v[164:171], v[202:209], v[68:71]
	s_setprio 0
	s_barrier
	s_mov_b32 m0, s23
	s_mov_b32 s6, s38
	s_mov_b32 s7, s39
	s_nop 0
	buffer_load_dwordx4 v149, s[4:7], s55 offen lds
	s_mov_b32 m0, s24
	ds_read_b128 v[64:67], v155 offset:16384
	s_add_i32 s66, s55, s21
	buffer_load_dwordx4 v151, s[4:7], s55 offen lds
	s_mov_b32 m0, s25
	ds_read_b128 v[68:71], v155 offset:17408
	buffer_load_dwordx4 v149, s[4:7], s66 offen lds
	s_mov_b32 m0, s22
	ds_read_b128 v[72:75], v155 offset:18432
	buffer_load_dwordx4 v148, s[36:39], s65 offen lds
	s_mov_b32 m0, s27
	ds_read_b128 v[76:79], v155 offset:19456
	buffer_load_dwordx4 v150, s[36:39], s65 offen lds
	ds_read_b128 v[80:83], v155 offset:20480
	ds_read_b128 v[84:87], v155 offset:21504
	ds_read_b128 v[88:91], v155 offset:22528
	ds_read_b128 v[92:95], v155 offset:23552
	s_waitcnt vmcnt(7)
	s_waitcnt lgkmcnt(0)
	s_barrier
	s_setprio 1
	v_mfma_f32_16x16x128_f8f6f4 v[56:59], v[128:135], v[64:71], v[56:59]
	v_mfma_f32_16x16x128_f8f6f4 v[60:63], v[136:143], v[64:71], v[60:63]
	v_mfma_f32_16x16x128_f8f6f4 v[8:11], v[128:135], v[88:95], v[8:11]
	v_mfma_f32_16x16x128_f8f6f4 v[192:195], v[128:135], v[72:79], v[40:43]
	v_mfma_f32_16x16x128_f8f6f4 v[196:199], v[136:143], v[72:79], v[44:47]
	v_mfma_f32_16x16x128_f8f6f4 v[200:203], v[128:135], v[80:87], v[24:27]
	v_mfma_f32_16x16x128_f8f6f4 v[204:207], v[136:143], v[80:87], v[28:31]
	v_mfma_f32_16x16x128_f8f6f4 v[218:221], v[136:143], v[88:95], v[12:15]
	v_mfma_f32_16x16x128_f8f6f4 v[52:55], v[164:171], v[64:71], v[52:55]
	v_mfma_f32_16x16x128_f8f6f4 v[226:229], v[156:163], v[64:71], v[48:51]
	v_mfma_f32_16x16x128_f8f6f4 v[230:233], v[156:163], v[72:79], v[32:35]
	v_mfma_f32_16x16x128_f8f6f4 v[234:237], v[164:171], v[72:79], v[36:39]
	v_mfma_f32_16x16x128_f8f6f4 v[238:241], v[156:163], v[80:87], v[16:19]
	v_mfma_f32_16x16x128_f8f6f4 v[242:245], v[164:171], v[80:87], v[20:23]
	v_mfma_f32_16x16x128_f8f6f4 v[246:249], v[156:163], v[88:95], v[4:7]
	v_mfma_f32_16x16x128_f8f6f4 v[250:253], v[164:171], v[88:95], v[0:3]
	s_setprio 0
	s_barrier
; #define PG8_STAGE(bufoff, rs_, soff_, voff) do { _Pragma("unroll") for (int _i = 0; _i < 2; ++_i) \
;         __builtin_amdgcn_raw_ptr_buffer_load_lds(rs_, (LAS void*)(lds + (bufoff) + ldsw + _i * 8192), 16, (int)(voff)[_i], (int)(soff_), 0, 0); } while (0)
; #define PG8_LDA(dst, b, h) do { _Pragma("unroll") for (int m = 0; m < 4; ++m) dst[m] = PG8_LD2(lds + PG8_SA(b, h) + aoff + m * 2048); } while (0)
; #define PG8_LDB(dst, b, h) do { _Pragma("unroll") for (int n = 0; n < 2; ++n) dst[n] = PG8_LD2(lds + PG8_SB(b, h) + boff + n * 2048); } while (0)
; #define PG8_WAIT_V(n) asm volatile("s_waitcnt vmcnt(" #n ")" ::: "memory")
; #define PG8_WAIT_L(n) asm volatile("s_waitcnt lgkmcnt(" #n ")" ::: "memory")
; #define PG8_BAR __builtin_amdgcn_s_barrier()
; #define PG8_SCHED __builtin_amdgcn_sched_barrier(0)
; template <class Epi, class Sched, bool ALIGN_EPI = false, bool SP2 = false, bool FP8 = false>
; __device__ __forceinline__ void gemm_phase(LAS unsigned char* lds, const Gemm g, const Sched& S, const Epi& E, int wbase) {
;     ...
;             PG8_LDA(At, 0, 1); PG8_STAGE(PG8_SB(0, 0), rB2, b2, voffB); PG8_STAGE(PG8_SB(0, 1), rB2, b2 + hstep, voffB); PG8_STAGE(PG8_SA(0, 0), rA2, a2, voffA);
;             PG8_WAIT_V(8); PG8_WAIT_L(0); PG8_BAR; PG8_MMA(1, 0, At, B0); PG8_MMA(1, 1, At, B1); PG8_BAR; PG8_SCHED;
;             PG8_LDB(B0, 1, 0); PG8_LDB(B1, 1, 1); PG8_SCHED; PG8_LDA(At, 1, 0); PG8_STAGE(PG8_SA(0, 1), rA2, a2 + hstep, voffA);
;             PG8_WAIT_V(8); PG8_WAIT_L(0); PG8_BAR; PG8_MMA(0, 0, At, B0); PG8_MMA(0, 1, At, B1); PG8_BAR; PG8_SCHED;
;             PG8_LDA(At, 1, 1); PG8_STAGE(PG8_SB(1, 0), rB2, b3, voffB); PG8_STAGE(PG8_SB(1, 1), rB2, b3 + hstep, voffB); PG8_STAGE(PG8_SA(1, 0), rA2, a3, voffA);
;             PG8_WAIT_V(8); PG8_WAIT_L(0); PG8_BAR; PG8_MMA(1, 0, At, B0); PG8_MMA(1, 1, At, B1); PG8_BAR; PG8_SCHED;
	s_mov_b32 m0, s26
	s_nop 0
	buffer_load_dwordx4 v151, s[4:7], s66 offen lds
	s_nop 1
	v_add_u32_e32 v16, 0x18000, v154
	v_add_u32_e32 v20, 0x1c000, v154
	s_nop 0
	ds_read_b128 v[0:3], v16
	ds_read_b128 v[4:7], v16 offset:1024
	ds_read_b128 v[12:15], v16 offset:2048
	ds_read_b128 v[16:19], v16 offset:3072
	ds_read_b128 v[128:131], v20
	ds_read_b128 v[132:135], v20 offset:1024
	ds_read_b128 v[136:139], v20 offset:2048
	ds_read_b128 v[140:143], v20 offset:3072
	s_add_i32 s65, s65, s21
	s_mov_b32 m0, s28
	ds_read_b128 v[20:23], v155 offset:32768
	ds_read_b128 v[24:27], v155 offset:33792
	ds_read_b128 v[28:31], v155 offset:34816
	ds_read_b128 v[32:35], v155 offset:35840
	ds_read_b128 v[36:39], v155 offset:36864
	ds_read_b128 v[40:43], v155 offset:37888
	ds_read_b128 v[44:47], v155 offset:38912
	ds_read_b128 v[48:51], v155 offset:39936
	buffer_load_dwordx4 v148, s[36:39], s65 offen lds
	s_mov_b32 m0, s29
	s_nop 0
	buffer_load_dwordx4 v150, s[36:39], s65 offen lds
	s_waitcnt vmcnt(8)
	s_waitcnt lgkmcnt(0)
	s_barrier
	s_setprio 1
	v_mfma_f32_16x16x128_f8f6f4 v[120:123], v[0:7], v[20:27], v[120:123]
	v_mfma_f32_16x16x128_f8f6f4 v[124:127], v[12:19], v[20:27], v[124:127]
	v_mfma_f32_16x16x128_f8f6f4 v[104:107], v[0:7], v[28:35], v[104:107]
	v_mfma_f32_16x16x128_f8f6f4 v[108:111], v[12:19], v[28:35], v[108:111]
	v_mfma_f32_16x16x128_f8f6f4 v[88:91], v[0:7], v[36:43], v[144:147]
	v_mfma_f32_16x16x128_f8f6f4 v[92:95], v[12:19], v[36:43], v[188:191]
	v_mfma_f32_16x16x128_f8f6f4 v[72:75], v[0:7], v[44:51], v[210:213]
	v_mfma_f32_16x16x128_f8f6f4 v[76:79], v[12:19], v[44:51], v[214:217]
	v_mfma_f32_16x16x128_f8f6f4 v[112:115], v[128:135], v[20:27], v[112:115]
	v_mfma_f32_16x16x128_f8f6f4 v[116:119], v[136:143], v[20:27], v[116:119]
	v_mfma_f32_16x16x128_f8f6f4 v[96:99], v[128:135], v[28:35], v[96:99]
	v_mfma_f32_16x16x128_f8f6f4 v[100:103], v[136:143], v[28:35], v[100:103]
	v_mfma_f32_16x16x128_f8f6f4 v[80:83], v[128:135], v[36:43], v[172:175]
	v_mfma_f32_16x16x128_f8f6f4 v[84:87], v[136:143], v[36:43], v[176:179]
	v_mfma_f32_16x16x128_f8f6f4 v[64:67], v[128:135], v[44:51], v[180:183]
	v_mfma_f32_16x16x128_f8f6f4 v[68:71], v[136:143], v[44:51], v[184:187]
	s_setprio 0
	s_barrier
	s_mov_b32 m0, s30
	s_bitset1_b32 s55, 7
	buffer_load_dwordx4 v149, s[4:7], s55 offen lds
	s_mov_b32 m0, s31
	ds_read_b128 v[32:35], v155 offset:49152
	buffer_load_dwordx4 v151, s[4:7], s55 offen lds
	s_add_i32 s55, s55, s21
	s_mov_b32 m0, s35
	ds_read_b128 v[36:39], v155 offset:50176
	buffer_load_dwordx4 v149, s[4:7], s55 offen lds
	s_mov_b32 m0, s33
	ds_read_b128 v[156:159], v155 offset:51200
	buffer_load_dwordx4 v148, s[36:39], s54 offen lds
	s_mov_b32 m0, s34
	ds_read_b128 v[160:163], v155 offset:52224
	buffer_load_dwordx4 v150, s[36:39], s54 offen lds
	ds_read_b128 v[164:167], v155 offset:53248
	ds_read_b128 v[168:171], v155 offset:54272
	ds_read_b128 v[172:175], v155 offset:55296
	ds_read_b128 v[176:179], v155 offset:56320
	s_waitcnt vmcnt(7)
	s_waitcnt lgkmcnt(0)
	s_barrier
	s_setprio 1
	v_mfma_f32_16x16x128_f8f6f4 v[56:59], v[0:7], v[32:39], v[56:59]
	v_mfma_f32_16x16x128_f8f6f4 v[60:63], v[12:19], v[32:39], v[60:63]
	v_mfma_f32_16x16x128_f8f6f4 v[40:43], v[0:7], v[156:163], v[192:195]
	v_mfma_f32_16x16x128_f8f6f4 v[44:47], v[12:19], v[156:163], v[196:199]
	v_mfma_f32_16x16x128_f8f6f4 v[24:27], v[0:7], v[164:171], v[200:203]
	v_mfma_f32_16x16x128_f8f6f4 v[28:31], v[12:19], v[164:171], v[204:207]
	v_mfma_f32_16x16x128_f8f6f4 v[8:11], v[0:7], v[172:179], v[8:11]
	v_mfma_f32_16x16x128_f8f6f4 v[12:15], v[12:19], v[172:179], v[218:221]
	v_mfma_f32_16x16x128_f8f6f4 v[48:51], v[128:135], v[32:39], v[226:229]
	v_mfma_f32_16x16x128_f8f6f4 v[52:55], v[136:143], v[32:39], v[52:55]
	v_mfma_f32_16x16x128_f8f6f4 v[32:35], v[128:135], v[156:163], v[230:233]
	v_mfma_f32_16x16x128_f8f6f4 v[36:39], v[136:143], v[156:163], v[234:237]
	v_mfma_f32_16x16x128_f8f6f4 v[16:19], v[128:135], v[164:171], v[238:241]
	v_mfma_f32_16x16x128_f8f6f4 v[20:23], v[136:143], v[164:171], v[242:245]
	v_mfma_f32_16x16x128_f8f6f4 v[4:7], v[128:135], v[172:179], v[246:249]
	v_mfma_f32_16x16x128_f8f6f4 v[0:3], v[136:143], v[172:179], v[250:253]
	s_setprio 0
	s_barrier
	s_add_i32 s63, s63, 2
	s_addk_i32 s61, 0x100
	s_addk_i32 s62, 0x100
	s_cmp_ge_i32 s63, s43
	s_cbranch_scc0 .LBB0_1781
	s_mov_b32 m0, s41
	s_nop 0
	buffer_load_dwordx4 v151, s[4:7], s55 offen lds

; #define PG8_STAGE(bufoff, rs_, soff_, voff) do { _Pragma("unroll") for (int _i = 0; _i < 2; ++_i) \
;         __builtin_amdgcn_raw_ptr_buffer_load_lds(rs_, (LAS void*)(lds + (bufoff) + ldsw + _i * 8192), 16, (int)(voff)[_i], (int)(soff_), 0, 0); } while (0)
; #define PG8_LDA(dst, b, h) do { _Pragma("unroll") for (int m = 0; m < 4; ++m) dst[m] = PG8_LD2(lds + PG8_SA(b, h) + aoff + m * 2048); } while (0)
; #define PG8_LDB(dst, b, h) do { _Pragma("unroll") for (int n = 0; n < 2; ++n) dst[n] = PG8_LD2(lds + PG8_SB(b, h) + boff + n * 2048); } while (0)
; #define PG8_WAIT_V(n) asm volatile("s_waitcnt vmcnt(" #n ")" ::: "memory")
; #define PG8_WAIT_L(n) asm volatile("s_waitcnt lgkmcnt(" #n ")" ::: "memory")
; #define PG8_BAR __builtin_amdgcn_s_barrier()
; #define PG8_SCHED __builtin_amdgcn_sched_barrier(0)
; template <class Epi, class Sched, bool ALIGN_EPI = false, bool SP2 = false, bool FP8 = false>
; __device__ __forceinline__ void gemm_phase(LAS unsigned char* lds, const Gemm g, const Sched& S, const Epi& E, int wbase) {
;     ...
;             PG8_LDB(B0, 0, 0); PG8_LDB(B1, 0, 1); PG8_SCHED; PG8_LDA(At, 0, 0); PG8_STAGE(PG8_SA(1, 1), rAc, a1 + hstep, voffA);
;             PG8_WAIT_V(8); PG8_WAIT_L(0); PG8_BAR; PG8_MMA(0, 0, At, B0); PG8_MMA(0, 1, At, B1); PG8_BAR; PG8_SCHED;
;             PG8_LDA(At, 0, 1); PG8_STAGE(PG8_SB(0, 0), rB2, b2, voffB); PG8_STAGE(PG8_SB(0, 1), rB2, b2 + hstep, voffB); PG8_STAGE(PG8_SA(0, 0), rA2, a2, voffA);
;             PG8_WAIT_V(8); PG8_WAIT_L(0); PG8_BAR; PG8_MMA(1, 0, At, B0); PG8_MMA(1, 1, At, B1); PG8_BAR; PG8_SCHED;
;             PG8_LDB(B0, 1, 0); PG8_LDB(B1, 1, 1); PG8_SCHED; PG8_LDA(At, 1, 0); PG8_STAGE(PG8_SA(0, 1), rA2, a2 + hstep, voffA);
;             PG8_WAIT_V(8); PG8_WAIT_L(0); PG8_BAR; PG8_MMA(0, 0, At, B0); PG8_MMA(0, 1, At, B1); PG8_BAR; PG8_SCHED;
.LBB0_1854:
	s_mov_b32 m0, s44
	s_nop 0
	buffer_load_dwordx4 v173, s[4:7], s55 offen lds
	v_add_u32_e32 v140, 0x10000, v176
	v_add_u32_e32 v156, 0x14000, v176
	ds_read_b128 v[128:131], v140
	ds_read_b128 v[132:135], v140 offset:1024
	ds_read_b128 v[136:139], v140 offset:2048
	ds_read_b128 v[140:143], v140 offset:3072
	ds_read_b128 v[144:147], v156
	ds_read_b128 v[148:151], v156 offset:1024
	ds_read_b128 v[152:155], v156 offset:2048
	ds_read_b128 v[156:159], v156 offset:3072
	s_add_i32 s6, s65, 0x80
	s_cmp_eq_u32 s52, s67
	s_cselect_b32 s68, s21, s6
	s_cselect_b32 s55, s63, s66
	s_or_b32 s54, s68, 0x80
	s_add_i32 s6, s24, s65
	s_mov_b32 m0, s53
	ds_read_b128 v[160:163], v177
	ds_read_b128 v[164:167], v177 offset:1024
	ds_read_b128 v[178:181], v177 offset:2048
	ds_read_b128 v[182:185], v177 offset:3072
	ds_read_b128 v[194:197], v177 offset:4096
	ds_read_b128 v[198:201], v177 offset:5120
	ds_read_b128 v[202:205], v177 offset:6144
	ds_read_b128 v[206:209], v177 offset:7168
	buffer_load_dwordx4 v170, s[36:39], s6 offen lds
	s_mov_b32 m0, s56
	s_nop 0
	buffer_load_dwordx4 v172, s[36:39], s6 offen lds
	s_waitcnt vmcnt(8)
	s_waitcnt lgkmcnt(0)
	s_barrier
	s_setprio 1
	v_mfma_f32_16x16x128_f8f6f4 v[124:127], v[128:135], v[160:167], v[124:127]
	v_mfma_f32_16x16x128_f8f6f4 v[120:123], v[136:143], v[160:167], v[120:123]
	v_mfma_f32_16x16x128_f8f6f4 v[108:111], v[128:135], v[178:185], v[108:111]
	v_mfma_f32_16x16x128_f8f6f4 v[104:107], v[136:143], v[178:185], v[104:107]
	v_mfma_f32_16x16x128_f8f6f4 v[186:189], v[128:135], v[194:201], v[92:95]
	v_mfma_f32_16x16x128_f8f6f4 v[190:193], v[136:143], v[194:201], v[88:91]
	v_mfma_f32_16x16x128_f8f6f4 v[210:213], v[128:135], v[202:209], v[76:79]
	v_mfma_f32_16x16x128_f8f6f4 v[214:217], v[136:143], v[202:209], v[72:75]
	v_mfma_f32_16x16x128_f8f6f4 v[116:119], v[144:151], v[160:167], v[116:119]
	v_mfma_f32_16x16x128_f8f6f4 v[112:115], v[152:159], v[160:167], v[112:115]
	v_mfma_f32_16x16x128_f8f6f4 v[100:103], v[144:151], v[178:185], v[100:103]
	v_mfma_f32_16x16x128_f8f6f4 v[96:99], v[152:159], v[178:185], v[96:99]
	v_mfma_f32_16x16x128_f8f6f4 v[160:163], v[144:151], v[194:201], v[84:87]
	v_mfma_f32_16x16x128_f8f6f4 v[164:167], v[152:159], v[194:201], v[80:83]
	v_mfma_f32_16x16x128_f8f6f4 v[178:181], v[144:151], v[202:209], v[68:71]
	v_mfma_f32_16x16x128_f8f6f4 v[182:185], v[152:159], v[202:209], v[64:67]
	s_setprio 0
	s_barrier
	s_mov_b32 m0, s26
	s_mov_b32 s6, s38
	s_mov_b32 s7, s39
	s_nop 1
	buffer_load_dwordx4 v171, s[4:7], s55 offen lds
	s_mov_b32 m0, s27
	ds_read_b128 v[64:67], v177 offset:16384
	s_add_i32 s69, s55, s24
	buffer_load_dwordx4 v173, s[4:7], s55 offen lds
	s_mov_b32 m0, s28
	ds_read_b128 v[68:71], v177 offset:17408
	buffer_load_dwordx4 v171, s[4:7], s69 offen lds
	s_mov_b32 m0, s25
	ds_read_b128 v[72:75], v177 offset:18432
	buffer_load_dwordx4 v170, s[36:39], s68 offen lds
	s_mov_b32 m0, s30
	ds_read_b128 v[76:79], v177 offset:19456
	buffer_load_dwordx4 v172, s[36:39], s68 offen lds
	ds_read_b128 v[80:83], v177 offset:20480
	ds_read_b128 v[84:87], v177 offset:21504
	ds_read_b128 v[88:91], v177 offset:22528
	ds_read_b128 v[92:95], v177 offset:23552
	s_waitcnt vmcnt(7)
	s_waitcnt lgkmcnt(0)
	s_barrier
	s_setprio 1
	v_mfma_f32_16x16x128_f8f6f4 v[60:63], v[128:135], v[64:71], v[60:63]
	v_mfma_f32_16x16x128_f8f6f4 v[56:59], v[136:143], v[64:71], v[56:59]
	v_mfma_f32_16x16x128_f8f6f4 v[194:197], v[128:135], v[72:79], v[44:47]
	v_mfma_f32_16x16x128_f8f6f4 v[198:201], v[136:143], v[72:79], v[40:43]
	v_mfma_f32_16x16x128_f8f6f4 v[202:205], v[128:135], v[80:87], v[28:31]
	v_mfma_f32_16x16x128_f8f6f4 v[206:209], v[136:143], v[80:87], v[24:27]
	v_mfma_f32_16x16x128_f8f6f4 v[218:221], v[128:135], v[88:95], v[12:15]
	v_mfma_f32_16x16x128_f8f6f4 v[226:229], v[136:143], v[88:95], v[8:11]
	v_mfma_f32_16x16x128_f8f6f4 v[52:55], v[144:151], v[64:71], v[52:55]
	v_mfma_f32_16x16x128_f8f6f4 v[48:51], v[152:159], v[64:71], v[48:51]
	v_mfma_f32_16x16x128_f8f6f4 v[230:233], v[144:151], v[72:79], v[36:39]
	v_mfma_f32_16x16x128_f8f6f4 v[234:237], v[152:159], v[72:79], v[32:35]
	v_mfma_f32_16x16x128_f8f6f4 v[238:241], v[144:151], v[80:87], v[20:23]
	v_mfma_f32_16x16x128_f8f6f4 v[242:245], v[152:159], v[80:87], v[16:19]
	v_mfma_f32_16x16x128_f8f6f4 v[246:249], v[144:151], v[88:95], v[4:7]
	v_mfma_f32_16x16x128_f8f6f4 v[250:253], v[152:159], v[88:95], v[0:3]
	s_setprio 0
	s_barrier
; #define PG8_STAGE(bufoff, rs_, soff_, voff) do { _Pragma("unroll") for (int _i = 0; _i < 2; ++_i) \
;         __builtin_amdgcn_raw_ptr_buffer_load_lds(rs_, (LAS void*)(lds + (bufoff) + ldsw + _i * 8192), 16, (int)(voff)[_i], (int)(soff_), 0, 0); } while (0)
; #define PG8_LDA(dst, b, h) do { _Pragma("unroll") for (int m = 0; m < 4; ++m) dst[m] = PG8_LD2(lds + PG8_SA(b, h) + aoff + m * 2048); } while (0)
; #define PG8_LDB(dst, b, h) do { _Pragma("unroll") for (int n = 0; n < 2; ++n) dst[n] = PG8_LD2(lds + PG8_SB(b, h) + boff + n * 2048); } while (0)
; template <class Epi, class Sched, bool ALIGN_EPI = false, bool SP2 = false, bool FP8 = false>
; __device__ __forceinline__ void gemm_phase(LAS unsigned char* lds, const Gemm g, const Sched& S, const Epi& E, int wbase) {
;     ...
;         for (int t = 0; t < nt; t += 2) {
;             const bool last = (t == nt - 2);
;             const unsigned a1 = cA + (unsigned)(t + 1) * kstep;
;             const unsigned a2 = last ? nA : cA + (unsigned)(t + 2) * kstep, b2 = last ? nB : cB + (unsigned)(t + 2) * kstep; const rsrc_t rA2 = (Sched::TWO && last) ? rAn : rAc, rB2 = (Sched::TWO && last) ? rBn : rBc;
;             const unsigned a3 = a2 + kstep, b3 = b2 + kstep;
;             if (last && has_next) S.a_ready(nxt);
;             if constexpr (SP2) {
;             PG8_LDB(B0, 0, 0); PG8_LDB(B1, 0, 1); PG8_SCHED; PG8_LDA(At, 0, 0); PG8_STAGE(PG8_SA(1, 1), rAc, a1 + hstep, voffA);
;             PG8_WAIT_V(8); PG8_WAIT_L(0); PG8_BAR; PG8_MMA(0, 0, At, B0); PG8_MMA(0, 1, At, B1); PG8_BAR; PG8_SCHED;
;             PG8_LDA(At, 0, 1); PG8_STAGE(PG8_SB(0, 0), rB2, b2, voffB); PG8_STAGE(PG8_SB(0, 1), rB2, b2 + hstep, voffB); PG8_STAGE(PG8_SA(0, 0), rA2, a2, voffA);
;             PG8_WAIT_V(8); PG8_WAIT_L(0); PG8_BAR; PG8_MMA(1, 0, At, B0); PG8_MMA(1, 1, At, B1); PG8_BAR; PG8_SCHED;
;             PG8_LDB(B0, 1, 0); PG8_LDB(B1, 1, 1); PG8_SCHED; PG8_LDA(At, 1, 0); PG8_STAGE(PG8_SA(0, 1), rA2, a2 + hstep, voffA);
;             PG8_WAIT_V(8); PG8_WAIT_L(0); PG8_BAR; PG8_MMA(0, 0, At, B0); PG8_MMA(0, 1, At, B1); PG8_BAR; PG8_SCHED;
;             PG8_LDA(At, 1, 1); PG8_STAGE(PG8_SB(1, 0), rB2, b3, voffB); PG8_STAGE(PG8_SB(1, 1), rB2, b3 + hstep, voffB); PG8_STAGE(PG8_SA(1, 0), rA2, a3, voffA);
;             PG8_WAIT_V(8); PG8_WAIT_L(0); PG8_BAR; PG8_MMA(1, 0, At, B0); PG8_MMA(1, 1, At, B1); PG8_BAR; PG8_SCHED;
	s_mov_b32 m0, s29
	s_nop 0
	buffer_load_dwordx4 v173, s[4:7], s69 offen lds
	v_add_u32_e32 v8, 0x18000, v176
	s_nop 3
	ds_read_b128 v[0:3], v8
	ds_read_b128 v[4:7], v8 offset:1024
	ds_read_b128 v[16:19], v8 offset:2048
	ds_read_b128 v[20:23], v8 offset:3072
	v_add_u32_e32 v8, 0x1c000, v176
	ds_read_b128 v[128:131], v8
	ds_read_b128 v[132:135], v8 offset:1024
	ds_read_b128 v[136:139], v8 offset:2048
	ds_read_b128 v[140:143], v8 offset:3072
	s_add_i32 s68, s68, s24
	s_mov_b32 m0, s31
	ds_read_b128 v[8:11], v177 offset:32768
	ds_read_b128 v[12:15], v177 offset:33792
	ds_read_b128 v[24:27], v177 offset:34816
	ds_read_b128 v[28:31], v177 offset:35840
	ds_read_b128 v[32:35], v177 offset:36864
	ds_read_b128 v[36:39], v177 offset:37888
	ds_read_b128 v[40:43], v177 offset:38912
	ds_read_b128 v[44:47], v177 offset:39936
	buffer_load_dwordx4 v170, s[36:39], s68 offen lds
	s_mov_b32 m0, s33
	s_nop 0
	buffer_load_dwordx4 v172, s[36:39], s68 offen lds
	s_waitcnt vmcnt(8)
	s_waitcnt lgkmcnt(0)
	s_barrier
	s_setprio 1
	v_mfma_f32_16x16x128_f8f6f4 v[124:127], v[0:7], v[8:15], v[124:127]
	v_mfma_f32_16x16x128_f8f6f4 v[120:123], v[16:23], v[8:15], v[120:123]
	v_mfma_f32_16x16x128_f8f6f4 v[108:111], v[0:7], v[24:31], v[108:111]
	v_mfma_f32_16x16x128_f8f6f4 v[104:107], v[16:23], v[24:31], v[104:107]
	v_mfma_f32_16x16x128_f8f6f4 v[92:95], v[0:7], v[32:39], v[186:189]
	v_mfma_f32_16x16x128_f8f6f4 v[88:91], v[16:23], v[32:39], v[190:193]
	v_mfma_f32_16x16x128_f8f6f4 v[76:79], v[0:7], v[40:47], v[210:213]
	v_mfma_f32_16x16x128_f8f6f4 v[72:75], v[16:23], v[40:47], v[214:217]
	v_mfma_f32_16x16x128_f8f6f4 v[116:119], v[128:135], v[8:15], v[116:119]
	v_mfma_f32_16x16x128_f8f6f4 v[112:115], v[136:143], v[8:15], v[112:115]
	v_mfma_f32_16x16x128_f8f6f4 v[100:103], v[128:135], v[24:31], v[100:103]
	v_mfma_f32_16x16x128_f8f6f4 v[96:99], v[136:143], v[24:31], v[96:99]
	v_mfma_f32_16x16x128_f8f6f4 v[84:87], v[128:135], v[32:39], v[160:163]
	v_mfma_f32_16x16x128_f8f6f4 v[80:83], v[136:143], v[32:39], v[164:167]
	v_mfma_f32_16x16x128_f8f6f4 v[68:71], v[128:135], v[40:47], v[178:181]
	v_mfma_f32_16x16x128_f8f6f4 v[64:67], v[136:143], v[40:47], v[182:185]
	s_setprio 0
	s_barrier
	s_mov_b32 m0, s34
	s_bitset1_b32 s55, 7
	buffer_load_dwordx4 v171, s[4:7], s55 offen lds
	s_mov_b32 m0, s35
	ds_read_b128 v[32:35], v177 offset:49152
	buffer_load_dwordx4 v173, s[4:7], s55 offen lds
	s_add_i32 s55, s55, s24
	s_mov_b32 m0, s43
	ds_read_b128 v[36:39], v177 offset:50176
	buffer_load_dwordx4 v171, s[4:7], s55 offen lds
	s_mov_b32 m0, s41
	ds_read_b128 v[144:147], v177 offset:51200
	buffer_load_dwordx4 v170, s[36:39], s54 offen lds
	s_mov_b32 m0, s42
	ds_read_b128 v[148:151], v177 offset:52224
	buffer_load_dwordx4 v172, s[36:39], s54 offen lds
	ds_read_b128 v[152:155], v177 offset:53248
	ds_read_b128 v[156:159], v177 offset:54272
	ds_read_b128 v[160:163], v177 offset:55296
	ds_read_b128 v[164:167], v177 offset:56320
	s_waitcnt vmcnt(7)
	s_waitcnt lgkmcnt(0)
	s_barrier
	s_setprio 1
	v_mfma_f32_16x16x128_f8f6f4 v[60:63], v[0:7], v[32:39], v[60:63]
	v_mfma_f32_16x16x128_f8f6f4 v[56:59], v[16:23], v[32:39], v[56:59]
	v_mfma_f32_16x16x128_f8f6f4 v[44:47], v[0:7], v[144:151], v[194:197]
	v_mfma_f32_16x16x128_f8f6f4 v[40:43], v[16:23], v[144:151], v[198:201]
	v_mfma_f32_16x16x128_f8f6f4 v[28:31], v[0:7], v[152:159], v[202:205]
	v_mfma_f32_16x16x128_f8f6f4 v[24:27], v[16:23], v[152:159], v[206:209]
	v_mfma_f32_16x16x128_f8f6f4 v[12:15], v[0:7], v[160:167], v[218:221]
	v_mfma_f32_16x16x128_f8f6f4 v[8:11], v[16:23], v[160:167], v[226:229]
	v_mfma_f32_16x16x128_f8f6f4 v[52:55], v[128:135], v[32:39], v[52:55]
	v_mfma_f32_16x16x128_f8f6f4 v[48:51], v[136:143], v[32:39], v[48:51]
	v_mfma_f32_16x16x128_f8f6f4 v[36:39], v[128:135], v[144:151], v[230:233]
	v_mfma_f32_16x16x128_f8f6f4 v[32:35], v[136:143], v[144:151], v[234:237]
	v_mfma_f32_16x16x128_f8f6f4 v[20:23], v[128:135], v[152:159], v[238:241]
	v_mfma_f32_16x16x128_f8f6f4 v[16:19], v[136:143], v[152:159], v[242:245]
	v_mfma_f32_16x16x128_f8f6f4 v[4:7], v[128:135], v[160:167], v[246:249]
	v_mfma_f32_16x16x128_f8f6f4 v[0:3], v[136:143], v[160:167], v[250:253]
	s_setprio 0
	s_barrier
	s_add_i32 s67, s67, 2
	s_addk_i32 s65, 0x100
	s_addk_i32 s66, 0x100
	s_cmp_ge_i32 s67, s47
	s_cbranch_scc0 .LBB0_1854
	s_mov_b32 m0, s44
	s_nop 0
	buffer_load_dwordx4 v173, s[4:7], s55 offen lds

; #define PG8_STAGE(bufoff, rs_, soff_, voff) do { _Pragma("unroll") for (int _i = 0; _i < 2; ++_i) \
;         __builtin_amdgcn_raw_ptr_buffer_load_lds(rs_, (LAS void*)(lds + (bufoff) + ldsw + _i * 8192), 16, (int)(voff)[_i], (int)(soff_), 0, 0); } while (0)
; #define PG8_LDA(dst, b, h) do { _Pragma("unroll") for (int m = 0; m < 4; ++m) dst[m] = PG8_LD2(lds + PG8_SA(b, h) + aoff + m * 2048); } while (0)
; #define PG8_LDB(dst, b, h) do { _Pragma("unroll") for (int n = 0; n < 2; ++n) dst[n] = PG8_LD2(lds + PG8_SB(b, h) + boff + n * 2048); } while (0)
; #define PG8_WAIT_V(n) asm volatile("s_waitcnt vmcnt(" #n ")" ::: "memory")
; #define PG8_WAIT_L(n) asm volatile("s_waitcnt lgkmcnt(" #n ")" ::: "memory")
; #define PG8_BAR __builtin_amdgcn_s_barrier()
; #define PG8_SCHED __builtin_amdgcn_sched_barrier(0)
; template <class Epi, class Sched, bool ALIGN_EPI = false, bool SP2 = false, bool FP8 = false>
; __device__ __forceinline__ void gemm_phase(LAS unsigned char* lds, const Gemm g, const Sched& S, const Epi& E, int wbase) {
;     ...
;         for (int t = 0; t < nt; t += 2) {
;             const bool last = (t == nt - 2);
;             const unsigned a1 = cA + (unsigned)(t + 1) * kstep;
;             const unsigned a2 = last ? nA : cA + (unsigned)(t + 2) * kstep, b2 = last ? nB : cB + (unsigned)(t + 2) * kstep; const rsrc_t rA2 = (Sched::TWO && last) ? rAn : rAc, rB2 = (Sched::TWO && last) ? rBn : rBc;
;             const unsigned a3 = a2 + kstep, b3 = b2 + kstep;
;             if (last && has_next) S.a_ready(nxt);
;             if constexpr (SP2) {
;             PG8_LDB(B0, 0, 0); PG8_LDB(B1, 0, 1); PG8_SCHED; PG8_LDA(At, 0, 0); PG8_STAGE(PG8_SA(1, 1), rAc, a1 + hstep, voffA);
;             PG8_WAIT_V(8); PG8_WAIT_L(0); PG8_BAR; PG8_MMA(0, 0, At, B0); PG8_MMA(0, 1, At, B1); PG8_BAR; PG8_SCHED;
;             PG8_LDA(At, 0, 1); PG8_STAGE(PG8_SB(0, 0), rB2, b2, voffB); PG8_STAGE(PG8_SB(0, 1), rB2, b2 + hstep, voffB); PG8_STAGE(PG8_SA(0, 0), rA2, a2, voffA);
;             PG8_WAIT_V(8); PG8_WAIT_L(0); PG8_BAR; PG8_MMA(1, 0, At, B0); PG8_MMA(1, 1, At, B1); PG8_BAR; PG8_SCHED;
.LBB0_1944:
	s_mov_b32 m0, s57
	s_nop 0
	buffer_load_dwordx4 v171, s[4:7], s55 offen lds
	v_add_u32_e32 v136, 0x10000, v174
	v_add_u32_e32 v156, 0x14000, v174
	ds_read_b128 v[120:123], v136
	ds_read_b128 v[124:127], v136 offset:1024
	ds_read_b128 v[132:135], v136 offset:2048
	ds_read_b128 v[136:139], v136 offset:3072
	ds_read_b128 v[144:147], v156
	ds_read_b128 v[148:151], v156 offset:1024
	ds_read_b128 v[152:155], v156 offset:2048
	ds_read_b128 v[156:159], v156 offset:3072
	s_add_i32 s6, s61, 0x80
	s_cmp_eq_u32 s77, s63
	s_cselect_b32 s66, s29, s6
	s_cselect_b32 s55, s60, s62
	s_or_b32 s54, s66, 0x80
	s_add_i32 s6, s33, s61
	s_mov_b32 m0, s79
	ds_read_b128 v[160:163], v175
	ds_read_b128 v[164:167], v175 offset:1024
	ds_read_b128 v[176:179], v175 offset:2048
	ds_read_b128 v[180:183], v175 offset:3072
	ds_read_b128 v[184:187], v175 offset:4096
	ds_read_b128 v[188:191], v175 offset:5120
	ds_read_b128 v[192:195], v175 offset:6144
	ds_read_b128 v[196:199], v175 offset:7168
	buffer_load_dwordx4 v168, s[36:39], s6 offen lds
	s_mov_b32 m0, s82
	s_nop 0
	buffer_load_dwordx4 v170, s[36:39], s6 offen lds
	s_waitcnt vmcnt(8)
	s_waitcnt lgkmcnt(0)
	s_barrier
	s_setprio 1
	v_mfma_f32_16x16x32_bf16 v[140:143], v[120:123], v[160:163], v[140:143]
	v_mfma_f32_16x16x32_bf16 v[128:131], v[132:135], v[160:163], v[128:131]
	v_mfma_f32_16x16x32_bf16 v[108:111], v[120:123], v[176:179], v[108:111]
	v_mfma_f32_16x16x32_bf16 v[104:107], v[132:135], v[176:179], v[104:107]
	v_mfma_f32_16x16x32_bf16 v[92:95], v[120:123], v[184:187], v[92:95]
	v_mfma_f32_16x16x32_bf16 v[88:91], v[132:135], v[184:187], v[88:91]
	v_mfma_f32_16x16x32_bf16 v[76:79], v[120:123], v[192:195], v[76:79]
	v_mfma_f32_16x16x32_bf16 v[72:75], v[132:135], v[192:195], v[72:75]
	v_mfma_f32_16x16x32_bf16 v[140:143], v[124:127], v[164:167], v[140:143]
	v_mfma_f32_16x16x32_bf16 v[128:131], v[136:139], v[164:167], v[128:131]
	v_mfma_f32_16x16x32_bf16 v[108:111], v[124:127], v[180:183], v[108:111]
	v_mfma_f32_16x16x32_bf16 v[104:107], v[136:139], v[180:183], v[104:107]
	v_mfma_f32_16x16x32_bf16 v[92:95], v[124:127], v[188:191], v[92:95]
	v_mfma_f32_16x16x32_bf16 v[88:91], v[136:139], v[188:191], v[88:91]
	v_mfma_f32_16x16x32_bf16 v[76:79], v[124:127], v[196:199], v[76:79]
	v_mfma_f32_16x16x32_bf16 v[72:75], v[136:139], v[196:199], v[72:75]
	v_mfma_f32_16x16x32_bf16 v[116:119], v[144:147], v[160:163], v[116:119]
	v_mfma_f32_16x16x32_bf16 v[112:115], v[152:155], v[160:163], v[112:115]
	v_mfma_f32_16x16x32_bf16 v[100:103], v[144:147], v[176:179], v[100:103]
	v_mfma_f32_16x16x32_bf16 v[96:99], v[152:155], v[176:179], v[96:99]
	v_mfma_f32_16x16x32_bf16 v[84:87], v[144:147], v[184:187], v[84:87]
	v_mfma_f32_16x16x32_bf16 v[80:83], v[152:155], v[184:187], v[80:83]
	v_mfma_f32_16x16x32_bf16 v[68:71], v[144:147], v[192:195], v[68:71]
	v_mfma_f32_16x16x32_bf16 v[64:67], v[152:155], v[192:195], v[64:67]
	v_mfma_f32_16x16x32_bf16 v[116:119], v[148:151], v[164:167], v[116:119]
	v_mfma_f32_16x16x32_bf16 v[112:115], v[156:159], v[164:167], v[112:115]
	v_mfma_f32_16x16x32_bf16 v[100:103], v[148:151], v[180:183], v[100:103]
	v_mfma_f32_16x16x32_bf16 v[96:99], v[156:159], v[180:183], v[96:99]
	v_mfma_f32_16x16x32_bf16 v[84:87], v[148:151], v[188:191], v[84:87]
	v_mfma_f32_16x16x32_bf16 v[80:83], v[156:159], v[188:191], v[80:83]
	v_mfma_f32_16x16x32_bf16 v[68:71], v[148:151], v[196:199], v[68:71]
	v_mfma_f32_16x16x32_bf16 v[64:67], v[156:159], v[196:199], v[64:67]
	s_setprio 0
	s_barrier
	s_mov_b32 m0, s35
	s_mov_b32 s6, s38
	s_mov_b32 s7, s39
	buffer_load_dwordx4 v169, s[4:7], s55 offen lds
	s_mov_b32 m0, s41
	ds_read_b128 v[160:163], v175 offset:16384
	s_add_i32 s67, s55, s33
	buffer_load_dwordx4 v171, s[4:7], s55 offen lds
	s_mov_b32 m0, s42
	ds_read_b128 v[164:167], v175 offset:17408
	buffer_load_dwordx4 v169, s[4:7], s67 offen lds
	s_mov_b32 m0, s34
	ds_read_b128 v[176:179], v175 offset:18432
	buffer_load_dwordx4 v168, s[36:39], s66 offen lds
	s_mov_b32 m0, s44
	ds_read_b128 v[180:183], v175 offset:19456
	buffer_load_dwordx4 v170, s[36:39], s66 offen lds
	ds_read_b128 v[184:187], v175 offset:20480
	ds_read_b128 v[188:191], v175 offset:21504
	ds_read_b128 v[192:195], v175 offset:22528
	ds_read_b128 v[196:199], v175 offset:23552
	s_waitcnt vmcnt(7)
	s_waitcnt lgkmcnt(0)
	s_barrier
	s_setprio 1
	v_mfma_f32_16x16x32_bf16 v[60:63], v[120:123], v[160:163], v[60:63]
	v_mfma_f32_16x16x32_bf16 v[56:59], v[132:135], v[160:163], v[56:59]
	v_mfma_f32_16x16x32_bf16 v[44:47], v[120:123], v[176:179], v[44:47]
	v_mfma_f32_16x16x32_bf16 v[40:43], v[132:135], v[176:179], v[40:43]
	v_mfma_f32_16x16x32_bf16 v[28:31], v[120:123], v[184:187], v[28:31]
	v_mfma_f32_16x16x32_bf16 v[24:27], v[132:135], v[184:187], v[24:27]
	v_mfma_f32_16x16x32_bf16 v[12:15], v[120:123], v[192:195], v[12:15]
	v_mfma_f32_16x16x32_bf16 v[8:11], v[132:135], v[192:195], v[8:11]
	v_mfma_f32_16x16x32_bf16 v[60:63], v[124:127], v[164:167], v[60:63]
	v_mfma_f32_16x16x32_bf16 v[56:59], v[136:139], v[164:167], v[56:59]
	v_mfma_f32_16x16x32_bf16 v[44:47], v[124:127], v[180:183], v[44:47]
	v_mfma_f32_16x16x32_bf16 v[40:43], v[136:139], v[180:183], v[40:43]
	v_mfma_f32_16x16x32_bf16 v[28:31], v[124:127], v[188:191], v[28:31]
	v_mfma_f32_16x16x32_bf16 v[24:27], v[136:139], v[188:191], v[24:27]
	v_mfma_f32_16x16x32_bf16 v[12:15], v[124:127], v[196:199], v[12:15]
	v_mfma_f32_16x16x32_bf16 v[8:11], v[136:139], v[196:199], v[8:11]
	v_mfma_f32_16x16x32_bf16 v[52:55], v[144:147], v[160:163], v[52:55]
	v_mfma_f32_16x16x32_bf16 v[48:51], v[152:155], v[160:163], v[48:51]
	v_mfma_f32_16x16x32_bf16 v[36:39], v[144:147], v[176:179], v[36:39]
	v_mfma_f32_16x16x32_bf16 v[32:35], v[152:155], v[176:179], v[32:35]
	v_mfma_f32_16x16x32_bf16 v[20:23], v[144:147], v[184:187], v[20:23]
	v_mfma_f32_16x16x32_bf16 v[16:19], v[152:155], v[184:187], v[16:19]
	v_mfma_f32_16x16x32_bf16 v[4:7], v[144:147], v[192:195], v[4:7]
	v_mfma_f32_16x16x32_bf16 v[0:3], v[152:155], v[192:195], v[0:3]
	v_mfma_f32_16x16x32_bf16 v[52:55], v[148:151], v[164:167], v[52:55]
	v_mfma_f32_16x16x32_bf16 v[48:51], v[156:159], v[164:167], v[48:51]
	v_mfma_f32_16x16x32_bf16 v[36:39], v[148:151], v[180:183], v[36:39]
	v_mfma_f32_16x16x32_bf16 v[32:35], v[156:159], v[180:183], v[32:35]
	v_mfma_f32_16x16x32_bf16 v[20:23], v[148:151], v[188:191], v[20:23]
	v_mfma_f32_16x16x32_bf16 v[16:19], v[156:159], v[188:191], v[16:19]
	v_mfma_f32_16x16x32_bf16 v[4:7], v[148:151], v[196:199], v[4:7]
	v_mfma_f32_16x16x32_bf16 v[0:3], v[156:159], v[196:199], v[0:3]
	s_setprio 0
	s_barrier
; #define PG8_STAGE(bufoff, rs_, soff_, voff) do { _Pragma("unroll") for (int _i = 0; _i < 2; ++_i) \
;         __builtin_amdgcn_raw_ptr_buffer_load_lds(rs_, (LAS void*)(lds + (bufoff) + ldsw + _i * 8192), 16, (int)(voff)[_i], (int)(soff_), 0, 0); } while (0)
; #define PG8_LDA(dst, b, h) do { _Pragma("unroll") for (int m = 0; m < 4; ++m) dst[m] = PG8_LD2(lds + PG8_SA(b, h) + aoff + m * 2048); } while (0)
; #define PG8_LDB(dst, b, h) do { _Pragma("unroll") for (int n = 0; n < 2; ++n) dst[n] = PG8_LD2(lds + PG8_SB(b, h) + boff + n * 2048); } while (0)
; #define PG8_WAIT_V(n) asm volatile("s_waitcnt vmcnt(" #n ")" ::: "memory")
; #define PG8_WAIT_L(n) asm volatile("s_waitcnt lgkmcnt(" #n ")" ::: "memory")
; #define PG8_BAR __builtin_amdgcn_s_barrier()
; #define PG8_SCHED __builtin_amdgcn_sched_barrier(0)
; template <class Epi, class Sched, bool ALIGN_EPI = false, bool SP2 = false, bool FP8 = false>
; __device__ __forceinline__ void gemm_phase(LAS unsigned char* lds, const Gemm g, const Sched& S, const Epi& E, int wbase) {
;     ...
;         for (int t = 0; t < nt; t += 2) {
;             const bool last = (t == nt - 2);
;     ...
;             PG8_LDB(B0, 1, 0); PG8_LDB(B1, 1, 1); PG8_SCHED; PG8_LDA(At, 1, 0); PG8_STAGE(PG8_SA(0, 1), rA2, a2 + hstep, voffA);
;             PG8_WAIT_V(8); PG8_WAIT_L(0); PG8_BAR; PG8_MMA(0, 0, At, B0); PG8_MMA(0, 1, At, B1); PG8_BAR; PG8_SCHED;
;             PG8_LDA(At, 1, 1); PG8_STAGE(PG8_SB(1, 0), rB2, b3, voffB); PG8_STAGE(PG8_SB(1, 1), rB2, b3 + hstep, voffB); PG8_STAGE(PG8_SA(1, 0), rA2, a3, voffA);
;             PG8_WAIT_V(8); PG8_WAIT_L(0); PG8_BAR; PG8_MMA(1, 0, At, B0); PG8_MMA(1, 1, At, B1); PG8_BAR; PG8_SCHED;
	s_mov_b32 m0, s43
	s_nop 0
	buffer_load_dwordx4 v171, s[4:7], s67 offen lds
	v_add_u32_e32 v136, 0x18000, v174
	v_add_u32_e32 v156, 0x1c000, v174
	ds_read_b128 v[120:123], v136
	ds_read_b128 v[124:127], v136 offset:1024
	ds_read_b128 v[132:135], v136 offset:2048
	ds_read_b128 v[136:139], v136 offset:3072
	ds_read_b128 v[144:147], v156
	ds_read_b128 v[148:151], v156 offset:1024
	ds_read_b128 v[152:155], v156 offset:2048
	ds_read_b128 v[156:159], v156 offset:3072
	s_add_i32 s66, s66, s33
	s_mov_b32 m0, s45
	ds_read_b128 v[160:163], v175 offset:32768
	ds_read_b128 v[164:167], v175 offset:33792
	ds_read_b128 v[176:179], v175 offset:34816
	ds_read_b128 v[180:183], v175 offset:35840
	ds_read_b128 v[184:187], v175 offset:36864
	ds_read_b128 v[188:191], v175 offset:37888
	ds_read_b128 v[192:195], v175 offset:38912
	ds_read_b128 v[196:199], v175 offset:39936
	buffer_load_dwordx4 v168, s[36:39], s66 offen lds
	s_mov_b32 m0, s46
	s_nop 0
	buffer_load_dwordx4 v170, s[36:39], s66 offen lds
	s_waitcnt vmcnt(8)
	s_waitcnt lgkmcnt(0)
	s_barrier
	s_setprio 1
	v_mfma_f32_16x16x32_bf16 v[140:143], v[120:123], v[160:163], v[140:143]
	v_mfma_f32_16x16x32_bf16 v[128:131], v[132:135], v[160:163], v[128:131]
	v_mfma_f32_16x16x32_bf16 v[108:111], v[120:123], v[176:179], v[108:111]
	v_mfma_f32_16x16x32_bf16 v[104:107], v[132:135], v[176:179], v[104:107]
	v_mfma_f32_16x16x32_bf16 v[92:95], v[120:123], v[184:187], v[92:95]
	v_mfma_f32_16x16x32_bf16 v[88:91], v[132:135], v[184:187], v[88:91]
	v_mfma_f32_16x16x32_bf16 v[76:79], v[120:123], v[192:195], v[76:79]
	v_mfma_f32_16x16x32_bf16 v[72:75], v[132:135], v[192:195], v[72:75]
	v_mfma_f32_16x16x32_bf16 v[140:143], v[124:127], v[164:167], v[140:143]
	v_mfma_f32_16x16x32_bf16 v[128:131], v[136:139], v[164:167], v[128:131]
	v_mfma_f32_16x16x32_bf16 v[108:111], v[124:127], v[180:183], v[108:111]
	v_mfma_f32_16x16x32_bf16 v[104:107], v[136:139], v[180:183], v[104:107]
	v_mfma_f32_16x16x32_bf16 v[92:95], v[124:127], v[188:191], v[92:95]
	v_mfma_f32_16x16x32_bf16 v[88:91], v[136:139], v[188:191], v[88:91]
	v_mfma_f32_16x16x32_bf16 v[76:79], v[124:127], v[196:199], v[76:79]
	v_mfma_f32_16x16x32_bf16 v[72:75], v[136:139], v[196:199], v[72:75]
	v_mfma_f32_16x16x32_bf16 v[116:119], v[144:147], v[160:163], v[116:119]
	v_mfma_f32_16x16x32_bf16 v[112:115], v[152:155], v[160:163], v[112:115]
	v_mfma_f32_16x16x32_bf16 v[100:103], v[144:147], v[176:179], v[100:103]
	v_mfma_f32_16x16x32_bf16 v[96:99], v[152:155], v[176:179], v[96:99]
	v_mfma_f32_16x16x32_bf16 v[84:87], v[144:147], v[184:187], v[84:87]
	v_mfma_f32_16x16x32_bf16 v[80:83], v[152:155], v[184:187], v[80:83]
	v_mfma_f32_16x16x32_bf16 v[68:71], v[144:147], v[192:195], v[68:71]
	v_mfma_f32_16x16x32_bf16 v[64:67], v[152:155], v[192:195], v[64:67]
	v_mfma_f32_16x16x32_bf16 v[116:119], v[148:151], v[164:167], v[116:119]
	v_mfma_f32_16x16x32_bf16 v[112:115], v[156:159], v[164:167], v[112:115]
	v_mfma_f32_16x16x32_bf16 v[100:103], v[148:151], v[180:183], v[100:103]
	v_mfma_f32_16x16x32_bf16 v[96:99], v[156:159], v[180:183], v[96:99]
	v_mfma_f32_16x16x32_bf16 v[84:87], v[148:151], v[188:191], v[84:87]
	v_mfma_f32_16x16x32_bf16 v[80:83], v[156:159], v[188:191], v[80:83]
	v_mfma_f32_16x16x32_bf16 v[68:71], v[148:151], v[196:199], v[68:71]
	v_mfma_f32_16x16x32_bf16 v[64:67], v[156:159], v[196:199], v[64:67]
	s_setprio 0
	s_barrier
	s_mov_b32 m0, s47
	s_bitset1_b32 s55, 7
	buffer_load_dwordx4 v169, s[4:7], s55 offen lds
	s_mov_b32 m0, s48
	ds_read_b128 v[160:163], v175 offset:49152
	buffer_load_dwordx4 v171, s[4:7], s55 offen lds
	s_add_i32 s55, s55, s33
	s_mov_b32 m0, s56
	ds_read_b128 v[164:167], v175 offset:50176
	buffer_load_dwordx4 v169, s[4:7], s55 offen lds
	s_mov_b32 m0, s52
	ds_read_b128 v[176:179], v175 offset:51200
	buffer_load_dwordx4 v168, s[36:39], s54 offen lds
	s_mov_b32 m0, s53
	ds_read_b128 v[180:183], v175 offset:52224
	buffer_load_dwordx4 v170, s[36:39], s54 offen lds
	ds_read_b128 v[184:187], v175 offset:53248
	ds_read_b128 v[188:191], v175 offset:54272
	ds_read_b128 v[192:195], v175 offset:55296
	ds_read_b128 v[196:199], v175 offset:56320
	s_waitcnt vmcnt(7)
	s_waitcnt lgkmcnt(0)
	s_barrier
	s_setprio 1
	v_mfma_f32_16x16x32_bf16 v[60:63], v[120:123], v[160:163], v[60:63]
	v_mfma_f32_16x16x32_bf16 v[56:59], v[132:135], v[160:163], v[56:59]
	v_mfma_f32_16x16x32_bf16 v[44:47], v[120:123], v[176:179], v[44:47]
	v_mfma_f32_16x16x32_bf16 v[40:43], v[132:135], v[176:179], v[40:43]
	v_mfma_f32_16x16x32_bf16 v[28:31], v[120:123], v[184:187], v[28:31]
	v_mfma_f32_16x16x32_bf16 v[24:27], v[132:135], v[184:187], v[24:27]
	v_mfma_f32_16x16x32_bf16 v[12:15], v[120:123], v[192:195], v[12:15]
	v_mfma_f32_16x16x32_bf16 v[8:11], v[132:135], v[192:195], v[8:11]
	v_mfma_f32_16x16x32_bf16 v[60:63], v[124:127], v[164:167], v[60:63]
	v_mfma_f32_16x16x32_bf16 v[56:59], v[136:139], v[164:167], v[56:59]
	v_mfma_f32_16x16x32_bf16 v[44:47], v[124:127], v[180:183], v[44:47]
	v_mfma_f32_16x16x32_bf16 v[40:43], v[136:139], v[180:183], v[40:43]
	v_mfma_f32_16x16x32_bf16 v[28:31], v[124:127], v[188:191], v[28:31]
	v_mfma_f32_16x16x32_bf16 v[24:27], v[136:139], v[188:191], v[24:27]
	v_mfma_f32_16x16x32_bf16 v[12:15], v[124:127], v[196:199], v[12:15]
	v_mfma_f32_16x16x32_bf16 v[8:11], v[136:139], v[196:199], v[8:11]
	v_mfma_f32_16x16x32_bf16 v[52:55], v[144:147], v[160:163], v[52:55]
	v_mfma_f32_16x16x32_bf16 v[48:51], v[152:155], v[160:163], v[48:51]
	v_mfma_f32_16x16x32_bf16 v[36:39], v[144:147], v[176:179], v[36:39]
	v_mfma_f32_16x16x32_bf16 v[32:35], v[152:155], v[176:179], v[32:35]
	v_mfma_f32_16x16x32_bf16 v[20:23], v[144:147], v[184:187], v[20:23]
	v_mfma_f32_16x16x32_bf16 v[16:19], v[152:155], v[184:187], v[16:19]
	v_mfma_f32_16x16x32_bf16 v[4:7], v[144:147], v[192:195], v[4:7]
	v_mfma_f32_16x16x32_bf16 v[0:3], v[152:155], v[192:195], v[0:3]
	v_mfma_f32_16x16x32_bf16 v[52:55], v[148:151], v[164:167], v[52:55]
	v_mfma_f32_16x16x32_bf16 v[48:51], v[156:159], v[164:167], v[48:51]
	v_mfma_f32_16x16x32_bf16 v[36:39], v[148:151], v[180:183], v[36:39]
	v_mfma_f32_16x16x32_bf16 v[32:35], v[156:159], v[180:183], v[32:35]
	v_mfma_f32_16x16x32_bf16 v[20:23], v[148:151], v[188:191], v[20:23]
	v_mfma_f32_16x16x32_bf16 v[16:19], v[156:159], v[188:191], v[16:19]
	v_mfma_f32_16x16x32_bf16 v[4:7], v[148:151], v[196:199], v[4:7]
	v_mfma_f32_16x16x32_bf16 v[0:3], v[156:159], v[196:199], v[0:3]
	s_setprio 0
	s_barrier
	s_add_i32 s63, s63, 2
	s_addk_i32 s61, 0x100
	s_addk_i32 s62, 0x100
	s_cmp_ge_i32 s63, s65
	s_cbranch_scc0 .LBB0_1944
	s_mov_b32 m0, s57
	s_nop 0
	buffer_load_dwordx4 v171, s[4:7], s55 offen lds

; #define PG8_STAGE(bufoff, rs_, soff_, voff) do { _Pragma("unroll") for (int _i = 0; _i < 2; ++_i) \
;         __builtin_amdgcn_raw_ptr_buffer_load_lds(rs_, (LAS void*)(lds + (bufoff) + ldsw + _i * 8192), 16, (int)(voff)[_i], (int)(soff_), 0, 0); } while (0)
; #define PG8_LDA(dst, b, h) do { _Pragma("unroll") for (int m = 0; m < 4; ++m) dst[m] = PG8_LD2(lds + PG8_SA(b, h) + aoff + m * 2048); } while (0)
; #define PG8_LDB(dst, b, h) do { _Pragma("unroll") for (int n = 0; n < 2; ++n) dst[n] = PG8_LD2(lds + PG8_SB(b, h) + boff + n * 2048); } while (0)
; #define PG8_WAIT_V(n) asm volatile("s_waitcnt vmcnt(" #n ")" ::: "memory")
; #define PG8_WAIT_L(n) asm volatile("s_waitcnt lgkmcnt(" #n ")" ::: "memory")
; #define PG8_BAR __builtin_amdgcn_s_barrier()
; #define PG8_SCHED __builtin_amdgcn_sched_barrier(0)
; template <class Epi, class Sched, bool ALIGN_EPI = false, bool SP2 = false, bool FP8 = false>
; __device__ __forceinline__ void gemm_phase(LAS unsigned char* lds, const Gemm g, const Sched& S, const Epi& E, int wbase) {
;     ...
;         for (int t = 0; t < nt; t += 2) {
;             const bool last = (t == nt - 2);
;             const unsigned a1 = cA + (unsigned)(t + 1) * kstep;
;             const unsigned a2 = last ? nA : cA + (unsigned)(t + 2) * kstep, b2 = last ? nB : cB + (unsigned)(t + 2) * kstep; const rsrc_t rA2 = (Sched::TWO && last) ? rAn : rAc, rB2 = (Sched::TWO && last) ? rBn : rBc;
;             const unsigned a3 = a2 + kstep, b3 = b2 + kstep;
;             if (last && has_next) S.a_ready(nxt);
;             if constexpr (SP2) {
;             PG8_LDB(B0, 0, 0); PG8_LDB(B1, 0, 1); PG8_SCHED; PG8_LDA(At, 0, 0); PG8_STAGE(PG8_SA(1, 1), rAc, a1 + hstep, voffA);
;             PG8_WAIT_V(8); PG8_WAIT_L(0); PG8_BAR; PG8_MMA(0, 0, At, B0); PG8_MMA(0, 1, At, B1); PG8_BAR; PG8_SCHED;
;             PG8_LDA(At, 0, 1); PG8_STAGE(PG8_SB(0, 0), rB2, b2, voffB); PG8_STAGE(PG8_SB(0, 1), rB2, b2 + hstep, voffB); PG8_STAGE(PG8_SA(0, 0), rA2, a2, voffA);
;             PG8_WAIT_V(8); PG8_WAIT_L(0); PG8_BAR; PG8_MMA(1, 0, At, B0); PG8_MMA(1, 1, At, B1); PG8_BAR; PG8_SCHED;
.LBB0_1990:
	s_mov_b32 m0, s76
	s_nop 0
	buffer_load_dwordx4 v177, s[12:15], s55 offen lds
	v_add_u32_e32 v136, 0x10000, v180
	v_add_u32_e32 v156, 0x14000, v180
	ds_read_b128 v[120:123], v136
	ds_read_b128 v[124:127], v136 offset:1024
	ds_read_b128 v[132:135], v136 offset:2048
	ds_read_b128 v[136:139], v136 offset:3072
	ds_read_b128 v[144:147], v156
	ds_read_b128 v[148:151], v156 offset:1024
	ds_read_b128 v[152:155], v156 offset:2048
	ds_read_b128 v[156:159], v156 offset:3072
	s_add_i32 s14, s4, 0x80
	s_cmp_eq_u32 s84, s61
	s_cselect_b32 s62, s2, s14
	s_cselect_b32 s55, s3, s5
	s_or_b32 s54, s62, 0x80
	s_add_i32 s14, s42, s4
	s_mov_b32 m0, s85
	ds_read_b128 v[160:163], v181
	ds_read_b128 v[164:167], v181 offset:1024
	ds_read_b128 v[182:185], v181 offset:2048
	ds_read_b128 v[186:189], v181 offset:3072
	ds_read_b128 v[194:197], v181 offset:4096
	ds_read_b128 v[198:201], v181 offset:5120
	ds_read_b128 v[202:205], v181 offset:6144
	ds_read_b128 v[206:209], v181 offset:7168
	buffer_load_dwordx4 v174, s[36:39], s14 offen lds
	s_mov_b32 m0, s8
	s_nop 0
	buffer_load_dwordx4 v176, s[36:39], s14 offen lds
	s_waitcnt vmcnt(8)
	s_waitcnt lgkmcnt(0)
	s_barrier
	s_setprio 1
	v_mfma_f32_16x16x128_f8f6f4 v[140:143], v[120:127], v[160:167], v[140:143]
	v_mfma_f32_16x16x128_f8f6f4 v[128:131], v[132:139], v[160:167], v[128:131]
	v_mfma_f32_16x16x128_f8f6f4 v[108:111], v[120:127], v[182:189], v[108:111]
	v_mfma_f32_16x16x128_f8f6f4 v[104:107], v[132:139], v[182:189], v[104:107]
	v_mfma_f32_16x16x128_f8f6f4 v[168:171], v[120:127], v[194:201], v[92:95]
	v_mfma_f32_16x16x128_f8f6f4 v[190:193], v[132:139], v[194:201], v[88:91]
	v_mfma_f32_16x16x128_f8f6f4 v[210:213], v[120:127], v[202:209], v[76:79]
	v_mfma_f32_16x16x128_f8f6f4 v[214:217], v[132:139], v[202:209], v[72:75]
	v_mfma_f32_16x16x128_f8f6f4 v[116:119], v[144:151], v[160:167], v[116:119]
	v_mfma_f32_16x16x128_f8f6f4 v[112:115], v[152:159], v[160:167], v[112:115]
	v_mfma_f32_16x16x128_f8f6f4 v[100:103], v[144:151], v[182:189], v[100:103]
	v_mfma_f32_16x16x128_f8f6f4 v[96:99], v[152:159], v[182:189], v[96:99]
	v_mfma_f32_16x16x128_f8f6f4 v[160:163], v[144:151], v[194:201], v[84:87]
	v_mfma_f32_16x16x128_f8f6f4 v[164:167], v[152:159], v[194:201], v[80:83]
	v_mfma_f32_16x16x128_f8f6f4 v[182:185], v[144:151], v[202:209], v[68:71]
	v_mfma_f32_16x16x128_f8f6f4 v[186:189], v[152:159], v[202:209], v[64:67]
	s_setprio 0
	s_barrier
	s_mov_b32 m0, s44
	s_mov_b32 s14, s38
	s_mov_b32 s15, s39
	s_nop 1
	buffer_load_dwordx4 v175, s[12:15], s55 offen lds
	s_mov_b32 m0, s45
	ds_read_b128 v[64:67], v181 offset:16384
	s_add_i32 s63, s55, s42
	buffer_load_dwordx4 v177, s[12:15], s55 offen lds
	s_mov_b32 m0, s46
	ds_read_b128 v[68:71], v181 offset:17408
	buffer_load_dwordx4 v175, s[12:15], s63 offen lds
	s_mov_b32 m0, s43
	ds_read_b128 v[72:75], v181 offset:18432
	buffer_load_dwordx4 v174, s[36:39], s62 offen lds
	s_mov_b32 m0, s48
	ds_read_b128 v[76:79], v181 offset:19456
	buffer_load_dwordx4 v176, s[36:39], s62 offen lds
	ds_read_b128 v[80:83], v181 offset:20480
	ds_read_b128 v[84:87], v181 offset:21504
	ds_read_b128 v[88:91], v181 offset:22528
	ds_read_b128 v[92:95], v181 offset:23552
	s_waitcnt vmcnt(7)
	s_waitcnt lgkmcnt(0)
	s_barrier
	s_setprio 1
	v_mfma_f32_16x16x128_f8f6f4 v[60:63], v[120:127], v[64:71], v[60:63]
	v_mfma_f32_16x16x128_f8f6f4 v[56:59], v[132:139], v[64:71], v[56:59]
	v_mfma_f32_16x16x128_f8f6f4 v[194:197], v[120:127], v[72:79], v[44:47]
	v_mfma_f32_16x16x128_f8f6f4 v[198:201], v[132:139], v[72:79], v[40:43]
	v_mfma_f32_16x16x128_f8f6f4 v[202:205], v[120:127], v[80:87], v[28:31]
	v_mfma_f32_16x16x128_f8f6f4 v[206:209], v[132:139], v[80:87], v[24:27]
	v_mfma_f32_16x16x128_f8f6f4 v[218:221], v[120:127], v[88:95], v[12:15]
	v_mfma_f32_16x16x128_f8f6f4 v[226:229], v[132:139], v[88:95], v[8:11]
	v_mfma_f32_16x16x128_f8f6f4 v[52:55], v[144:151], v[64:71], v[52:55]
	v_mfma_f32_16x16x128_f8f6f4 v[48:51], v[152:159], v[64:71], v[48:51]
	v_mfma_f32_16x16x128_f8f6f4 v[230:233], v[144:151], v[72:79], v[36:39]
	v_mfma_f32_16x16x128_f8f6f4 v[234:237], v[152:159], v[72:79], v[32:35]
	v_mfma_f32_16x16x128_f8f6f4 v[238:241], v[144:151], v[80:87], v[20:23]
	v_mfma_f32_16x16x128_f8f6f4 v[242:245], v[152:159], v[80:87], v[16:19]
	v_mfma_f32_16x16x128_f8f6f4 v[246:249], v[144:151], v[88:95], v[4:7]
	v_mfma_f32_16x16x128_f8f6f4 v[250:253], v[152:159], v[88:95], v[0:3]
	s_setprio 0
	s_barrier
; #define PG8_STAGE(bufoff, rs_, soff_, voff) do { _Pragma("unroll") for (int _i = 0; _i < 2; ++_i) \
;         __builtin_amdgcn_raw_ptr_buffer_load_lds(rs_, (LAS void*)(lds + (bufoff) + ldsw + _i * 8192), 16, (int)(voff)[_i], (int)(soff_), 0, 0); } while (0)
; #define PG8_LDA(dst, b, h) do { _Pragma("unroll") for (int m = 0; m < 4; ++m) dst[m] = PG8_LD2(lds + PG8_SA(b, h) + aoff + m * 2048); } while (0)
; #define PG8_LDB(dst, b, h) do { _Pragma("unroll") for (int n = 0; n < 2; ++n) dst[n] = PG8_LD2(lds + PG8_SB(b, h) + boff + n * 2048); } while (0)
; #define PG8_WAIT_V(n) asm volatile("s_waitcnt vmcnt(" #n ")" ::: "memory")
; #define PG8_WAIT_L(n) asm volatile("s_waitcnt lgkmcnt(" #n ")" ::: "memory")
; #define PG8_BAR __builtin_amdgcn_s_barrier()
; #define PG8_SCHED __builtin_amdgcn_sched_barrier(0)
; template <class Epi, class Sched, bool ALIGN_EPI = false, bool SP2 = false, bool FP8 = false>
; __device__ __forceinline__ void gemm_phase(LAS unsigned char* lds, const Gemm g, const Sched& S, const Epi& E, int wbase) {
;     ...
;         for (int t = 0; t < nt; t += 2) {
;             const bool last = (t == nt - 2);
;     ...
;             PG8_LDB(B0, 1, 0); PG8_LDB(B1, 1, 1); PG8_SCHED; PG8_LDA(At, 1, 0); PG8_STAGE(PG8_SA(0, 1), rA2, a2 + hstep, voffA);
;             PG8_WAIT_V(8); PG8_WAIT_L(0); PG8_BAR; PG8_MMA(0, 0, At, B0); PG8_MMA(0, 1, At, B1); PG8_BAR; PG8_SCHED;
;             PG8_LDA(At, 1, 1); PG8_STAGE(PG8_SB(1, 0), rB2, b3, voffB); PG8_STAGE(PG8_SB(1, 1), rB2, b3 + hstep, voffB); PG8_STAGE(PG8_SA(1, 0), rA2, a3, voffA);
;             PG8_WAIT_V(8); PG8_WAIT_L(0); PG8_BAR; PG8_MMA(1, 0, At, B0); PG8_MMA(1, 1, At, B1); PG8_BAR; PG8_SCHED;
	s_mov_b32 m0, s47
	s_nop 0
	buffer_load_dwordx4 v177, s[12:15], s63 offen lds
	v_add_u32_e32 v8, 0x18000, v180
	s_nop 3
	ds_read_b128 v[0:3], v8
	ds_read_b128 v[4:7], v8 offset:1024
	ds_read_b128 v[16:19], v8 offset:2048
	ds_read_b128 v[20:23], v8 offset:3072
	v_add_u32_e32 v8, 0x1c000, v180
	ds_read_b128 v[120:123], v8
	ds_read_b128 v[124:127], v8 offset:1024
	ds_read_b128 v[132:135], v8 offset:2048
	ds_read_b128 v[136:139], v8 offset:3072
	s_add_i32 s62, s62, s42
	s_mov_b32 m0, s52
	ds_read_b128 v[8:11], v181 offset:32768
	ds_read_b128 v[12:15], v181 offset:33792
	ds_read_b128 v[24:27], v181 offset:34816
	ds_read_b128 v[28:31], v181 offset:35840
	ds_read_b128 v[32:35], v181 offset:36864
	ds_read_b128 v[36:39], v181 offset:37888
	ds_read_b128 v[40:43], v181 offset:38912
	ds_read_b128 v[44:47], v181 offset:39936
	buffer_load_dwordx4 v174, s[36:39], s62 offen lds
	s_mov_b32 m0, s53
	s_nop 0
	buffer_load_dwordx4 v176, s[36:39], s62 offen lds
	s_waitcnt vmcnt(8)
	s_waitcnt lgkmcnt(0)
	s_barrier
	s_setprio 1
	v_mfma_f32_16x16x128_f8f6f4 v[140:143], v[0:7], v[8:15], v[140:143]
	v_mfma_f32_16x16x128_f8f6f4 v[128:131], v[16:23], v[8:15], v[128:131]
	v_mfma_f32_16x16x128_f8f6f4 v[108:111], v[0:7], v[24:31], v[108:111]
	v_mfma_f32_16x16x128_f8f6f4 v[104:107], v[16:23], v[24:31], v[104:107]
	v_mfma_f32_16x16x128_f8f6f4 v[92:95], v[0:7], v[32:39], v[168:171]
	v_mfma_f32_16x16x128_f8f6f4 v[88:91], v[16:23], v[32:39], v[190:193]
	v_mfma_f32_16x16x128_f8f6f4 v[76:79], v[0:7], v[40:47], v[210:213]
	v_mfma_f32_16x16x128_f8f6f4 v[72:75], v[16:23], v[40:47], v[214:217]
	v_mfma_f32_16x16x128_f8f6f4 v[116:119], v[120:127], v[8:15], v[116:119]
	v_mfma_f32_16x16x128_f8f6f4 v[112:115], v[132:139], v[8:15], v[112:115]
	v_mfma_f32_16x16x128_f8f6f4 v[100:103], v[120:127], v[24:31], v[100:103]
	v_mfma_f32_16x16x128_f8f6f4 v[96:99], v[132:139], v[24:31], v[96:99]
	v_mfma_f32_16x16x128_f8f6f4 v[84:87], v[120:127], v[32:39], v[160:163]
	v_mfma_f32_16x16x128_f8f6f4 v[80:83], v[132:139], v[32:39], v[164:167]
	v_mfma_f32_16x16x128_f8f6f4 v[68:71], v[120:127], v[40:47], v[182:185]
	v_mfma_f32_16x16x128_f8f6f4 v[64:67], v[132:139], v[40:47], v[186:189]
	s_setprio 0
	s_barrier
	s_mov_b32 m0, s56
	s_bitset1_b32 s55, 7
	buffer_load_dwordx4 v175, s[12:15], s55 offen lds
	s_mov_b32 m0, s57
	ds_read_b128 v[32:35], v181 offset:49152
	buffer_load_dwordx4 v177, s[12:15], s55 offen lds
	s_add_i32 s55, s55, s42
	s_mov_b32 m0, s65
	ds_read_b128 v[36:39], v181 offset:50176
	buffer_load_dwordx4 v175, s[12:15], s55 offen lds
	s_mov_b32 m0, s58
	ds_read_b128 v[144:147], v181 offset:51200
	buffer_load_dwordx4 v174, s[36:39], s54 offen lds
	s_mov_b32 m0, s59
	ds_read_b128 v[148:151], v181 offset:52224
	buffer_load_dwordx4 v176, s[36:39], s54 offen lds
	ds_read_b128 v[152:155], v181 offset:53248
	ds_read_b128 v[156:159], v181 offset:54272
	ds_read_b128 v[160:163], v181 offset:55296
	ds_read_b128 v[164:167], v181 offset:56320
	s_waitcnt vmcnt(7)
	s_waitcnt lgkmcnt(0)
	s_barrier
	s_setprio 1
	v_mfma_f32_16x16x128_f8f6f4 v[60:63], v[0:7], v[32:39], v[60:63]
	v_mfma_f32_16x16x128_f8f6f4 v[56:59], v[16:23], v[32:39], v[56:59]
	v_mfma_f32_16x16x128_f8f6f4 v[44:47], v[0:7], v[144:151], v[194:197]
	v_mfma_f32_16x16x128_f8f6f4 v[40:43], v[16:23], v[144:151], v[198:201]
	v_mfma_f32_16x16x128_f8f6f4 v[28:31], v[0:7], v[152:159], v[202:205]
	v_mfma_f32_16x16x128_f8f6f4 v[24:27], v[16:23], v[152:159], v[206:209]
	v_mfma_f32_16x16x128_f8f6f4 v[12:15], v[0:7], v[160:167], v[218:221]
	v_mfma_f32_16x16x128_f8f6f4 v[8:11], v[16:23], v[160:167], v[226:229]
	v_mfma_f32_16x16x128_f8f6f4 v[52:55], v[120:127], v[32:39], v[52:55]
	v_mfma_f32_16x16x128_f8f6f4 v[48:51], v[132:139], v[32:39], v[48:51]
	v_mfma_f32_16x16x128_f8f6f4 v[36:39], v[120:127], v[144:151], v[230:233]
	v_mfma_f32_16x16x128_f8f6f4 v[32:35], v[132:139], v[144:151], v[234:237]
	v_mfma_f32_16x16x128_f8f6f4 v[20:23], v[120:127], v[152:159], v[238:241]
	v_mfma_f32_16x16x128_f8f6f4 v[16:19], v[132:139], v[152:159], v[242:245]
	v_mfma_f32_16x16x128_f8f6f4 v[4:7], v[120:127], v[160:167], v[246:249]
	v_mfma_f32_16x16x128_f8f6f4 v[0:3], v[132:139], v[160:167], v[250:253]
	s_setprio 0
	s_barrier
	s_add_i32 s61, s61, 2
	s_addk_i32 s4, 0x100
	s_addk_i32 s5, 0x100
	s_cmp_ge_i32 s61, s82
	s_cbranch_scc0 .LBB0_1990
	s_mov_b32 m0, s76
	s_nop 0
	buffer_load_dwordx4 v177, s[12:15], s55 offen lds
